# norm phases: wave all-reduce by four DPP adds + readlane combine instead of six ds_bpermute round trips (12 sites, bit-identical sum order)
# speedup vs baseline: 1.0036x; 1.0023x over previous
.LBB0_325:
	s_or_b64 exec, exec, s[10:11]
	v_mov_b32_e32 v78, v65
	v_mov_b32_e32 v79, v61
	s_and_b64 s[0:1], exec, s[0:1]
	v_mov_b32_e32 v76, v64
	v_mov_b32_e32 v77, v60
	v_pk_mul_f32 v[78:79], v[78:79], v[78:79]
	v_mov_b32_e32 v80, v67
	v_mov_b32_e32 v81, v63
	s_or_b64 s[36:37], s[0:1], s[36:37]
	v_readlane_b32 s0, v249, 33
	v_pk_fma_f32 v[76:77], v[76:77], v[76:77], v[78:79]
	v_mov_b32_e32 v78, v66
	v_mov_b32_e32 v79, v62
	v_pk_mul_f32 v[80:81], v[80:81], v[80:81]
	v_cmp_gt_i32_e32 vcc, s0, v70
	v_readlane_b32 s0, v249, 30
	v_pk_fma_f32 v[78:79], v[78:79], v[78:79], v[80:81]
	v_pk_mul_f32 v[80:81], v[52:53], v[52:53]
	v_mov_b32_e32 v71, s0
	v_readlane_b32 s0, v249, 23
	v_pk_add_f32 v[76:77], v[76:77], v[78:79]
	v_pk_mul_f32 v[78:79], v[54:55], v[54:55]
	v_mov_b32_e32 v72, s0
	v_pk_mov_b32 v[82:83], v[80:81], v[78:79] op_sel:[1,0]
	v_mov_b32_e32 v81, v79
	v_cndmask_b32_e32 v71, v71, v72, vcc
	v_pk_add_f32 v[78:79], v[82:83], v[80:81]
	v_add_u32_e32 v70, v71, v70
	v_mul_f32_e32 v71, v16, v16
	v_mul_f32_e32 v72, v17, v17
	v_pk_add_f32 v[76:77], v[76:77], v[76:77] op_sel:[0,1] op_sel_hi:[1,0]
	v_pk_add_f32 v[78:79], v[78:79], v[78:79] op_sel:[0,1] op_sel_hi:[1,0]
	v_mov_b32_e32 v77, v71
	v_mov_b32_e32 v79, v72
	v_mul_f32_e32 v72, v21, v21
	v_mul_f32_e32 v80, v18, v18
	v_pk_add_f32 v[76:77], v[76:77], v[78:79]
	v_pk_fma_f32 v[78:79], v[20:21], v[20:21], v[72:73] op_sel_hi:[1,1,0]
	v_mul_f32_e32 v72, v23, v23
	v_mul_f32_e32 v82, v19, v19
	v_mov_b32_e32 v79, v80
	v_pk_fma_f32 v[80:81], v[22:23], v[22:23], v[72:73] op_sel_hi:[1,1,0]
	v_mul_f32_e32 v71, v4, v4
	v_mov_b32_e32 v81, v82
	v_pk_add_f32 v[78:79], v[78:79], v[80:81]
	v_pk_mul_f32 v[80:81], v[12:13], v[12:13]
	v_pk_add_f32 v[76:77], v[76:77], v[78:79]
	v_pk_mul_f32 v[78:79], v[14:15], v[14:15]
	v_mul_f32_e32 v72, v5, v5
	v_pk_mov_b32 v[82:83], v[80:81], v[78:79] op_sel:[1,0]
	v_mov_b32_e32 v81, v79
	v_pk_add_f32 v[78:79], v[82:83], v[80:81]
	v_pk_add_f32 v[76:77], v[76:77], v[76:77] op_sel:[0,1] op_sel_hi:[1,0]
	v_pk_add_f32 v[78:79], v[78:79], v[78:79] op_sel:[0,1] op_sel_hi:[1,0]
	v_mov_b32_e32 v77, v71
	v_mov_b32_e32 v79, v72
	v_mul_f32_e32 v72, v9, v9
	v_mul_f32_e32 v80, v6, v6
	v_pk_add_f32 v[76:77], v[76:77], v[78:79]
	v_pk_fma_f32 v[78:79], v[8:9], v[8:9], v[72:73] op_sel_hi:[1,1,0]
	v_mul_f32_e32 v72, v11, v11
	v_mul_f32_e32 v82, v7, v7
	v_mov_b32_e32 v79, v80
	v_pk_fma_f32 v[80:81], v[10:11], v[10:11], v[72:73] op_sel_hi:[1,1,0]
	v_mov_b32_e32 v81, v82
	v_pk_add_f32 v[78:79], v[78:79], v[80:81]
	s_mov_b32 s0, 0x800000
	v_pk_add_f32 v[76:77], v[76:77], v[78:79]
	v_add_f32_e32 v71, v76, v77
	s_nop 1
	v_add_f32_dpp v71, v71, v71 quad_perm:[1,0,3,2] row_mask:0xf bank_mask:0xf
	s_nop 1
	v_add_f32_dpp v71, v71, v71 quad_perm:[2,3,0,1] row_mask:0xf bank_mask:0xf
	s_nop 1
	v_add_f32_dpp v71, v71, v71 row_half_mirror row_mask:0xf bank_mask:0xf
	s_nop 1
	v_add_f32_dpp v71, v71, v71 row_mirror row_mask:0xf bank_mask:0xf
	s_nop 0
	v_readlane_b32 s100, v71, 0
	v_readlane_b32 s101, v71, 16
	s_nop 1
	v_mov_b32_e32 v72, s101
	v_add_f32_e32 v72, s100, v72
	v_readlane_b32 s100, v71, 32
	v_readlane_b32 s101, v71, 48
	s_nop 1
	v_mov_b32_e32 v71, s101
	v_add_f32_e32 v71, s100, v71
	v_add_f32_e32 v71, v72, v71
	v_min_i32_e32 v75, 0x2000, v70
	v_lshlrev_b32_e32 v75, 1, v75
	v_and_b32_e32 v75, 0xffffe000, v75
	v_add_u32_e32 v75, v73, v75
	s_waitcnt lgkmcnt(0)
	ds_read_b128 v[76:79], v1
	ds_read_b128 v[80:83], v75 offset:24576
	ds_read_b128 v[84:87], v75 offset:49152
	v_fmamk_f32 v71, v71, 0x3a000000, v213
	v_cmp_gt_f32_e32 vcc, s0, v71
	v_mul_f32_e32 v72, 0x4b800000, v71
	s_nop 0
	v_cndmask_b32_e32 v71, v71, v72, vcc
	v_rsq_f32_e32 v71, v71
	s_nop 0
	v_mul_f32_e32 v72, 0x45800000, v71
	v_cndmask_b32_e32 v72, v71, v72, vcc
	v_pk_mul_f32 v[66:67], v[66:67], v[72:73] op_sel_hi:[1,0]
	v_pk_mul_f32 v[64:65], v[64:65], v[72:73] op_sel_hi:[1,0]
	v_ashrrev_i32_e32 v71, 31, v70
	s_waitcnt lgkmcnt(0)
	v_pk_mul_f32 v[64:65], v[76:77], v[64:65]
	v_pk_mul_f32 v[66:67], v[78:79], v[66:67]
	v_pk_add_f32 v[76:77], v[86:87], 1.0 op_sel_hi:[1,0]
	v_pk_add_f32 v[78:79], v[84:85], 1.0 op_sel_hi:[1,0]
	v_lshlrev_b64 v[70:71], 12, v[70:71]
	v_pk_fma_f32 v[66:67], v[76:77], v[66:67], v[82:83]
	v_pk_fma_f32 v[64:65], v[78:79], v[64:65], v[80:81]
	v_lshl_add_u64 v[70:71], v[68:69], 0, v[70:71]
	v_cvt_pk_bf16_f32 v64, v64, v65
	v_cvt_pk_bf16_f32 v65, v66, v67
	global_store_dwordx2 v[70:71], v[64:65], off
	ds_read_b128 v[64:67], v1 offset:1024
	ds_read_b128 v[76:79], v75 offset:25600
	ds_read_b128 v[80:83], v75 offset:50176
	v_pk_mul_f32 v[62:63], v[62:63], v[72:73] op_sel_hi:[1,0]
	v_pk_mul_f32 v[60:61], v[60:61], v[72:73] op_sel_hi:[1,0]
	s_waitcnt lgkmcnt(2)
	v_pk_mul_f32 v[62:63], v[66:67], v[62:63]
	v_pk_mul_f32 v[60:61], v[64:65], v[60:61]
	s_waitcnt lgkmcnt(0)
	v_pk_add_f32 v[64:65], v[82:83], 1.0 op_sel_hi:[1,0]
	v_pk_add_f32 v[66:67], v[80:81], 1.0 op_sel_hi:[1,0]
	v_pk_fma_f32 v[62:63], v[64:65], v[62:63], v[78:79]
	v_pk_fma_f32 v[60:61], v[66:67], v[60:61], v[76:77]
	v_pk_mul_f32 v[54:55], v[54:55], v[72:73] op_sel_hi:[1,0]
	v_cvt_pk_bf16_f32 v60, v60, v61
	v_cvt_pk_bf16_f32 v61, v62, v63
	global_store_dwordx2 v[70:71], v[60:61], off offset:512
	ds_read_b128 v[60:63], v1 offset:2048
	ds_read_b128 v[64:67], v75 offset:26624
	ds_read_b128 v[76:79], v75 offset:51200
	v_pk_mul_f32 v[52:53], v[52:53], v[72:73] op_sel_hi:[1,0]
	v_pk_mul_f32 v[22:23], v[22:23], v[72:73] op_sel_hi:[1,0]
	s_waitcnt lgkmcnt(2)
	v_pk_mul_f32 v[52:53], v[60:61], v[52:53]
	v_pk_mul_f32 v[54:55], v[62:63], v[54:55]
	s_waitcnt lgkmcnt(0)
	v_pk_add_f32 v[60:61], v[78:79], 1.0 op_sel_hi:[1,0]
	v_pk_add_f32 v[62:63], v[76:77], 1.0 op_sel_hi:[1,0]
	v_pk_fma_f32 v[54:55], v[60:61], v[54:55], v[66:67]
	v_pk_fma_f32 v[52:53], v[62:63], v[52:53], v[64:65]
	v_pk_mul_f32 v[20:21], v[20:21], v[72:73] op_sel_hi:[1,0]
	v_cvt_pk_bf16_f32 v52, v52, v53
	v_cvt_pk_bf16_f32 v53, v54, v55
	global_store_dwordx2 v[70:71], v[52:53], off offset:1024
	ds_read_b128 v[52:55], v1 offset:3072
	ds_read_b128 v[60:63], v75 offset:27648
	ds_read_b128 v[64:67], v75 offset:52224
	v_pk_mul_f32 v[18:19], v[18:19], v[72:73] op_sel_hi:[1,0]
	v_pk_mul_f32 v[16:17], v[16:17], v[72:73] op_sel_hi:[1,0]
	s_waitcnt lgkmcnt(2)
	v_pk_mul_f32 v[20:21], v[20:21], v[52:53]
	v_pk_mul_f32 v[22:23], v[22:23], v[54:55]
	s_waitcnt lgkmcnt(0)
	v_pk_add_f32 v[52:53], v[66:67], 1.0 op_sel_hi:[1,0]
	v_pk_add_f32 v[54:55], v[64:65], 1.0 op_sel_hi:[1,0]
	v_pk_fma_f32 v[22:23], v[22:23], v[52:53], v[62:63]
	v_pk_fma_f32 v[20:21], v[20:21], v[54:55], v[60:61]
	v_pk_mul_f32 v[14:15], v[14:15], v[72:73] op_sel_hi:[1,0]
	v_cvt_pk_bf16_f32 v20, v20, v21
	v_cvt_pk_bf16_f32 v21, v22, v23
	global_store_dwordx2 v[70:71], v[20:21], off offset:1536
	ds_read_b128 v[20:23], v1 offset:4096
	ds_read_b128 v[52:55], v75 offset:28672
	ds_read_b128 v[60:63], v75 offset:53248
	v_pk_mul_f32 v[12:13], v[12:13], v[72:73] op_sel_hi:[1,0]
	v_pk_mul_f32 v[10:11], v[10:11], v[72:73] op_sel_hi:[1,0]
	s_waitcnt lgkmcnt(2)
	v_pk_mul_f32 v[16:17], v[16:17], v[20:21]
	v_pk_mul_f32 v[18:19], v[18:19], v[22:23]
	s_waitcnt lgkmcnt(0)
	v_pk_add_f32 v[20:21], v[62:63], 1.0 op_sel_hi:[1,0]
	v_pk_add_f32 v[22:23], v[60:61], 1.0 op_sel_hi:[1,0]
	v_pk_fma_f32 v[18:19], v[18:19], v[20:21], v[54:55]
	v_pk_fma_f32 v[16:17], v[16:17], v[22:23], v[52:53]
	v_pk_mul_f32 v[8:9], v[8:9], v[72:73] op_sel_hi:[1,0]
	v_cvt_pk_bf16_f32 v16, v16, v17
	v_cvt_pk_bf16_f32 v17, v18, v19
	global_store_dwordx2 v[70:71], v[16:17], off offset:2048
	ds_read_b128 v[16:19], v1 offset:5120
	ds_read_b128 v[20:23], v75 offset:29696
	ds_read_b128 v[52:55], v75 offset:54272
	v_pk_mul_f32 v[6:7], v[6:7], v[72:73] op_sel_hi:[1,0]
	v_pk_mul_f32 v[4:5], v[4:5], v[72:73] op_sel_hi:[1,0]
	s_waitcnt lgkmcnt(2)
	v_pk_mul_f32 v[12:13], v[12:13], v[16:17]
	v_pk_mul_f32 v[14:15], v[14:15], v[18:19]
	s_waitcnt lgkmcnt(0)
	v_pk_add_f32 v[16:17], v[54:55], 1.0 op_sel_hi:[1,0]
	v_pk_add_f32 v[18:19], v[52:53], 1.0 op_sel_hi:[1,0]
	v_pk_fma_f32 v[14:15], v[14:15], v[16:17], v[22:23]
	v_pk_fma_f32 v[12:13], v[12:13], v[18:19], v[20:21]
	s_waitcnt vmcnt(12)
	v_mov_b64_e32 v[66:67], v[26:27]
	v_cvt_pk_bf16_f32 v12, v12, v13
	v_cvt_pk_bf16_f32 v13, v14, v15
	global_store_dwordx2 v[70:71], v[12:13], off offset:2560
	ds_read_b128 v[12:15], v1 offset:6144
	ds_read_b128 v[16:19], v75 offset:30720
	ds_read_b128 v[20:23], v75 offset:55296
	s_waitcnt vmcnt(12)
	v_mov_b64_e32 v[62:63], v[30:31]
	s_waitcnt vmcnt(11)
	v_mov_b64_e32 v[54:55], v[34:35]
	s_waitcnt lgkmcnt(2)
	v_pk_mul_f32 v[8:9], v[8:9], v[12:13]
	v_pk_mul_f32 v[10:11], v[10:11], v[14:15]
	s_waitcnt lgkmcnt(0)
	v_pk_add_f32 v[12:13], v[22:23], 1.0 op_sel_hi:[1,0]
	v_pk_add_f32 v[14:15], v[20:21], 1.0 op_sel_hi:[1,0]
	v_pk_fma_f32 v[10:11], v[10:11], v[12:13], v[18:19]
	v_pk_fma_f32 v[8:9], v[8:9], v[14:15], v[16:17]
	s_waitcnt vmcnt(10)
	v_mov_b64_e32 v[20:21], v[36:37]
	v_cvt_pk_bf16_f32 v8, v8, v9
	v_cvt_pk_bf16_f32 v9, v10, v11
	global_store_dwordx2 v[70:71], v[8:9], off offset:3072
	ds_read_b128 v[8:11], v1 offset:7168
	ds_read_b128 v[12:15], v75 offset:31744
	ds_read_b128 v[16:19], v75 offset:56320
	v_mov_b64_e32 v[64:65], v[24:25]
	v_mov_b64_e32 v[60:61], v[28:29]
	s_waitcnt lgkmcnt(2)
	v_pk_mul_f32 v[4:5], v[4:5], v[8:9]
	v_pk_mul_f32 v[6:7], v[6:7], v[10:11]
	s_waitcnt lgkmcnt(0)
	v_pk_add_f32 v[8:9], v[18:19], 1.0 op_sel_hi:[1,0]
	v_pk_add_f32 v[10:11], v[16:17], 1.0 op_sel_hi:[1,0]
	v_pk_fma_f32 v[6:7], v[6:7], v[8:9], v[14:15]
	v_pk_fma_f32 v[4:5], v[4:5], v[10:11], v[12:13]
	s_waitcnt vmcnt(10)
	v_mov_b64_e32 v[16:17], v[40:41]
	v_cvt_pk_bf16_f32 v4, v4, v5
	v_cvt_pk_bf16_f32 v5, v6, v7
	global_store_dwordx2 v[70:71], v[4:5], off offset:3584
	s_waitcnt vmcnt(10)
	v_mov_b64_e32 v[12:13], v[44:45]
	s_waitcnt vmcnt(9)
	v_mov_b64_e32 v[8:9], v[48:49]
	s_waitcnt vmcnt(8)
	v_mov_b64_e32 v[4:5], v[56:57]
	v_mov_b64_e32 v[52:53], v[32:33]
	v_mov_b64_e32 v[22:23], v[38:39]
	v_mov_b64_e32 v[18:19], v[42:43]
	v_mov_b64_e32 v[14:15], v[46:47]
	v_mov_b64_e32 v[10:11], v[50:51]
	v_mov_b64_e32 v[6:7], v[58:59]
	v_mov_b32_e32 v70, v74
	s_andn2_b64 exec, exec, s[36:37]
	s_cbranch_execz .LBB0_328

.LBB0_1516:
	s_or_b64 exec, exec, s[0:1]
	s_waitcnt lgkmcnt(0)
	v_add_f32_e32 v76, v99, v100
	v_fmamk_f32 v76, v76, 0x3a000000, v213
	s_and_b64 s[0:1], exec, vcc
	v_cmp_gt_f32_e32 vcc, s22, v76
	v_mul_f32_e32 v77, 0x4b800000, v76
	v_lshlrev_b32_e32 v108, 16, v42
	v_cndmask_b32_e32 v76, v76, v77, vcc
	v_rsq_f32_e32 v76, v76
	v_and_b32_e32 v109, 0xffff0000, v42
	v_lshlrev_b32_e32 v110, 16, v43
	v_and_b32_e32 v111, 0xffff0000, v43
	v_mul_f32_e32 v77, 0x45800000, v76
	v_cndmask_b32_e32 v76, v76, v77, vcc
	v_min_i32_e32 v77, 0x2000, v26
	v_lshlrev_b32_e32 v77, 1, v77
	v_and_b32_e32 v77, 0xffffe000, v77
	v_add_u32_e32 v77, v96, v77
	ds_read_b128 v[100:103], v77
	ds_read_b128 v[104:107], v97
	v_pk_mul_f32 v[74:75], v[74:75], v[76:77] op_sel_hi:[1,0]
	v_pk_mul_f32 v[72:73], v[72:73], v[76:77] op_sel_hi:[1,0]
	v_lshl_add_u64 v[94:95], v[94:95], 0, v[2:3]
	v_pk_mul_f32 v[70:71], v[70:71], v[76:77] op_sel_hi:[1,0]
	s_waitcnt lgkmcnt(0)
	v_pk_mul_f32 v[104:105], v[72:73], v[104:105]
	v_pk_mul_f32 v[72:73], v[74:75], v[106:107]
	v_pk_fma_f32 v[74:75], v[100:101], v[104:105], v[108:109]
	v_pk_fma_f32 v[72:73], v[102:103], v[72:73], v[110:111]
	v_cvt_pk_bf16_f32 v100, v74, v75
	v_cvt_pk_bf16_f32 v101, v72, v73
	global_store_dwordx2 v[94:95], v[100:101], off
	ds_read_b128 v[100:103], v77 offset:1024
	ds_read_b128 v[104:107], v97 offset:1024
	v_pk_mul_f32 v[68:69], v[68:69], v[76:77] op_sel_hi:[1,0]
	v_lshlrev_b32_e32 v112, 16, v40
	v_and_b32_e32 v113, 0xffff0000, v40
	v_lshlrev_b32_e32 v114, 16, v41
	v_and_b32_e32 v115, 0xffff0000, v41
	s_waitcnt lgkmcnt(0)
	v_pk_mul_f32 v[104:105], v[68:69], v[104:105]
	v_pk_mul_f32 v[68:69], v[70:71], v[106:107]
	v_pk_fma_f32 v[70:71], v[100:101], v[104:105], v[112:113]
	v_pk_fma_f32 v[68:69], v[102:103], v[68:69], v[114:115]
	v_cvt_pk_bf16_f32 v100, v70, v71
	v_cvt_pk_bf16_f32 v101, v68, v69
	global_store_dwordx2 v[94:95], v[100:101], off offset:512
	ds_read_b128 v[100:103], v77 offset:2048
	ds_read_b128 v[104:107], v97 offset:2048
	v_pk_mul_f32 v[66:67], v[66:67], v[76:77] op_sel_hi:[1,0]
	v_pk_mul_f32 v[64:65], v[64:65], v[76:77] op_sel_hi:[1,0]
	v_lshlrev_b32_e32 v116, 16, v38
	v_and_b32_e32 v117, 0xffff0000, v38
	v_lshlrev_b32_e32 v118, 16, v39
	v_and_b32_e32 v119, 0xffff0000, v39
	s_waitcnt lgkmcnt(0)
	v_pk_mul_f32 v[104:105], v[64:65], v[104:105]
	v_pk_mul_f32 v[64:65], v[66:67], v[106:107]
	v_pk_fma_f32 v[66:67], v[100:101], v[104:105], v[116:117]
	v_pk_fma_f32 v[64:65], v[102:103], v[64:65], v[118:119]
	v_cvt_pk_bf16_f32 v100, v66, v67
	v_cvt_pk_bf16_f32 v101, v64, v65
	global_store_dwordx2 v[94:95], v[100:101], off offset:1024
	ds_read_b128 v[100:103], v77 offset:3072
	ds_read_b128 v[104:107], v97 offset:3072
	v_pk_mul_f32 v[62:63], v[62:63], v[76:77] op_sel_hi:[1,0]
	v_pk_mul_f32 v[60:61], v[60:61], v[76:77] op_sel_hi:[1,0]
	v_lshlrev_b32_e32 v120, 16, v36
	v_and_b32_e32 v121, 0xffff0000, v36
	v_lshlrev_b32_e32 v122, 16, v37
	v_and_b32_e32 v123, 0xffff0000, v37
	s_waitcnt lgkmcnt(0)
	v_pk_mul_f32 v[104:105], v[60:61], v[104:105]
	v_pk_mul_f32 v[60:61], v[62:63], v[106:107]
	v_pk_fma_f32 v[62:63], v[100:101], v[104:105], v[120:121]
	v_pk_fma_f32 v[60:61], v[102:103], v[60:61], v[122:123]
	v_cvt_pk_bf16_f32 v100, v62, v63
	v_cvt_pk_bf16_f32 v101, v60, v61
	global_store_dwordx2 v[94:95], v[100:101], off offset:1536
	ds_read_b128 v[100:103], v77 offset:4096
	ds_read_b128 v[104:107], v97 offset:4096
	v_pk_mul_f32 v[58:59], v[58:59], v[76:77] op_sel_hi:[1,0]
	v_pk_mul_f32 v[56:57], v[56:57], v[76:77] op_sel_hi:[1,0]
	v_lshlrev_b32_e32 v42, 16, v34
	v_and_b32_e32 v43, 0xffff0000, v34
	v_lshlrev_b32_e32 v40, 16, v35
	v_and_b32_e32 v41, 0xffff0000, v35
	s_waitcnt lgkmcnt(0)
	v_pk_mul_f32 v[56:57], v[56:57], v[104:105]
	v_pk_mul_f32 v[58:59], v[58:59], v[106:107]
	v_pk_fma_f32 v[42:43], v[100:101], v[56:57], v[42:43]
	v_pk_fma_f32 v[40:41], v[102:103], v[58:59], v[40:41]
	v_cvt_pk_bf16_f32 v56, v42, v43
	v_cvt_pk_bf16_f32 v57, v40, v41
	global_store_dwordx2 v[94:95], v[56:57], off offset:2048
	ds_read_b128 v[56:59], v77 offset:5120
	ds_read_b128 v[100:103], v97 offset:5120
	v_pk_mul_f32 v[54:55], v[54:55], v[76:77] op_sel_hi:[1,0]
	v_pk_mul_f32 v[52:53], v[52:53], v[76:77] op_sel_hi:[1,0]
	v_lshlrev_b32_e32 v38, 16, v32
	v_and_b32_e32 v39, 0xffff0000, v32
	v_lshlrev_b32_e32 v36, 16, v33
	v_and_b32_e32 v37, 0xffff0000, v33
	s_waitcnt lgkmcnt(0)
	v_pk_mul_f32 v[52:53], v[52:53], v[100:101]
	v_pk_mul_f32 v[54:55], v[54:55], v[102:103]
	v_pk_fma_f32 v[38:39], v[56:57], v[52:53], v[38:39]
	v_pk_fma_f32 v[36:37], v[58:59], v[54:55], v[36:37]
	v_cvt_pk_bf16_f32 v52, v38, v39
	v_cvt_pk_bf16_f32 v53, v36, v37
	global_store_dwordx2 v[94:95], v[52:53], off offset:2560
	ds_read_b128 v[52:55], v77 offset:6144
	ds_read_b128 v[56:59], v97 offset:6144
	v_pk_mul_f32 v[50:51], v[50:51], v[76:77] op_sel_hi:[1,0]
	v_pk_mul_f32 v[48:49], v[48:49], v[76:77] op_sel_hi:[1,0]
	v_lshlrev_b32_e32 v34, 16, v30
	v_and_b32_e32 v35, 0xffff0000, v30
	v_lshlrev_b32_e32 v32, 16, v31
	v_and_b32_e32 v33, 0xffff0000, v31
	s_waitcnt lgkmcnt(0)
	v_pk_mul_f32 v[48:49], v[48:49], v[56:57]
	v_pk_mul_f32 v[50:51], v[50:51], v[58:59]
	v_pk_fma_f32 v[34:35], v[52:53], v[48:49], v[34:35]
	v_pk_fma_f32 v[32:33], v[54:55], v[50:51], v[32:33]
	v_cvt_pk_bf16_f32 v48, v34, v35
	v_cvt_pk_bf16_f32 v49, v32, v33
	global_store_dwordx2 v[94:95], v[48:49], off offset:3072
	ds_read_b128 v[48:51], v77 offset:7168
	ds_read_b128 v[52:55], v97 offset:7168
	v_pk_mul_f32 v[44:45], v[44:45], v[76:77] op_sel_hi:[1,0]
	v_pk_mul_f32 v[46:47], v[46:47], v[76:77] op_sel_hi:[1,0]
	v_lshlrev_b32_e32 v30, 16, v28
	v_and_b32_e32 v31, 0xffff0000, v28
	v_lshlrev_b32_e32 v28, 16, v29
	v_and_b32_e32 v29, 0xffff0000, v29
	s_waitcnt lgkmcnt(0)
	v_pk_mul_f32 v[46:47], v[46:47], v[52:53]
	v_pk_mul_f32 v[44:45], v[44:45], v[54:55]
	v_pk_fma_f32 v[30:31], v[48:49], v[46:47], v[30:31]
	v_pk_fma_f32 v[28:29], v[50:51], v[44:45], v[28:29]
	v_cvt_pk_bf16_f32 v44, v30, v31
	v_cvt_pk_bf16_f32 v45, v28, v29
	v_mov_b32_e32 v46, v75
	v_mov_b32_e32 v47, v71
	global_store_dwordx2 v[94:95], v[44:45], off offset:3584
	v_mov_b32_e32 v44, v74
	v_mov_b32_e32 v45, v70
	v_pk_mul_f32 v[46:47], v[46:47], v[46:47]
	v_mov_b32_e32 v48, v73
	v_mov_b32_e32 v49, v69
	v_pk_fma_f32 v[44:45], v[44:45], v[44:45], v[46:47]
	v_mov_b32_e32 v46, v72
	v_mov_b32_e32 v47, v68
	v_pk_mul_f32 v[48:49], v[48:49], v[48:49]
	v_lshlrev_b64 v[26:27], 11, v[26:27]
	v_pk_fma_f32 v[46:47], v[46:47], v[46:47], v[48:49]
	v_pk_mul_f32 v[48:49], v[66:67], v[66:67]
	v_pk_add_f32 v[44:45], v[44:45], v[46:47]
	v_pk_mul_f32 v[46:47], v[64:65], v[64:65]
	v_pk_add_f32 v[44:45], v[44:45], v[44:45] op_sel:[0,1] op_sel_hi:[1,0]
	v_pk_mov_b32 v[50:51], v[48:49], v[46:47] op_sel:[1,0]
	v_mov_b32_e32 v49, v47
	v_pk_add_f32 v[46:47], v[50:51], v[48:49]
	v_mul_f32_e32 v48, v42, v42
	v_mul_f32_e32 v49, v43, v43
	v_pk_add_f32 v[46:47], v[46:47], v[46:47] op_sel:[0,1] op_sel_hi:[1,0]
	v_mov_b32_e32 v45, v48
	v_mov_b32_e32 v47, v49
	v_pk_add_f32 v[44:45], v[44:45], v[46:47]
	v_mul_f32_e32 v46, v63, v63
	v_mul_f32_e32 v48, v61, v61
	v_mul_f32_e32 v50, v40, v40
	v_mul_f32_e32 v51, v41, v41
	v_pk_fma_f32 v[46:47], v[62:63], v[62:63], v[46:47] op_sel_hi:[1,1,0]
	v_pk_fma_f32 v[48:49], v[60:61], v[60:61], v[48:49] op_sel_hi:[1,1,0]
	v_mov_b32_e32 v47, v50
	v_mov_b32_e32 v49, v51
	v_pk_add_f32 v[46:47], v[46:47], v[48:49]
	v_pk_mul_f32 v[48:49], v[38:39], v[38:39]
	v_pk_add_f32 v[44:45], v[44:45], v[46:47]
	v_pk_mul_f32 v[46:47], v[36:37], v[36:37]
	v_pk_add_f32 v[44:45], v[44:45], v[44:45] op_sel:[0,1] op_sel_hi:[1,0]
	v_pk_mov_b32 v[50:51], v[48:49], v[46:47] op_sel:[1,0]
	v_mov_b32_e32 v49, v47
	v_pk_add_f32 v[46:47], v[50:51], v[48:49]
	v_mul_f32_e32 v48, v30, v30
	v_mul_f32_e32 v49, v31, v31
	v_pk_add_f32 v[46:47], v[46:47], v[46:47] op_sel:[0,1] op_sel_hi:[1,0]
	v_mov_b32_e32 v45, v48
	v_mov_b32_e32 v47, v49
	v_pk_add_f32 v[44:45], v[44:45], v[46:47]
	v_mul_f32_e32 v46, v35, v35
	v_mul_f32_e32 v48, v33, v33
	v_mul_f32_e32 v50, v28, v28
	v_mul_f32_e32 v51, v29, v29
	v_pk_fma_f32 v[46:47], v[34:35], v[34:35], v[46:47] op_sel_hi:[1,1,0]
	v_pk_fma_f32 v[48:49], v[32:33], v[32:33], v[48:49] op_sel_hi:[1,1,0]
	v_mov_b32_e32 v47, v50
	v_mov_b32_e32 v49, v51
	v_pk_add_f32 v[46:47], v[46:47], v[48:49]
	v_lshl_add_u64 v[26:27], v[24:25], 0, v[26:27]
	v_pk_add_f32 v[44:45], v[44:45], v[46:47]
	s_or_b64 s[14:15], s[0:1], s[14:15]
	v_add_f32_e32 v44, v44, v45
	s_nop 1
	v_add_f32_dpp v44, v44, v44 quad_perm:[1,0,3,2] row_mask:0xf bank_mask:0xf
	s_nop 1
	v_add_f32_dpp v44, v44, v44 quad_perm:[2,3,0,1] row_mask:0xf bank_mask:0xf
	s_nop 1
	v_add_f32_dpp v44, v44, v44 row_half_mirror row_mask:0xf bank_mask:0xf
	s_nop 1
	v_add_f32_dpp v44, v44, v44 row_mirror row_mask:0xf bank_mask:0xf
	s_nop 0
	v_readlane_b32 s100, v44, 0
	v_readlane_b32 s101, v44, 16
	s_nop 1
	v_mov_b32_e32 v45, s101
	v_add_f32_e32 v45, s100, v45
	v_readlane_b32 s100, v44, 32
	v_readlane_b32 s101, v44, 48
	s_nop 1
	v_mov_b32_e32 v44, s101
	v_add_f32_e32 v44, s100, v44
	v_add_f32_e32 v44, v45, v44
	s_waitcnt lgkmcnt(0)
	ds_read_b128 v[46:49], v98
	ds_read_b128 v[50:53], v77 offset:24576
	ds_read_b128 v[54:57], v77 offset:49152
	s_waitcnt lgkmcnt(0)
	v_pk_add_f32 v[54:55], v[54:55], 1.0 op_sel_hi:[1,0]
	v_pk_add_f32 v[56:57], v[56:57], 1.0 op_sel_hi:[1,0]
	v_fmamk_f32 v44, v44, 0x3a000000, v213
	v_cmp_gt_f32_e32 vcc, s22, v44
	v_mul_f32_e32 v45, 0x4b800000, v44
	s_nop 0
	v_cndmask_b32_e32 v44, v44, v45, vcc
	v_rsq_f32_e32 v44, v44
	s_nop 0
	v_mul_f32_e32 v45, 0x45800000, v44
	v_cndmask_b32_e32 v44, v44, v45, vcc
	v_pk_mul_f32 v[58:59], v[72:73], v[44:45] op_sel_hi:[1,0]
	v_pk_mul_f32 v[72:73], v[74:75], v[44:45] op_sel_hi:[1,0]
	v_pk_mul_f32 v[48:49], v[48:49], v[58:59]
	v_pk_mul_f32 v[46:47], v[46:47], v[72:73]
	v_pk_fma_f32 v[48:49], v[56:57], v[48:49], v[52:53]
	v_pk_fma_f32 v[46:47], v[54:55], v[46:47], v[50:51]
	s_nop 0
	v_mul_f32_e32 v45, 0x41000000, v46
	v_mul_f32_e32 v46, 0x41000000, v47
	v_mul_f32_e32 v47, 0x41000000, v48
	v_mul_f32_e32 v48, 0x41000000, v49
	v_med3_f32 v45, v45, s8, v225
	v_med3_f32 v46, v46, s8, v225
	v_mov_b32_e32 v49, v3
	v_cvt_pk_fp8_f32 v49, v45, v46
	v_med3_f32 v45, v47, s8, v225
	v_med3_f32 v46, v48, s8, v225
	v_pk_mul_f32 v[58:59], v[68:69], v[44:45] op_sel_hi:[1,0]
	v_cvt_pk_fp8_f32 v49, v45, v46 op_sel:[0,0,1]
	v_pk_mul_f32 v[68:69], v[70:71], v[44:45] op_sel_hi:[1,0]
	global_store_dword v[26:27], v49, off
	ds_read_b128 v[46:49], v98 offset:1024
	ds_read_b128 v[50:53], v77 offset:25600
	ds_read_b128 v[54:57], v77 offset:50176
	s_waitcnt lgkmcnt(2)
	v_pk_mul_f32 v[46:47], v[46:47], v[68:69]
	v_pk_mul_f32 v[48:49], v[48:49], v[58:59]
	s_waitcnt lgkmcnt(0)
	v_pk_add_f32 v[54:55], v[54:55], 1.0 op_sel_hi:[1,0]
	v_pk_add_f32 v[56:57], v[56:57], 1.0 op_sel_hi:[1,0]
	v_pk_fma_f32 v[46:47], v[54:55], v[46:47], v[50:51]
	v_pk_fma_f32 v[48:49], v[56:57], v[48:49], v[52:53]
	v_mul_f32_e32 v45, 0x41000000, v46
	v_mul_f32_e32 v46, 0x41000000, v47
	v_mul_f32_e32 v47, 0x41000000, v48
	v_mul_f32_e32 v48, 0x41000000, v49
	v_med3_f32 v45, v45, s8, v225
	v_med3_f32 v46, v46, s8, v225
	v_mov_b32_e32 v49, v3
	v_cvt_pk_fp8_f32 v49, v45, v46
	v_med3_f32 v45, v47, s8, v225
	v_med3_f32 v46, v48, s8, v225
	v_pk_mul_f32 v[58:59], v[64:65], v[44:45] op_sel_hi:[1,0]
	v_cvt_pk_fp8_f32 v49, v45, v46 op_sel:[0,0,1]
	v_pk_mul_f32 v[64:65], v[66:67], v[44:45] op_sel_hi:[1,0]
	global_store_dword v[26:27], v49, off offset:256
	ds_read_b128 v[46:49], v98 offset:2048
	ds_read_b128 v[50:53], v77 offset:26624
	ds_read_b128 v[54:57], v77 offset:51200
	s_waitcnt lgkmcnt(2)
	v_pk_mul_f32 v[46:47], v[64:65], v[46:47]
	v_pk_mul_f32 v[48:49], v[58:59], v[48:49]
	s_waitcnt lgkmcnt(0)
	v_pk_add_f32 v[54:55], v[54:55], 1.0 op_sel_hi:[1,0]
	v_pk_add_f32 v[56:57], v[56:57], 1.0 op_sel_hi:[1,0]
	v_pk_fma_f32 v[46:47], v[46:47], v[54:55], v[50:51]
	v_pk_fma_f32 v[48:49], v[48:49], v[56:57], v[52:53]
	v_mul_f32_e32 v45, 0x41000000, v46
	v_mul_f32_e32 v46, 0x41000000, v47
	v_mul_f32_e32 v47, 0x41000000, v48
	v_mul_f32_e32 v48, 0x41000000, v49
	v_med3_f32 v45, v45, s8, v225
	v_med3_f32 v46, v46, s8, v225
	v_mov_b32_e32 v49, v3
	v_cvt_pk_fp8_f32 v49, v45, v46
	v_med3_f32 v45, v47, s8, v225
	v_med3_f32 v46, v48, s8, v225
	v_pk_mul_f32 v[58:59], v[60:61], v[44:45] op_sel_hi:[1,0]
	v_cvt_pk_fp8_f32 v49, v45, v46 op_sel:[0,0,1]
	v_pk_mul_f32 v[60:61], v[62:63], v[44:45] op_sel_hi:[1,0]
	global_store_dword v[26:27], v49, off offset:512
	ds_read_b128 v[46:49], v98 offset:3072
	ds_read_b128 v[50:53], v77 offset:27648
	ds_read_b128 v[54:57], v77 offset:52224
	s_waitcnt lgkmcnt(2)
	v_pk_mul_f32 v[46:47], v[60:61], v[46:47]
	v_pk_mul_f32 v[48:49], v[58:59], v[48:49]
	s_waitcnt lgkmcnt(0)
	v_pk_add_f32 v[54:55], v[54:55], 1.0 op_sel_hi:[1,0]
	v_pk_add_f32 v[56:57], v[56:57], 1.0 op_sel_hi:[1,0]
	v_pk_fma_f32 v[46:47], v[46:47], v[54:55], v[50:51]
	v_pk_fma_f32 v[48:49], v[48:49], v[56:57], v[52:53]
	v_mul_f32_e32 v45, 0x41000000, v46
	v_mul_f32_e32 v46, 0x41000000, v47
	v_mul_f32_e32 v47, 0x41000000, v48
	v_mul_f32_e32 v48, 0x41000000, v49
	v_med3_f32 v45, v45, s8, v225
	v_med3_f32 v46, v46, s8, v225
	v_mov_b32_e32 v49, v3
	v_cvt_pk_fp8_f32 v49, v45, v46
	v_med3_f32 v45, v47, s8, v225
	v_med3_f32 v46, v48, s8, v225
	v_pk_mul_f32 v[40:41], v[40:41], v[44:45] op_sel_hi:[1,0]
	v_cvt_pk_fp8_f32 v49, v45, v46 op_sel:[0,0,1]
	v_pk_mul_f32 v[42:43], v[42:43], v[44:45] op_sel_hi:[1,0]
	v_mov_b32_e32 v45, v3
	global_store_dword v[26:27], v49, off offset:768
	ds_read_b128 v[46:49], v98 offset:4096
	ds_read_b128 v[50:53], v77 offset:28672
	ds_read_b128 v[54:57], v77 offset:53248
	s_waitcnt lgkmcnt(2)
	v_pk_mul_f32 v[42:43], v[42:43], v[46:47]
	v_pk_mul_f32 v[40:41], v[40:41], v[48:49]
	s_waitcnt lgkmcnt(0)
	v_pk_add_f32 v[48:49], v[54:55], 1.0 op_sel_hi:[1,0]
	v_pk_add_f32 v[46:47], v[56:57], 1.0 op_sel_hi:[1,0]
	v_pk_fma_f32 v[42:43], v[42:43], v[48:49], v[50:51]
	v_pk_fma_f32 v[40:41], v[40:41], v[46:47], v[52:53]
	v_mul_f32_e32 v42, 0x41000000, v42
	v_mul_f32_e32 v43, 0x41000000, v43
	v_med3_f32 v42, v42, s8, v225
	v_med3_f32 v43, v43, s8, v225
	v_cvt_pk_fp8_f32 v45, v42, v43
	v_mul_f32_e32 v40, 0x41000000, v40
	v_mul_f32_e32 v41, 0x41000000, v41
	v_med3_f32 v40, v40, s8, v225
	v_med3_f32 v41, v41, s8, v225
	v_cvt_pk_fp8_f32 v45, v40, v41 op_sel:[0,0,1]
	global_store_dword v[26:27], v45, off offset:1024
	ds_read_b128 v[40:43], v98 offset:5120
	ds_read_b128 v[46:49], v77 offset:29696
	ds_read_b128 v[50:53], v77 offset:54272
	v_pk_mul_f32 v[36:37], v[36:37], v[44:45] op_sel_hi:[1,0]
	v_pk_mul_f32 v[38:39], v[38:39], v[44:45] op_sel_hi:[1,0]
	s_waitcnt lgkmcnt(2)
	v_pk_mul_f32 v[36:37], v[36:37], v[42:43]
	v_pk_mul_f32 v[38:39], v[38:39], v[40:41]
	s_waitcnt lgkmcnt(0)
	v_pk_add_f32 v[42:43], v[50:51], 1.0 op_sel_hi:[1,0]
	v_pk_add_f32 v[40:41], v[52:53], 1.0 op_sel_hi:[1,0]
	v_pk_fma_f32 v[38:39], v[38:39], v[42:43], v[46:47]
	v_pk_fma_f32 v[36:37], v[36:37], v[40:41], v[48:49]
	v_mul_f32_e32 v38, 0x41000000, v38
	v_mul_f32_e32 v39, 0x41000000, v39
	v_med3_f32 v38, v38, s8, v225
	v_med3_f32 v39, v39, s8, v225
	v_mov_b32_e32 v40, v3
	v_cvt_pk_fp8_f32 v40, v38, v39
	v_mul_f32_e32 v36, 0x41000000, v36
	v_mul_f32_e32 v37, 0x41000000, v37
	v_med3_f32 v36, v36, s8, v225
	v_med3_f32 v37, v37, s8, v225
	v_cvt_pk_fp8_f32 v40, v36, v37 op_sel:[0,0,1]
	v_pk_mul_f32 v[32:33], v[32:33], v[44:45] op_sel_hi:[1,0]
	v_pk_mul_f32 v[34:35], v[34:35], v[44:45] op_sel_hi:[1,0]
	v_pk_mul_f32 v[28:29], v[28:29], v[44:45] op_sel_hi:[1,0]
	global_store_dword v[26:27], v40, off offset:1280
	ds_read_b128 v[36:39], v98 offset:6144
	ds_read_b128 v[40:43], v77 offset:30720
	ds_read_b128 v[46:49], v77 offset:55296
	v_pk_mul_f32 v[30:31], v[30:31], v[44:45] op_sel_hi:[1,0]
	s_waitcnt lgkmcnt(2)
	v_pk_mul_f32 v[34:35], v[34:35], v[36:37]
	v_pk_mul_f32 v[32:33], v[32:33], v[38:39]
	s_waitcnt lgkmcnt(0)
	v_pk_add_f32 v[38:39], v[46:47], 1.0 op_sel_hi:[1,0]
	v_pk_add_f32 v[36:37], v[48:49], 1.0 op_sel_hi:[1,0]
	v_pk_fma_f32 v[34:35], v[34:35], v[38:39], v[40:41]
	v_pk_fma_f32 v[32:33], v[32:33], v[36:37], v[42:43]
	v_mul_f32_e32 v34, 0x41000000, v34
	v_mul_f32_e32 v35, 0x41000000, v35
	v_med3_f32 v34, v34, s8, v225
	v_med3_f32 v35, v35, s8, v225
	v_mov_b32_e32 v36, v3
	v_cvt_pk_fp8_f32 v36, v34, v35
	v_mul_f32_e32 v32, 0x41000000, v32
	v_mul_f32_e32 v33, 0x41000000, v33
	v_med3_f32 v32, v32, s8, v225
	v_med3_f32 v33, v33, s8, v225
	v_cvt_pk_fp8_f32 v36, v32, v33 op_sel:[0,0,1]
	global_store_dword v[26:27], v36, off offset:1536
	ds_read_b128 v[32:35], v98 offset:7168
	ds_read_b128 v[36:39], v77 offset:31744
	ds_read_b128 v[40:43], v77 offset:56320
	s_waitcnt lgkmcnt(2)
	v_pk_mul_f32 v[30:31], v[30:31], v[32:33]
	v_pk_mul_f32 v[28:29], v[28:29], v[34:35]
	s_waitcnt lgkmcnt(0)
	v_pk_add_f32 v[34:35], v[40:41], 1.0 op_sel_hi:[1,0]
	v_pk_add_f32 v[32:33], v[42:43], 1.0 op_sel_hi:[1,0]
	v_pk_fma_f32 v[30:31], v[30:31], v[34:35], v[36:37]
	v_pk_fma_f32 v[28:29], v[28:29], v[32:33], v[38:39]
	v_mul_f32_e32 v30, 0x41000000, v30
	v_mul_f32_e32 v31, 0x41000000, v31
	v_med3_f32 v30, v30, s8, v225
	v_med3_f32 v31, v31, s8, v225
	v_mov_b32_e32 v32, v3
	v_cvt_pk_fp8_f32 v32, v30, v31
	v_mul_f32_e32 v28, 0x41000000, v28
	v_mul_f32_e32 v29, 0x41000000, v29
	v_med3_f32 v28, v28, s8, v225
	v_med3_f32 v29, v29, s8, v225
	v_cvt_pk_fp8_f32 v32, v28, v29 op_sel:[0,0,1]
	s_waitcnt vmcnt(22)
	v_mov_b64_e32 v[42:43], v[78:79]
	s_waitcnt vmcnt(21)
	v_mov_b64_e32 v[40:41], v[80:81]
	s_waitcnt vmcnt(20)
	v_mov_b64_e32 v[38:39], v[82:83]
	global_store_dword v[26:27], v32, off offset:1792
	s_waitcnt vmcnt(20)
	v_mov_b64_e32 v[36:37], v[84:85]
	s_waitcnt vmcnt(19)
	v_mov_b64_e32 v[34:35], v[86:87]
	s_waitcnt vmcnt(18)
	v_mov_b64_e32 v[32:33], v[88:89]
	s_waitcnt vmcnt(17)
	v_mov_b64_e32 v[30:31], v[90:91]
	s_waitcnt vmcnt(16)
	v_mov_b64_e32 v[28:29], v[92:93]
	s_andn2_b64 exec, exec, s[14:15]
	s_cbranch_execz .LBB0_1530

.LBB0_1526:
	s_or_b64 exec, exec, s[48:49]
	v_pk_mul_f32 v[110:111], v[72:73], v[72:73]
	v_pk_mul_f32 v[112:113], v[68:69], v[68:69]
	v_pk_mul_f32 v[106:107], v[74:75], v[74:75]
	v_pk_mul_f32 v[108:109], v[70:71], v[70:71]
	v_mov_b32_e32 v114, v110
	v_mov_b32_e32 v115, v112
	v_mov_b32_e32 v112, v111
	v_pk_mul_f32 v[102:103], v[66:67], v[66:67]
	v_pk_mul_f32 v[104:105], v[64:65], v[64:65]
	v_pk_add_f32 v[110:111], v[114:115], v[112:113]
	v_mov_b32_e32 v112, v106
	v_mov_b32_e32 v113, v108
	v_mov_b32_e32 v108, v107
	v_pk_add_f32 v[106:107], v[112:113], v[108:109]
	v_pk_mov_b32 v[108:109], v[104:105], v[102:103] op_sel:[1,0]
	v_mov_b32_e32 v105, v103
	v_pk_add_f32 v[102:103], v[108:109], v[104:105]
	v_pk_add_f32 v[106:107], v[110:111], v[106:107]
	v_pk_add_f32 v[102:103], v[102:103], v[102:103] op_sel_hi:[0,1]
	v_mul_f32_e32 v102, v60, v60
	v_pk_fma_f32 v[104:105], v[60:61], v[60:61], v[102:103] op_sel_hi:[1,1,0]
	v_mul_f32_e32 v102, v62, v62
	v_pk_add_f32 v[106:107], v[106:107], v[106:107] op_sel_hi:[0,1]
	v_pk_fma_f32 v[108:109], v[62:63], v[62:63], v[102:103] op_sel_hi:[1,1,0]
	v_mul_f32_e32 v104, v56, v56
	v_mul_f32_e32 v108, v57, v57
	v_mul_f32_e32 v102, v58, v58
	v_mul_f32_e32 v106, v59, v59
	v_pk_mul_f32 v[94:95], v[54:55], v[54:55]
	v_pk_mul_f32 v[100:101], v[52:53], v[52:53]
	v_pk_add_f32 v[104:105], v[104:105], v[108:109]
	v_pk_add_f32 v[102:103], v[102:103], v[106:107]
	v_mov_b32_e32 v77, v222
	v_pk_add_f32 v[102:103], v[104:105], v[102:103]
	v_pk_mov_b32 v[104:105], v[100:101], v[94:95] op_sel:[1,0]
	v_mov_b32_e32 v101, v95
	v_pk_add_f32 v[94:95], v[104:105], v[100:101]
	v_pk_add_f32 v[102:103], v[102:103], v[102:103] op_sel_hi:[0,1]
	v_pk_add_f32 v[94:95], v[94:95], v[94:95] op_sel_hi:[0,1]
	v_mul_f32_e32 v94, v48, v48
	v_pk_fma_f32 v[100:101], v[48:49], v[48:49], v[94:95] op_sel_hi:[1,1,0]
	v_mul_f32_e32 v94, v50, v50
	v_pk_fma_f32 v[104:105], v[50:51], v[50:51], v[94:95] op_sel_hi:[1,1,0]
	v_mul_f32_e32 v100, v46, v46
	v_mul_f32_e32 v104, v47, v47
	v_mul_f32_e32 v94, v44, v44
	v_mul_f32_e32 v102, v45, v45
	v_pk_add_f32 v[100:101], v[100:101], v[104:105]
	v_pk_add_f32 v[94:95], v[94:95], v[102:103]
	s_movk_i32 s0, 0x1fff
	v_pk_add_f32 v[94:95], v[100:101], v[94:95]
	v_add_f32_e32 v27, v94, v95
	s_nop 1
	v_add_f32_dpp v27, v27, v27 quad_perm:[1,0,3,2] row_mask:0xf bank_mask:0xf
	s_nop 1
	v_add_f32_dpp v27, v27, v27 quad_perm:[2,3,0,1] row_mask:0xf bank_mask:0xf
	s_nop 1
	v_add_f32_dpp v27, v27, v27 row_half_mirror row_mask:0xf bank_mask:0xf
	s_nop 1
	v_add_f32_dpp v27, v27, v27 row_mirror row_mask:0xf bank_mask:0xf
	s_nop 0
	v_readlane_b32 s100, v27, 0
	v_readlane_b32 s101, v27, 16
	s_nop 1
	v_mov_b32_e32 v77, s101
	v_add_f32_e32 v77, s100, v77
	v_readlane_b32 s100, v27, 32
	v_readlane_b32 s101, v27, 48
	s_nop 1
	v_mov_b32_e32 v99, s101
	v_add_f32_e32 v99, s100, v99
	v_add_f32_e32 v99, v77, v99
	v_mov_b32_e32 v100, 0
	v_cmp_lt_i32_e64 s[0:1], s0, v26
	s_waitcnt lgkmcnt(0)
	s_and_saveexec_b64 s[10:11], s[0:1]
	s_xor_b64 s[0:1], exec, s[10:11]
	s_cbranch_execz .LBB0_1528
	v_mov_b32_e32 v77, v3
	v_readlane_b32 s10, v253, 35
	v_lshlrev_b64 v[76:77], 12, v[76:77]
	v_readlane_b32 s11, v253, 36
	v_mov_b32_e32 v27, v3
	s_nop 0
	v_lshl_add_u64 v[94:95], s[10:11], 0, v[76:77]

.LBB0_1542:
	s_or_b64 exec, exec, s[4:5]
	s_waitcnt lgkmcnt(0)
	v_add_f32_e32 v85, v85, v133
	v_fmamk_f32 v85, v85, 0x3a000000, v213
	v_cmp_gt_f32_e32 vcc, s22, v85
	v_mul_f32_e32 v126, 0x4b800000, v85
	v_lshl_add_u64 v[128:129], v[128:129], 0, v[2:3]
	v_cndmask_b32_e32 v85, v85, v126, vcc
	v_rsq_f32_e32 v85, v85
	s_and_b64 s[0:1], exec, s[0:1]
	s_or_b64 s[48:49], s[0:1], s[48:49]
	v_mul_f32_e32 v126, 0x45800000, v85
	v_cndmask_b32_e32 v126, v85, v126, vcc
	v_min_i32_e32 v85, 0x2000, v92
	v_lshlrev_b32_e32 v85, 1, v85
	v_and_b32_e32 v85, 0xffffe000, v85
	v_add_u32_e32 v85, v130, v85
	ds_read_b128 v[134:137], v85
	ds_read_b128 v[138:141], v131
	v_pk_mul_f32 v[124:125], v[124:125], v[126:127] op_sel_hi:[1,0]
	v_pk_mul_f32 v[122:123], v[122:123], v[126:127] op_sel_hi:[1,0]
	v_pk_mul_f32 v[120:121], v[120:121], v[126:127] op_sel_hi:[1,0]
	v_pk_mul_f32 v[118:119], v[118:119], v[126:127] op_sel_hi:[1,0]
	s_waitcnt lgkmcnt(0)
	v_pk_mul_f32 v[138:139], v[122:123], v[138:139]
	v_pk_mul_f32 v[122:123], v[124:125], v[140:141]
	v_pk_fma_f32 v[124:125], v[134:135], v[138:139], v[32:33]
	v_pk_fma_f32 v[122:123], v[136:137], v[122:123], v[34:35]
	v_cvt_pk_bf16_f32 v32, v124, v125
	v_cvt_pk_bf16_f32 v33, v122, v123
	global_store_dwordx2 v[128:129], v[32:33], off
	ds_read_b128 v[134:137], v85 offset:1024
	ds_read_b128 v[32:35], v131 offset:1024
	v_pk_mul_f32 v[116:117], v[116:117], v[126:127] op_sel_hi:[1,0]
	v_pk_mul_f32 v[114:115], v[114:115], v[126:127] op_sel_hi:[1,0]
	v_pk_mul_f32 v[112:113], v[112:113], v[126:127] op_sel_hi:[1,0]
	v_pk_mul_f32 v[110:111], v[110:111], v[126:127] op_sel_hi:[1,0]
	s_waitcnt lgkmcnt(0)
	v_pk_mul_f32 v[118:119], v[118:119], v[32:33]
	v_pk_mul_f32 v[32:33], v[120:121], v[34:35]
	v_pk_fma_f32 v[34:35], v[134:135], v[118:119], v[28:29]
	v_pk_fma_f32 v[32:33], v[136:137], v[32:33], v[30:31]
	v_cvt_pk_bf16_f32 v28, v34, v35
	v_cvt_pk_bf16_f32 v29, v32, v33
	global_store_dwordx2 v[128:129], v[28:29], off offset:512
	ds_read_b128 v[118:121], v85 offset:2048
	ds_read_b128 v[28:31], v131 offset:2048
	v_pk_mul_f32 v[108:109], v[108:109], v[126:127] op_sel_hi:[1,0]
	v_pk_mul_f32 v[106:107], v[106:107], v[126:127] op_sel_hi:[1,0]
	v_pk_mul_f32 v[104:105], v[104:105], v[126:127] op_sel_hi:[1,0]
	v_pk_mul_f32 v[102:103], v[102:103], v[126:127] op_sel_hi:[1,0]
	s_waitcnt lgkmcnt(0)
	v_pk_mul_f32 v[114:115], v[114:115], v[28:29]
	v_pk_mul_f32 v[28:29], v[116:117], v[30:31]
	v_pk_fma_f32 v[30:31], v[118:119], v[114:115], v[24:25]
	v_pk_fma_f32 v[28:29], v[120:121], v[28:29], v[26:27]
	v_cvt_pk_bf16_f32 v24, v30, v31
	v_cvt_pk_bf16_f32 v25, v28, v29
	global_store_dwordx2 v[128:129], v[24:25], off offset:1024
	ds_read_b128 v[114:117], v85 offset:3072
	ds_read_b128 v[24:27], v131 offset:3072
	v_pk_mul_f32 v[100:101], v[100:101], v[126:127] op_sel_hi:[1,0]
	v_pk_mul_f32 v[98:99], v[98:99], v[126:127] op_sel_hi:[1,0]
	v_pk_mul_f32 v[94:95], v[94:95], v[126:127] op_sel_hi:[1,0]
	v_pk_mul_f32 v[96:97], v[96:97], v[126:127] op_sel_hi:[1,0]
	s_waitcnt lgkmcnt(0)
	v_pk_mul_f32 v[110:111], v[110:111], v[24:25]
	v_pk_mul_f32 v[24:25], v[112:113], v[26:27]
	v_pk_fma_f32 v[26:27], v[114:115], v[110:111], v[20:21]
	v_pk_fma_f32 v[24:25], v[116:117], v[24:25], v[22:23]
	v_cvt_pk_bf16_f32 v20, v26, v27
	v_cvt_pk_bf16_f32 v21, v24, v25
	global_store_dwordx2 v[128:129], v[20:21], off offset:1536
	ds_read_b128 v[110:113], v85 offset:4096
	ds_read_b128 v[20:23], v131 offset:4096
	s_waitcnt lgkmcnt(0)
	v_pk_mul_f32 v[106:107], v[106:107], v[20:21]
	v_pk_mul_f32 v[20:21], v[108:109], v[22:23]
	v_pk_fma_f32 v[22:23], v[110:111], v[106:107], v[16:17]
	v_pk_fma_f32 v[20:21], v[112:113], v[20:21], v[18:19]
	v_cvt_pk_bf16_f32 v16, v22, v23
	v_cvt_pk_bf16_f32 v17, v20, v21
	global_store_dwordx2 v[128:129], v[16:17], off offset:2048
	ds_read_b128 v[16:19], v85 offset:5120
	ds_read_b128 v[106:109], v131 offset:5120
	s_waitcnt lgkmcnt(0)
	v_pk_mul_f32 v[102:103], v[102:103], v[106:107]
	v_pk_mul_f32 v[104:105], v[104:105], v[108:109]
	v_pk_fma_f32 v[12:13], v[16:17], v[102:103], v[12:13]
	v_pk_fma_f32 v[14:15], v[18:19], v[104:105], v[14:15]
	v_cvt_pk_bf16_f32 v16, v12, v13
	v_cvt_pk_bf16_f32 v17, v14, v15
	global_store_dwordx2 v[128:129], v[16:17], off offset:2560
	ds_read_b128 v[16:19], v85 offset:6144
	ds_read_b128 v[102:105], v131 offset:6144
	s_waitcnt lgkmcnt(0)
	v_pk_mul_f32 v[98:99], v[98:99], v[102:103]
	v_pk_mul_f32 v[100:101], v[100:101], v[104:105]
	v_pk_fma_f32 v[8:9], v[16:17], v[98:99], v[8:9]
	v_pk_fma_f32 v[10:11], v[18:19], v[100:101], v[10:11]
	v_cvt_pk_bf16_f32 v16, v8, v9
	v_cvt_pk_bf16_f32 v17, v10, v11
	global_store_dwordx2 v[128:129], v[16:17], off offset:3072
	ds_read_b128 v[16:19], v85 offset:7168
	ds_read_b128 v[98:101], v131 offset:7168
	s_waitcnt lgkmcnt(0)
	v_pk_mul_f32 v[96:97], v[96:97], v[98:99]
	v_pk_mul_f32 v[94:95], v[94:95], v[100:101]
	v_pk_fma_f32 v[4:5], v[16:17], v[96:97], v[4:5]
	v_pk_fma_f32 v[6:7], v[18:19], v[94:95], v[6:7]
	v_cvt_pk_bf16_f32 v16, v4, v5
	v_cvt_pk_bf16_f32 v17, v6, v7
	v_mov_b32_e32 v18, v125
	v_mov_b32_e32 v19, v35
	global_store_dwordx2 v[128:129], v[16:17], off offset:3584
	v_mov_b32_e32 v16, v124
	v_mov_b32_e32 v17, v34
	v_pk_mul_f32 v[18:19], v[18:19], v[18:19]
	v_mov_b32_e32 v94, v123
	v_mov_b32_e32 v95, v33
	v_pk_fma_f32 v[16:17], v[16:17], v[16:17], v[18:19]
	v_mov_b32_e32 v18, v122
	v_mov_b32_e32 v19, v32
	v_pk_mul_f32 v[94:95], v[94:95], v[94:95]
	s_nop 0
	v_pk_fma_f32 v[18:19], v[18:19], v[18:19], v[94:95]
	v_pk_mul_f32 v[94:95], v[30:31], v[30:31]
	v_pk_add_f32 v[16:17], v[16:17], v[18:19]
	v_pk_mul_f32 v[18:19], v[28:29], v[28:29]
	v_pk_add_f32 v[16:17], v[16:17], v[16:17] op_sel:[0,1] op_sel_hi:[1,0]
	v_pk_mov_b32 v[96:97], v[94:95], v[18:19] op_sel:[1,0]
	v_mov_b32_e32 v95, v19
	v_pk_add_f32 v[18:19], v[96:97], v[94:95]
	v_mul_f32_e32 v94, v22, v22
	v_mul_f32_e32 v95, v23, v23
	v_pk_add_f32 v[18:19], v[18:19], v[18:19] op_sel:[0,1] op_sel_hi:[1,0]
	v_mov_b32_e32 v17, v94
	v_mov_b32_e32 v19, v95
	v_pk_add_f32 v[16:17], v[16:17], v[18:19]
	v_mul_f32_e32 v18, v27, v27
	v_mul_f32_e32 v94, v25, v25
	v_mul_f32_e32 v96, v20, v20
	v_mul_f32_e32 v97, v21, v21
	v_pk_fma_f32 v[18:19], v[26:27], v[26:27], v[18:19] op_sel_hi:[1,1,0]
	v_pk_fma_f32 v[94:95], v[24:25], v[24:25], v[94:95] op_sel_hi:[1,1,0]
	v_mov_b32_e32 v19, v96
	v_mov_b32_e32 v95, v97
	v_pk_add_f32 v[18:19], v[18:19], v[94:95]
	v_pk_mul_f32 v[94:95], v[12:13], v[12:13]
	v_pk_add_f32 v[16:17], v[16:17], v[18:19]
	v_pk_mul_f32 v[18:19], v[14:15], v[14:15]
	v_pk_add_f32 v[16:17], v[16:17], v[16:17] op_sel:[0,1] op_sel_hi:[1,0]
	v_pk_mov_b32 v[96:97], v[94:95], v[18:19] op_sel:[1,0]
	v_mov_b32_e32 v95, v19
	v_pk_add_f32 v[18:19], v[96:97], v[94:95]
	v_mul_f32_e32 v94, v4, v4
	v_mul_f32_e32 v95, v5, v5
	v_pk_add_f32 v[18:19], v[18:19], v[18:19] op_sel:[0,1] op_sel_hi:[1,0]
	v_mov_b32_e32 v17, v94
	v_mov_b32_e32 v19, v95
	v_pk_add_f32 v[16:17], v[16:17], v[18:19]
	v_mul_f32_e32 v18, v9, v9
	v_mul_f32_e32 v94, v11, v11
	v_mul_f32_e32 v96, v6, v6
	v_mul_f32_e32 v97, v7, v7
	v_pk_fma_f32 v[18:19], v[8:9], v[8:9], v[18:19] op_sel_hi:[1,1,0]
	v_pk_fma_f32 v[94:95], v[10:11], v[10:11], v[94:95] op_sel_hi:[1,1,0]
	v_mov_b32_e32 v19, v96
	v_mov_b32_e32 v95, v97
	v_pk_add_f32 v[18:19], v[18:19], v[94:95]
	s_nop 0
	v_pk_add_f32 v[16:17], v[16:17], v[18:19]
	s_nop 0
	v_add_f32_e32 v16, v16, v17
	s_nop 1
	v_add_f32_dpp v16, v16, v16 quad_perm:[1,0,3,2] row_mask:0xf bank_mask:0xf
	s_nop 1
	v_add_f32_dpp v16, v16, v16 quad_perm:[2,3,0,1] row_mask:0xf bank_mask:0xf
	s_nop 1
	v_add_f32_dpp v16, v16, v16 row_half_mirror row_mask:0xf bank_mask:0xf
	s_nop 1
	v_add_f32_dpp v16, v16, v16 row_mirror row_mask:0xf bank_mask:0xf
	s_nop 0
	v_readlane_b32 s100, v16, 0
	v_readlane_b32 s101, v16, 16
	s_nop 1
	v_mov_b32_e32 v17, s101
	v_add_f32_e32 v17, s100, v17
	v_readlane_b32 s100, v16, 32
	v_readlane_b32 s101, v16, 48
	s_nop 1
	v_mov_b32_e32 v16, s101
	v_add_f32_e32 v16, s100, v16
	v_add_f32_e32 v16, v17, v16
	s_waitcnt lgkmcnt(0)
	v_fmamk_f32 v16, v16, 0x3a000000, v213
	v_cmp_gt_f32_e32 vcc, s22, v16
	v_mul_f32_e32 v17, 0x4b800000, v16
	s_nop 0
	v_cndmask_b32_e32 v16, v16, v17, vcc
	v_rsq_f32_e32 v16, v16
	s_nop 0
	v_mul_f32_e32 v17, 0x45800000, v16
	v_cndmask_b32_e32 v18, v16, v17, vcc
	v_lshlrev_b64 v[16:17], 11, v[92:93]
	ds_read_b128 v[92:95], v132
	ds_read_b128 v[96:99], v85 offset:24576
	ds_read_b128 v[100:103], v85 offset:49152
	v_pk_mul_f32 v[106:107], v[124:125], v[18:19] op_sel_hi:[1,0]
	v_pk_mul_f32 v[104:105], v[122:123], v[18:19] op_sel_hi:[1,0]
	s_waitcnt lgkmcnt(2)
	v_pk_mul_f32 v[92:93], v[92:93], v[106:107]
	v_pk_mul_f32 v[94:95], v[94:95], v[104:105]
	s_waitcnt lgkmcnt(0)
	v_pk_add_f32 v[100:101], v[100:101], 1.0 op_sel_hi:[1,0]
	v_pk_add_f32 v[102:103], v[102:103], 1.0 op_sel_hi:[1,0]
	v_pk_fma_f32 v[92:93], v[100:101], v[92:93], v[96:97]
	v_pk_fma_f32 v[94:95], v[102:103], v[94:95], v[98:99]
	v_mul_f32_e32 v19, 0x41000000, v92
	v_mul_f32_e32 v92, 0x41000000, v93
	v_mul_f32_e32 v93, 0x41000000, v94
	v_mul_f32_e32 v94, 0x41000000, v95
	v_med3_f32 v19, v19, s8, v225
	v_med3_f32 v92, v92, s8, v225
	v_mov_b32_e32 v95, v3
	v_cvt_pk_fp8_f32 v95, v19, v92
	v_med3_f32 v19, v93, s8, v225
	v_med3_f32 v92, v94, s8, v225
	v_lshl_add_u64 v[16:17], v[90:91], 0, v[16:17]
	v_cvt_pk_fp8_f32 v95, v19, v92 op_sel:[0,0,1]
	v_pk_mul_f32 v[32:33], v[32:33], v[18:19] op_sel_hi:[1,0]
	v_pk_mul_f32 v[34:35], v[34:35], v[18:19] op_sel_hi:[1,0]
	global_store_dword v[16:17], v95, off
	ds_read_b128 v[92:95], v132 offset:1024
	ds_read_b128 v[96:99], v85 offset:25600
	ds_read_b128 v[100:103], v85 offset:50176
	s_waitcnt lgkmcnt(2)
	v_pk_mul_f32 v[34:35], v[92:93], v[34:35]
	v_pk_mul_f32 v[32:33], v[94:95], v[32:33]
	s_waitcnt lgkmcnt(0)
	v_pk_add_f32 v[94:95], v[100:101], 1.0 op_sel_hi:[1,0]
	v_pk_add_f32 v[92:93], v[102:103], 1.0 op_sel_hi:[1,0]
	v_pk_fma_f32 v[34:35], v[94:95], v[34:35], v[96:97]
	v_pk_fma_f32 v[32:33], v[92:93], v[32:33], v[98:99]
	v_mul_f32_e32 v19, 0x41000000, v34
	v_mul_f32_e32 v34, 0x41000000, v35
	v_med3_f32 v19, v19, s8, v225
	v_med3_f32 v34, v34, s8, v225
	v_mov_b32_e32 v35, v3
	v_cvt_pk_fp8_f32 v35, v19, v34
	v_mul_f32_e32 v32, 0x41000000, v32
	v_mul_f32_e32 v33, 0x41000000, v33
	v_med3_f32 v19, v32, s8, v225
	v_med3_f32 v32, v33, s8, v225
	v_cvt_pk_fp8_f32 v35, v19, v32 op_sel:[0,0,1]
	v_pk_mul_f32 v[28:29], v[28:29], v[18:19] op_sel_hi:[1,0]
	v_pk_mul_f32 v[30:31], v[30:31], v[18:19] op_sel_hi:[1,0]
	global_store_dword v[16:17], v35, off offset:256
	ds_read_b128 v[32:35], v132 offset:2048
	ds_read_b128 v[92:95], v85 offset:26624
	ds_read_b128 v[96:99], v85 offset:51200
	s_waitcnt lgkmcnt(2)
	v_pk_mul_f32 v[30:31], v[30:31], v[32:33]
	v_pk_mul_f32 v[28:29], v[28:29], v[34:35]
	s_waitcnt lgkmcnt(0)
	v_pk_add_f32 v[34:35], v[96:97], 1.0 op_sel_hi:[1,0]
	v_pk_add_f32 v[32:33], v[98:99], 1.0 op_sel_hi:[1,0]
	v_pk_fma_f32 v[30:31], v[30:31], v[34:35], v[92:93]
	v_pk_fma_f32 v[28:29], v[28:29], v[32:33], v[94:95]
	v_mul_f32_e32 v19, 0x41000000, v30
	v_mul_f32_e32 v30, 0x41000000, v31
	v_med3_f32 v19, v19, s8, v225
	v_med3_f32 v30, v30, s8, v225
	v_mov_b32_e32 v31, v3
	v_cvt_pk_fp8_f32 v31, v19, v30
	v_mul_f32_e32 v28, 0x41000000, v28
	v_mul_f32_e32 v29, 0x41000000, v29
	v_med3_f32 v19, v28, s8, v225
	v_med3_f32 v28, v29, s8, v225
	v_cvt_pk_fp8_f32 v31, v19, v28 op_sel:[0,0,1]
	v_pk_mul_f32 v[24:25], v[24:25], v[18:19] op_sel_hi:[1,0]
	v_pk_mul_f32 v[26:27], v[26:27], v[18:19] op_sel_hi:[1,0]
	global_store_dword v[16:17], v31, off offset:512
	ds_read_b128 v[28:31], v132 offset:3072
	ds_read_b128 v[32:35], v85 offset:27648
	ds_read_b128 v[92:95], v85 offset:52224
	s_waitcnt lgkmcnt(2)
	v_pk_mul_f32 v[26:27], v[26:27], v[28:29]
	v_pk_mul_f32 v[24:25], v[24:25], v[30:31]
	s_waitcnt lgkmcnt(0)
	v_pk_add_f32 v[30:31], v[92:93], 1.0 op_sel_hi:[1,0]
	v_pk_add_f32 v[28:29], v[94:95], 1.0 op_sel_hi:[1,0]
	v_pk_fma_f32 v[26:27], v[26:27], v[30:31], v[32:33]
	v_pk_fma_f32 v[24:25], v[24:25], v[28:29], v[34:35]
	v_mul_f32_e32 v19, 0x41000000, v26
	v_mul_f32_e32 v26, 0x41000000, v27
	v_med3_f32 v19, v19, s8, v225
	v_med3_f32 v26, v26, s8, v225
	v_mov_b32_e32 v27, v3
	v_cvt_pk_fp8_f32 v27, v19, v26
	v_mul_f32_e32 v24, 0x41000000, v24
	v_mul_f32_e32 v25, 0x41000000, v25
	v_med3_f32 v19, v24, s8, v225
	v_med3_f32 v24, v25, s8, v225
	v_cvt_pk_fp8_f32 v27, v19, v24 op_sel:[0,0,1]
	v_pk_mul_f32 v[20:21], v[20:21], v[18:19] op_sel_hi:[1,0]
	v_pk_mul_f32 v[22:23], v[22:23], v[18:19] op_sel_hi:[1,0]
	global_store_dword v[16:17], v27, off offset:768
	ds_read_b128 v[24:27], v132 offset:4096
	ds_read_b128 v[28:31], v85 offset:28672
	ds_read_b128 v[32:35], v85 offset:53248
	s_waitcnt lgkmcnt(2)
	v_pk_mul_f32 v[22:23], v[22:23], v[24:25]
	v_pk_mul_f32 v[20:21], v[20:21], v[26:27]
	s_waitcnt lgkmcnt(0)
	v_pk_add_f32 v[26:27], v[32:33], 1.0 op_sel_hi:[1,0]
	v_pk_add_f32 v[24:25], v[34:35], 1.0 op_sel_hi:[1,0]
	v_pk_fma_f32 v[22:23], v[22:23], v[26:27], v[28:29]
	v_pk_fma_f32 v[20:21], v[20:21], v[24:25], v[30:31]
	v_mul_f32_e32 v19, 0x41000000, v22
	v_mul_f32_e32 v22, 0x41000000, v23
	v_med3_f32 v19, v19, s8, v225
	v_med3_f32 v22, v22, s8, v225
	v_mov_b32_e32 v23, v3
	v_cvt_pk_fp8_f32 v23, v19, v22
	v_mul_f32_e32 v20, 0x41000000, v20
	v_mul_f32_e32 v21, 0x41000000, v21
	v_med3_f32 v19, v20, s8, v225
	v_med3_f32 v20, v21, s8, v225
	v_cvt_pk_fp8_f32 v23, v19, v20 op_sel:[0,0,1]
	v_pk_mul_f32 v[14:15], v[14:15], v[18:19] op_sel_hi:[1,0]
	v_pk_mul_f32 v[12:13], v[12:13], v[18:19] op_sel_hi:[1,0]
	v_mov_b32_e32 v19, v3
	global_store_dword v[16:17], v23, off offset:1024
	ds_read_b128 v[20:23], v132 offset:5120
	ds_read_b128 v[24:27], v85 offset:29696
	ds_read_b128 v[28:31], v85 offset:54272
	s_waitcnt vmcnt(20)
	v_mov_b64_e32 v[32:33], v[36:37]
	v_mov_b64_e32 v[34:35], v[38:39]
	s_waitcnt lgkmcnt(2)
	v_pk_mul_f32 v[12:13], v[12:13], v[20:21]
	v_pk_mul_f32 v[14:15], v[14:15], v[22:23]
	s_waitcnt lgkmcnt(0)
	v_pk_add_f32 v[22:23], v[28:29], 1.0 op_sel_hi:[1,0]
	v_pk_add_f32 v[20:21], v[30:31], 1.0 op_sel_hi:[1,0]
	v_pk_fma_f32 v[12:13], v[12:13], v[22:23], v[24:25]
	v_pk_fma_f32 v[14:15], v[14:15], v[20:21], v[26:27]
	v_mul_f32_e32 v12, 0x41000000, v12
	v_mul_f32_e32 v13, 0x41000000, v13
	v_med3_f32 v12, v12, s8, v225
	v_med3_f32 v13, v13, s8, v225
	v_cvt_pk_fp8_f32 v19, v12, v13
	v_mul_f32_e32 v14, 0x41000000, v14
	v_mul_f32_e32 v15, 0x41000000, v15
	v_med3_f32 v12, v14, s8, v225
	v_med3_f32 v13, v15, s8, v225
	v_cvt_pk_fp8_f32 v19, v12, v13 op_sel:[0,0,1]
	s_waitcnt vmcnt(19)
	v_mov_b64_e32 v[28:29], v[40:41]
	v_mov_b64_e32 v[30:31], v[42:43]
	global_store_dword v[16:17], v19, off offset:1280
	ds_read_b128 v[12:15], v132 offset:6144
	ds_read_b128 v[20:23], v85 offset:30720
	ds_read_b128 v[24:27], v85 offset:55296
	v_pk_mul_f32 v[10:11], v[10:11], v[18:19] op_sel_hi:[1,0]
	v_pk_mul_f32 v[8:9], v[8:9], v[18:19] op_sel_hi:[1,0]
	s_waitcnt lgkmcnt(2)
	v_pk_mul_f32 v[10:11], v[10:11], v[14:15]
	v_pk_mul_f32 v[8:9], v[8:9], v[12:13]
	s_waitcnt lgkmcnt(0)
	v_pk_add_f32 v[14:15], v[24:25], 1.0 op_sel_hi:[1,0]
	v_pk_add_f32 v[12:13], v[26:27], 1.0 op_sel_hi:[1,0]
	v_pk_fma_f32 v[8:9], v[8:9], v[14:15], v[20:21]
	v_pk_fma_f32 v[10:11], v[10:11], v[12:13], v[22:23]
	v_mul_f32_e32 v8, 0x41000000, v8
	v_mul_f32_e32 v9, 0x41000000, v9
	v_med3_f32 v8, v8, s8, v225
	v_med3_f32 v9, v9, s8, v225
	v_mov_b32_e32 v12, v3
	v_cvt_pk_fp8_f32 v12, v8, v9
	v_mul_f32_e32 v10, 0x41000000, v10
	v_mul_f32_e32 v11, 0x41000000, v11
	v_med3_f32 v8, v10, s8, v225
	v_med3_f32 v9, v11, s8, v225
	v_cvt_pk_fp8_f32 v12, v8, v9 op_sel:[0,0,1]
	v_pk_mul_f32 v[6:7], v[6:7], v[18:19] op_sel_hi:[1,0]
	v_pk_mul_f32 v[4:5], v[4:5], v[18:19] op_sel_hi:[1,0]
	s_waitcnt vmcnt(19)
	v_mov_b64_e32 v[24:25], v[44:45]
	global_store_dword v[16:17], v12, off offset:1536
	ds_read_b128 v[8:11], v132 offset:7168
	ds_read_b128 v[12:15], v85 offset:31744
	ds_read_b128 v[20:23], v85 offset:56320
	v_mov_b64_e32 v[26:27], v[46:47]
	s_waitcnt lgkmcnt(2)
	v_pk_mul_f32 v[4:5], v[4:5], v[8:9]
	v_pk_mul_f32 v[6:7], v[6:7], v[10:11]
	s_waitcnt lgkmcnt(0)
	v_pk_add_f32 v[10:11], v[20:21], 1.0 op_sel_hi:[1,0]
	v_pk_add_f32 v[8:9], v[22:23], 1.0 op_sel_hi:[1,0]
	v_pk_fma_f32 v[4:5], v[4:5], v[10:11], v[12:13]
	v_pk_fma_f32 v[6:7], v[6:7], v[8:9], v[14:15]
	v_mul_f32_e32 v4, 0x41000000, v4
	v_mul_f32_e32 v5, 0x41000000, v5
	v_med3_f32 v4, v4, s8, v225
	v_med3_f32 v5, v5, s8, v225
	v_mov_b32_e32 v8, v3
	v_cvt_pk_fp8_f32 v8, v4, v5
	v_mul_f32_e32 v6, 0x41000000, v6
	v_mul_f32_e32 v7, 0x41000000, v7
	v_med3_f32 v4, v6, s8, v225
	v_med3_f32 v5, v7, s8, v225
	v_cvt_pk_fp8_f32 v8, v4, v5 op_sel:[0,0,1]
	s_waitcnt vmcnt(19)
	v_mov_b64_e32 v[20:21], v[48:49]
	s_waitcnt vmcnt(17)
	v_mov_b64_e32 v[12:13], v[56:57]
	s_waitcnt vmcnt(15)
	v_mov_b64_e32 v[4:5], v[64:65]
	global_store_dword v[16:17], v8, off offset:1792
	v_mov_b64_e32 v[16:17], v[52:53]
	v_mov_b64_e32 v[8:9], v[60:61]
	v_mov_b64_e32 v[22:23], v[50:51]
	v_mov_b64_e32 v[18:19], v[54:55]
	v_mov_b64_e32 v[14:15], v[58:59]
	v_mov_b64_e32 v[10:11], v[62:63]
	v_mov_b64_e32 v[6:7], v[66:67]
	s_andn2_b64 exec, exec, s[48:49]
	s_cbranch_execz .LBB0_1556

.LBB0_1552:
	s_or_b64 exec, exec, s[50:51]
	v_pk_mul_f32 v[144:145], v[122:123], v[122:123]
	v_pk_mul_f32 v[146:147], v[118:119], v[118:119]
	v_pk_mul_f32 v[140:141], v[124:125], v[124:125]
	v_pk_mul_f32 v[142:143], v[120:121], v[120:121]
	v_mov_b32_e32 v148, v144
	v_mov_b32_e32 v149, v146
	v_mov_b32_e32 v146, v145
	v_pk_mul_f32 v[136:137], v[116:117], v[116:117]
	v_pk_mul_f32 v[138:139], v[114:115], v[114:115]
	v_pk_add_f32 v[144:145], v[148:149], v[146:147]
	v_mov_b32_e32 v146, v140
	v_mov_b32_e32 v147, v142
	v_mov_b32_e32 v142, v141
	v_pk_add_f32 v[140:141], v[146:147], v[142:143]
	v_pk_mov_b32 v[142:143], v[138:139], v[136:137] op_sel:[1,0]
	v_mov_b32_e32 v139, v137
	v_pk_add_f32 v[136:137], v[142:143], v[138:139]
	v_pk_add_f32 v[140:141], v[144:145], v[140:141]
	v_pk_add_f32 v[136:137], v[136:137], v[136:137] op_sel_hi:[0,1]
	v_mul_f32_e32 v136, v110, v110
	v_pk_fma_f32 v[138:139], v[110:111], v[110:111], v[136:137] op_sel_hi:[1,1,0]
	v_mul_f32_e32 v136, v112, v112
	v_pk_add_f32 v[140:141], v[140:141], v[140:141] op_sel_hi:[0,1]
	v_pk_fma_f32 v[142:143], v[112:113], v[112:113], v[136:137] op_sel_hi:[1,1,0]
	v_mul_f32_e32 v138, v106, v106
	v_mul_f32_e32 v142, v107, v107
	v_mul_f32_e32 v136, v108, v108
	v_mul_f32_e32 v140, v109, v109
	v_pk_mul_f32 v[128:129], v[104:105], v[104:105]
	v_pk_mul_f32 v[134:135], v[102:103], v[102:103]
	v_pk_add_f32 v[138:139], v[138:139], v[142:143]
	v_pk_add_f32 v[136:137], v[136:137], v[140:141]
	v_mov_b32_e32 v93, v222
	v_pk_add_f32 v[136:137], v[138:139], v[136:137]
	v_pk_mov_b32 v[138:139], v[134:135], v[128:129] op_sel:[1,0]
	v_mov_b32_e32 v135, v129
	v_pk_add_f32 v[128:129], v[138:139], v[134:135]
	v_pk_add_f32 v[136:137], v[136:137], v[136:137] op_sel_hi:[0,1]
	v_pk_add_f32 v[128:129], v[128:129], v[128:129] op_sel_hi:[0,1]
	v_mul_f32_e32 v128, v98, v98
	v_pk_fma_f32 v[134:135], v[98:99], v[98:99], v[128:129] op_sel_hi:[1,1,0]
	v_mul_f32_e32 v128, v100, v100
	v_pk_fma_f32 v[138:139], v[100:101], v[100:101], v[128:129] op_sel_hi:[1,1,0]
	v_mul_f32_e32 v134, v96, v96
	v_mul_f32_e32 v138, v97, v97
	v_mul_f32_e32 v128, v94, v94
	v_mul_f32_e32 v136, v95, v95
	v_pk_add_f32 v[134:135], v[134:135], v[138:139]
	v_pk_add_f32 v[128:129], v[128:129], v[136:137]
	s_movk_i32 s4, 0x1fff
	v_pk_add_f32 v[128:129], v[134:135], v[128:129]
	v_add_f32_e32 v85, v128, v129
	s_nop 1
	v_add_f32_dpp v85, v85, v85 quad_perm:[1,0,3,2] row_mask:0xf bank_mask:0xf
	s_nop 1
	v_add_f32_dpp v85, v85, v85 quad_perm:[2,3,0,1] row_mask:0xf bank_mask:0xf
	s_nop 1
	v_add_f32_dpp v85, v85, v85 row_half_mirror row_mask:0xf bank_mask:0xf
	s_nop 1
	v_add_f32_dpp v85, v85, v85 row_mirror row_mask:0xf bank_mask:0xf
	s_nop 0
	v_readlane_b32 s100, v85, 0
	v_readlane_b32 s101, v85, 16
	s_nop 1
	v_mov_b32_e32 v93, s101
	v_add_f32_e32 v93, s100, v93
	v_readlane_b32 s100, v85, 32
	v_readlane_b32 s101, v85, 48
	s_nop 1
	v_mov_b32_e32 v85, s101
	v_add_f32_e32 v85, s100, v85
	v_add_f32_e32 v85, v93, v85
	v_mov_b32_e32 v133, 0
	v_cmp_lt_i32_e32 vcc, s4, v92
	s_waitcnt lgkmcnt(0)
	s_and_saveexec_b64 s[4:5], vcc
	s_xor_b64 s[4:5], exec, s[4:5]
	s_cbranch_execz .LBB0_1554
	v_mov_b32_e32 v127, v3
	v_readlane_b32 s10, v253, 35
	v_lshlrev_b64 v[126:127], 12, v[126:127]
	v_readlane_b32 s11, v253, 36
	v_mov_b32_e32 v93, v3
	s_nop 0
	v_lshl_add_u64 v[128:129], s[10:11], 0, v[126:127]

.LBB0_1583:
	s_or_b64 exec, exec, s[0:1]
	v_pk_mul_f32 v[112:113], v[88:89], v[88:89]
	v_pk_mul_f32 v[114:115], v[84:85], v[84:85]
	v_pk_mul_f32 v[102:103], v[90:91], v[90:91]
	v_pk_mul_f32 v[110:111], v[86:87], v[86:87]
	v_mov_b32_e32 v116, v112
	v_mov_b32_e32 v117, v114
	v_mov_b32_e32 v114, v113
	v_pk_mul_f32 v[98:99], v[82:83], v[82:83]
	v_pk_mul_f32 v[100:101], v[80:81], v[80:81]
	v_pk_add_f32 v[112:113], v[116:117], v[114:115]
	v_mov_b32_e32 v114, v102
	v_mov_b32_e32 v115, v110
	v_mov_b32_e32 v110, v103
	v_pk_add_f32 v[102:103], v[114:115], v[110:111]
	v_pk_mov_b32 v[110:111], v[100:101], v[98:99] op_sel:[1,0]
	v_mov_b32_e32 v101, v99
	v_pk_add_f32 v[98:99], v[110:111], v[100:101]
	v_pk_add_f32 v[102:103], v[112:113], v[102:103]
	v_pk_add_f32 v[98:99], v[98:99], v[98:99] op_sel_hi:[0,1]
	v_mul_f32_e32 v98, v76, v76
	v_pk_fma_f32 v[100:101], v[76:77], v[76:77], v[98:99] op_sel_hi:[1,1,0]
	v_mul_f32_e32 v98, v78, v78
	v_pk_add_f32 v[102:103], v[102:103], v[102:103] op_sel_hi:[0,1]
	v_pk_fma_f32 v[110:111], v[78:79], v[78:79], v[98:99] op_sel_hi:[1,1,0]
	v_mul_f32_e32 v100, v32, v32
	v_mul_f32_e32 v110, v33, v33
	v_mul_f32_e32 v98, v34, v34
	v_mul_f32_e32 v102, v35, v35
	v_pk_mul_f32 v[94:95], v[30:31], v[30:31]
	v_pk_mul_f32 v[96:97], v[28:29], v[28:29]
	v_pk_add_f32 v[100:101], v[100:101], v[110:111]
	v_pk_add_f32 v[98:99], v[98:99], v[102:103]
	v_mov_b32_e32 v93, v222
	v_pk_add_f32 v[98:99], v[100:101], v[98:99]
	v_pk_mov_b32 v[100:101], v[96:97], v[94:95] op_sel:[1,0]
	v_mov_b32_e32 v97, v95
	v_pk_add_f32 v[94:95], v[100:101], v[96:97]
	v_pk_add_f32 v[98:99], v[98:99], v[98:99] op_sel_hi:[0,1]
	v_pk_add_f32 v[94:95], v[94:95], v[94:95] op_sel_hi:[0,1]
	v_mul_f32_e32 v94, v24, v24
	v_pk_fma_f32 v[96:97], v[24:25], v[24:25], v[94:95] op_sel_hi:[1,1,0]
	v_mul_f32_e32 v94, v26, v26
	v_pk_fma_f32 v[100:101], v[26:27], v[26:27], v[94:95] op_sel_hi:[1,1,0]
	v_mul_f32_e32 v96, v22, v22
	v_mul_f32_e32 v100, v23, v23
	v_mul_f32_e32 v94, v20, v20
	v_mul_f32_e32 v98, v21, v21
	v_pk_add_f32 v[96:97], v[96:97], v[100:101]
	v_pk_add_f32 v[94:95], v[94:95], v[98:99]
	s_movk_i32 s0, 0x1fff
	v_pk_add_f32 v[94:95], v[96:97], v[94:95]
	v_add_f32_e32 v59, v94, v95
	s_nop 1
	v_add_f32_dpp v59, v59, v59 quad_perm:[1,0,3,2] row_mask:0xf bank_mask:0xf
	s_nop 1
	v_add_f32_dpp v59, v59, v59 quad_perm:[2,3,0,1] row_mask:0xf bank_mask:0xf
	s_nop 1
	v_add_f32_dpp v59, v59, v59 row_half_mirror row_mask:0xf bank_mask:0xf
	s_nop 1
	v_add_f32_dpp v59, v59, v59 row_mirror row_mask:0xf bank_mask:0xf
	s_nop 0
	v_readlane_b32 s100, v59, 0
	v_readlane_b32 s101, v59, 16
	s_nop 1
	v_mov_b32_e32 v93, s101
	v_add_f32_e32 v93, s100, v93
	v_readlane_b32 s100, v59, 32
	v_readlane_b32 s101, v59, 48
	s_nop 1
	v_mov_b32_e32 v96, s101
	v_add_f32_e32 v96, s100, v96
	v_add_f32_e32 v96, v93, v96
	v_mov_b32_e32 v97, 0
	v_cmp_lt_i32_e32 vcc, s0, v58
	s_waitcnt lgkmcnt(0)
	s_and_saveexec_b64 s[0:1], vcc
	s_xor_b64 s[0:1], exec, s[0:1]
	s_cbranch_execz .LBB0_1585
	v_mov_b32_e32 v93, v3
	v_readlane_b32 s4, v253, 35
	v_lshlrev_b64 v[92:93], 12, v[92:93]
	v_readlane_b32 s5, v253, 36
	v_mov_b32_e32 v59, v3
	s_nop 0
	v_lshl_add_u64 v[94:95], s[4:5], 0, v[92:93]

.LBB0_1587:
	s_or_b64 exec, exec, s[0:1]
	s_waitcnt lgkmcnt(0)
	v_add_f32_e32 v92, v96, v97
	v_fmamk_f32 v92, v92, 0x3a000000, v213
	s_mov_b32 s0, 0x800000
	v_cmp_gt_f32_e32 vcc, s0, v92
	v_mul_f32_e32 v93, 0x4b800000, v92
	v_min_i32_e32 v97, 0x2000, v58
	v_cndmask_b32_e32 v92, v92, v93, vcc
	v_rsq_f32_e32 v93, v92
	v_lshlrev_b32_e32 v100, 16, v8
	v_and_b32_e32 v101, 0xffff0000, v8
	v_lshlrev_b32_e32 v102, 16, v9
	v_and_b32_e32 v103, 0xffff0000, v9
	v_lshlrev_b32_e32 v8, 16, v4
	v_and_b32_e32 v9, 0xffff0000, v4
	v_lshlrev_b32_e32 v4, 1, v97
	v_and_b32_e32 v4, 0xffffe000, v4
	v_mul_f32_e32 v96, 0x45800000, v93
	v_lshlrev_b32_e32 v118, 16, v14
	v_and_b32_e32 v119, 0xffff0000, v14
	v_lshlrev_b32_e32 v120, 16, v15
	v_and_b32_e32 v121, 0xffff0000, v15
	v_lshlrev_b32_e32 v126, 16, v10
	v_and_b32_e32 v127, 0xffff0000, v10
	v_lshlrev_b32_e32 v128, 16, v11
	v_and_b32_e32 v129, 0xffff0000, v11
	v_lshlrev_b32_e32 v14, 16, v6
	v_and_b32_e32 v15, 0xffff0000, v6
	v_lshlrev_b32_e32 v98, 16, v7
	v_and_b32_e32 v99, 0xffff0000, v7
	v_lshlrev_b32_e32 v10, 16, v5
	v_and_b32_e32 v11, 0xffff0000, v5
	v_add_u32_e32 v110, v106, v4
	ds_read_b128 v[4:7], v107
	v_lshlrev_b32_e32 v92, 16, v18
	v_cndmask_b32_e32 v96, v93, v96, vcc
	v_and_b32_e32 v93, 0xffff0000, v18
	v_lshlrev_b32_e32 v112, 16, v19
	v_and_b32_e32 v113, 0xffff0000, v19
	v_lshlrev_b32_e32 v114, 16, v16
	v_and_b32_e32 v115, 0xffff0000, v16
	v_lshlrev_b32_e32 v116, 16, v17
	v_and_b32_e32 v117, 0xffff0000, v17
	ds_read_b128 v[16:19], v110
	v_pk_mul_f32 v[90:91], v[90:91], v[96:97] op_sel_hi:[1,0]
	v_pk_mul_f32 v[88:89], v[88:89], v[96:97] op_sel_hi:[1,0]
	v_lshlrev_b32_e32 v122, 16, v12
	s_waitcnt lgkmcnt(1)
	v_pk_mul_f32 v[88:89], v[88:89], v[4:5]
	v_pk_mul_f32 v[4:5], v[90:91], v[6:7]
	s_waitcnt lgkmcnt(0)
	v_pk_fma_f32 v[6:7], v[16:17], v[88:89], v[92:93]
	v_pk_fma_f32 v[4:5], v[18:19], v[4:5], v[112:113]
	v_and_b32_e32 v123, 0xffff0000, v12
	v_lshlrev_b32_e32 v124, 16, v13
	v_and_b32_e32 v125, 0xffff0000, v13
	v_lshl_add_u64 v[12:13], v[94:95], 0, v[2:3]
	v_cvt_pk_bf16_f32 v88, v6, v7
	v_cvt_pk_bf16_f32 v89, v4, v5
	ds_read_b128 v[16:19], v107 offset:1024
	global_store_dwordx2 v[12:13], v[88:89], off
	ds_read_b128 v[88:91], v110 offset:1024
	v_pk_mul_f32 v[86:87], v[86:87], v[96:97] op_sel_hi:[1,0]
	v_pk_mul_f32 v[84:85], v[84:85], v[96:97] op_sel_hi:[1,0]
	v_pk_mul_f32 v[82:83], v[82:83], v[96:97] op_sel_hi:[1,0]
	s_waitcnt lgkmcnt(1)
	v_pk_mul_f32 v[84:85], v[84:85], v[16:17]
	v_pk_mul_f32 v[16:17], v[86:87], v[18:19]
	s_waitcnt lgkmcnt(0)
	v_pk_fma_f32 v[18:19], v[88:89], v[84:85], v[114:115]
	v_pk_fma_f32 v[16:17], v[90:91], v[16:17], v[116:117]
	v_cvt_pk_bf16_f32 v88, v18, v19
	v_cvt_pk_bf16_f32 v89, v16, v17
	ds_read_b128 v[84:87], v107 offset:2048
	global_store_dwordx2 v[12:13], v[88:89], off offset:512
	ds_read_b128 v[88:91], v110 offset:2048
	v_pk_mul_f32 v[80:81], v[80:81], v[96:97] op_sel_hi:[1,0]
	v_pk_mul_f32 v[78:79], v[78:79], v[96:97] op_sel_hi:[1,0]
	s_waitcnt lgkmcnt(1)
	v_pk_mul_f32 v[80:81], v[80:81], v[84:85]
	v_pk_mul_f32 v[82:83], v[82:83], v[86:87]
	s_waitcnt lgkmcnt(0)
	v_pk_fma_f32 v[94:95], v[88:89], v[80:81], v[118:119]
	v_pk_fma_f32 v[92:93], v[90:91], v[82:83], v[120:121]
	v_cvt_pk_bf16_f32 v84, v94, v95
	v_cvt_pk_bf16_f32 v85, v92, v93
	ds_read_b128 v[80:83], v107 offset:3072
	global_store_dwordx2 v[12:13], v[84:85], off offset:1024
	ds_read_b128 v[84:87], v110 offset:3072
	v_pk_mul_f32 v[76:77], v[76:77], v[96:97] op_sel_hi:[1,0]
	v_pk_mul_f32 v[34:35], v[34:35], v[96:97] op_sel_hi:[1,0]
	s_waitcnt lgkmcnt(1)
	v_pk_mul_f32 v[76:77], v[76:77], v[80:81]
	v_pk_mul_f32 v[78:79], v[78:79], v[82:83]
	s_waitcnt lgkmcnt(0)
	v_pk_fma_f32 v[90:91], v[84:85], v[76:77], v[122:123]
	v_pk_fma_f32 v[88:89], v[86:87], v[78:79], v[124:125]
	v_cvt_pk_bf16_f32 v80, v90, v91
	v_cvt_pk_bf16_f32 v81, v88, v89
	ds_read_b128 v[76:79], v107 offset:4096
	global_store_dwordx2 v[12:13], v[80:81], off offset:1536
	ds_read_b128 v[80:83], v110 offset:4096
	v_pk_mul_f32 v[32:33], v[32:33], v[96:97] op_sel_hi:[1,0]
	v_pk_mul_f32 v[30:31], v[30:31], v[96:97] op_sel_hi:[1,0]
	s_waitcnt lgkmcnt(1)
	v_pk_mul_f32 v[32:33], v[32:33], v[76:77]
	v_pk_mul_f32 v[34:35], v[34:35], v[78:79]
	s_waitcnt lgkmcnt(0)
	v_pk_fma_f32 v[86:87], v[80:81], v[32:33], v[126:127]
	v_pk_fma_f32 v[84:85], v[82:83], v[34:35], v[128:129]
	v_cvt_pk_bf16_f32 v76, v86, v87
	v_cvt_pk_bf16_f32 v77, v84, v85
	ds_read_b128 v[32:35], v107 offset:5120
	global_store_dwordx2 v[12:13], v[76:77], off offset:2048
	ds_read_b128 v[76:79], v110 offset:5120
	v_pk_mul_f32 v[28:29], v[28:29], v[96:97] op_sel_hi:[1,0]
	v_pk_mul_f32 v[24:25], v[24:25], v[96:97] op_sel_hi:[1,0]
	s_waitcnt lgkmcnt(1)
	v_pk_mul_f32 v[28:29], v[28:29], v[32:33]
	v_pk_mul_f32 v[30:31], v[30:31], v[34:35]
	s_waitcnt lgkmcnt(0)
	v_pk_fma_f32 v[82:83], v[76:77], v[28:29], v[100:101]
	v_pk_fma_f32 v[80:81], v[78:79], v[30:31], v[102:103]
	v_cvt_pk_bf16_f32 v32, v82, v83
	v_cvt_pk_bf16_f32 v33, v80, v81
	ds_read_b128 v[28:31], v107 offset:6144
	global_store_dwordx2 v[12:13], v[32:33], off offset:2560
	ds_read_b128 v[32:35], v110 offset:6144
	v_pk_mul_f32 v[26:27], v[26:27], v[96:97] op_sel_hi:[1,0]
	s_waitcnt lgkmcnt(1)
	v_pk_mul_f32 v[28:29], v[24:25], v[28:29]
	v_pk_mul_f32 v[24:25], v[26:27], v[30:31]
	s_waitcnt lgkmcnt(0)
	v_pk_fma_f32 v[26:27], v[32:33], v[28:29], v[14:15]
	ds_read_b128 v[28:31], v107 offset:7168
	v_pk_fma_f32 v[24:25], v[34:35], v[24:25], v[98:99]
	ds_read_b128 v[32:35], v110 offset:7168
	v_cvt_pk_bf16_f32 v14, v26, v27
	v_cvt_pk_bf16_f32 v15, v24, v25
	global_store_dwordx2 v[12:13], v[14:15], off offset:3072
	v_pk_mul_f32 v[14:15], v[20:21], v[96:97] op_sel_hi:[1,0]
	v_pk_mul_f32 v[20:21], v[22:23], v[96:97] op_sel_hi:[1,0]
	s_waitcnt lgkmcnt(1)
	v_pk_mul_f32 v[14:15], v[14:15], v[30:31]
	v_pk_mul_f32 v[20:21], v[20:21], v[28:29]
	s_waitcnt lgkmcnt(0)
	v_pk_fma_f32 v[28:29], v[34:35], v[14:15], v[10:11]
	v_pk_fma_f32 v[30:31], v[32:33], v[20:21], v[8:9]
	v_cvt_pk_bf16_f32 v9, v28, v29
	v_cvt_pk_bf16_f32 v8, v30, v31
	v_mov_b32_e32 v10, v7
	v_mov_b32_e32 v11, v19
	global_store_dwordx2 v[12:13], v[8:9], off offset:3584
	v_mov_b32_e32 v8, v6
	v_mov_b32_e32 v9, v18
	v_pk_mul_f32 v[10:11], v[10:11], v[10:11]
	v_mov_b32_e32 v12, v5
	v_mov_b32_e32 v13, v17
	v_pk_fma_f32 v[8:9], v[8:9], v[8:9], v[10:11]
	v_mov_b32_e32 v10, v4
	v_mov_b32_e32 v11, v16
	v_pk_mul_f32 v[12:13], v[12:13], v[12:13]
	s_nop 0
	v_pk_fma_f32 v[10:11], v[10:11], v[10:11], v[12:13]
	v_pk_mul_f32 v[12:13], v[94:95], v[94:95]
	v_pk_add_f32 v[8:9], v[8:9], v[10:11]
	v_pk_mul_f32 v[10:11], v[92:93], v[92:93]
	v_pk_add_f32 v[8:9], v[8:9], v[8:9] op_sel:[0,1] op_sel_hi:[1,0]
	v_pk_mov_b32 v[14:15], v[12:13], v[10:11] op_sel:[1,0]
	v_mov_b32_e32 v13, v11
	v_pk_add_f32 v[10:11], v[14:15], v[12:13]
	v_mul_f32_e32 v12, v86, v86
	v_mul_f32_e32 v13, v87, v87
	v_pk_add_f32 v[10:11], v[10:11], v[10:11] op_sel:[0,1] op_sel_hi:[1,0]
	v_mov_b32_e32 v9, v12
	v_mov_b32_e32 v11, v13
	v_pk_add_f32 v[8:9], v[8:9], v[10:11]
	v_mul_f32_e32 v10, v91, v91
	v_mul_f32_e32 v12, v89, v89
	v_mul_f32_e32 v14, v84, v84
	v_mul_f32_e32 v15, v85, v85
	v_pk_fma_f32 v[10:11], v[90:91], v[90:91], v[10:11] op_sel_hi:[1,1,0]
	v_pk_fma_f32 v[12:13], v[88:89], v[88:89], v[12:13] op_sel_hi:[1,1,0]
	v_mov_b32_e32 v11, v14
	v_mov_b32_e32 v13, v15
	v_pk_add_f32 v[10:11], v[10:11], v[12:13]
	v_pk_mul_f32 v[12:13], v[82:83], v[82:83]
	v_pk_add_f32 v[8:9], v[8:9], v[10:11]
	v_pk_mul_f32 v[10:11], v[80:81], v[80:81]
	v_pk_add_f32 v[8:9], v[8:9], v[8:9] op_sel:[0,1] op_sel_hi:[1,0]
	v_pk_mov_b32 v[14:15], v[12:13], v[10:11] op_sel:[1,0]
	v_mov_b32_e32 v13, v11
	v_pk_add_f32 v[10:11], v[14:15], v[12:13]
	v_mul_f32_e32 v12, v30, v30
	v_mul_f32_e32 v13, v31, v31
	v_pk_add_f32 v[10:11], v[10:11], v[10:11] op_sel:[0,1] op_sel_hi:[1,0]
	v_mov_b32_e32 v9, v12
	v_mov_b32_e32 v11, v13
	v_pk_add_f32 v[8:9], v[8:9], v[10:11]
	v_mul_f32_e32 v10, v27, v27
	v_mul_f32_e32 v12, v25, v25
	v_mul_f32_e32 v14, v28, v28
	v_mul_f32_e32 v15, v29, v29
	v_pk_fma_f32 v[10:11], v[26:27], v[26:27], v[10:11] op_sel_hi:[1,1,0]
	v_pk_fma_f32 v[12:13], v[24:25], v[24:25], v[12:13] op_sel_hi:[1,1,0]
	v_mov_b32_e32 v11, v14
	v_mov_b32_e32 v13, v15
	v_pk_add_f32 v[10:11], v[10:11], v[12:13]
	s_nop 0
	v_pk_add_f32 v[8:9], v[8:9], v[10:11]
	s_nop 0
	v_add_f32_e32 v8, v8, v9
	s_nop 1
	v_add_f32_dpp v8, v8, v8 quad_perm:[1,0,3,2] row_mask:0xf bank_mask:0xf
	s_nop 1
	v_add_f32_dpp v8, v8, v8 quad_perm:[2,3,0,1] row_mask:0xf bank_mask:0xf
	s_nop 1
	v_add_f32_dpp v8, v8, v8 row_half_mirror row_mask:0xf bank_mask:0xf
	s_nop 1
	v_add_f32_dpp v8, v8, v8 row_mirror row_mask:0xf bank_mask:0xf
	s_nop 0
	v_readlane_b32 s100, v8, 0
	v_readlane_b32 s101, v8, 16
	s_nop 1
	v_mov_b32_e32 v9, s101
	v_add_f32_e32 v9, s100, v9
	v_readlane_b32 s100, v8, 32
	v_readlane_b32 s101, v8, 48
	s_nop 1
	v_mov_b32_e32 v8, s101
	v_add_f32_e32 v8, s100, v8
	v_add_f32_e32 v8, v9, v8
	s_waitcnt lgkmcnt(0)
	v_fmamk_f32 v8, v8, 0x3a000000, v213
	v_cmp_gt_f32_e32 vcc, s0, v8
	v_mul_f32_e32 v9, 0x4b800000, v8
	s_nop 0
	v_cndmask_b32_e32 v8, v8, v9, vcc
	v_rsq_f32_e32 v8, v8
	s_nop 0
	v_mul_f32_e32 v9, 0x45800000, v8
	v_cndmask_b32_e32 v34, v8, v9, vcc
	ds_read_b128 v[8:11], v108
	ds_read_b128 v[12:15], v110 offset:24576
	ds_read_b128 v[20:23], v110 offset:49152
	v_pk_mul_f32 v[4:5], v[4:5], v[34:35] op_sel_hi:[1,0]
	v_pk_mul_f32 v[6:7], v[6:7], v[34:35] op_sel_hi:[1,0]
	s_waitcnt lgkmcnt(2)
	v_pk_mul_f32 v[4:5], v[10:11], v[4:5]
	v_pk_mul_f32 v[6:7], v[8:9], v[6:7]
	s_waitcnt lgkmcnt(0)
	v_pk_add_f32 v[10:11], v[20:21], 1.0 op_sel_hi:[1,0]
	v_pk_add_f32 v[8:9], v[22:23], 1.0 op_sel_hi:[1,0]
	v_pk_fma_f32 v[78:79], v[10:11], v[6:7], v[12:13]
	v_pk_fma_f32 v[76:77], v[8:9], v[4:5], v[14:15]
	v_mul_f32_e32 v4, 0x41000000, v78
	v_mul_f32_e32 v5, 0x41000000, v79
	v_med3_f32 v4, v4, s8, v225
	v_med3_f32 v5, v5, s8, v225
	v_mov_b32_e32 v7, v3
	v_cvt_pk_fp8_f32 v7, v4, v5
	v_mul_f32_e32 v6, 0x41000000, v76
	v_mul_f32_e32 v4, 0x41000000, v77
	v_med3_f32 v5, v6, s8, v225
	v_med3_f32 v4, v4, s8, v225
	v_cvt_pk_fp8_f32 v7, v5, v4 op_sel:[0,0,1]
	ds_read_b128 v[12:15], v109 offset:16384
	v_lshlrev_b64 v[4:5], 11, v[58:59]
	v_lshl_add_u64 v[32:33], v[56:57], 0, v[4:5]
	global_store_dword v[32:33], v7, off
	ds_read_b128 v[4:7], v109
	ds_read_b128 v[8:11], v109 offset:8192
	ds_read_b128 v[20:23], v109 offset:24576
	s_waitcnt lgkmcnt(3)
	v_mul_f32_e32 v13, v13, v79
	v_fmac_f32_e32 v13, v12, v78
	v_mul_f32_e32 v12, v15, v77
	v_fmac_f32_e32 v12, v14, v76
	v_add_f32_e32 v12, v13, v12
	v_add_f32_e32 v100, 0, v12
	s_waitcnt lgkmcnt(0)
	v_mul_f32_e32 v21, v21, v79
	ds_read_b128 v[12:15], v109 offset:32768
	v_fmac_f32_e32 v21, v20, v78
	v_mul_f32_e32 v20, v23, v77
	v_fmac_f32_e32 v20, v22, v76
	v_add_f32_e32 v20, v21, v20
	v_add_f32_e32 v99, 0, v20
	ds_read_b128 v[20:23], v109 offset:40960
	s_waitcnt lgkmcnt(1)
	v_mul_f32_e32 v13, v13, v79
	v_fmac_f32_e32 v13, v12, v78
	v_mul_f32_e32 v12, v15, v77
	ds_read_b128 v[112:115], v109 offset:49152
	v_fmac_f32_e32 v12, v14, v76
	v_add_f32_e32 v12, v13, v12
	v_add_f32_e32 v98, 0, v12
	s_waitcnt lgkmcnt(1)
	v_mul_f32_e32 v12, v21, v79
	v_mul_f32_e32 v13, v23, v77
	v_fmac_f32_e32 v12, v20, v78
	v_fmac_f32_e32 v13, v22, v76
	v_add_f32_e32 v12, v12, v13
	s_waitcnt lgkmcnt(0)
	v_mul_f32_e32 v20, v113, v79
	v_mul_f32_e32 v21, v115, v77
	v_add_f32_e32 v97, 0, v12
	v_fmac_f32_e32 v20, v112, v78
	ds_read_b128 v[12:15], v109 offset:57344
	v_fmac_f32_e32 v21, v114, v76
	v_add_f32_e32 v20, v20, v21
	v_add_f32_e32 v35, 0, v20
	ds_read_b128 v[20:23], v108 offset:1024
	ds_read_b128 v[112:115], v110 offset:25600
	ds_read_b128 v[116:119], v110 offset:50176
	s_waitcnt lgkmcnt(3)
	v_mul_f32_e32 v96, v13, v79
	v_fmac_f32_e32 v96, v12, v78
	v_pk_mul_f32 v[12:13], v[16:17], v[34:35] op_sel_hi:[1,0]
	v_pk_mul_f32 v[16:17], v[18:19], v[34:35] op_sel_hi:[1,0]
	s_waitcnt lgkmcnt(2)
	v_pk_mul_f32 v[12:13], v[12:13], v[22:23]
	v_pk_mul_f32 v[16:17], v[16:17], v[20:21]
	s_waitcnt lgkmcnt(0)
	v_pk_add_f32 v[22:23], v[116:117], 1.0 op_sel_hi:[1,0]
	v_pk_add_f32 v[18:19], v[118:119], 1.0 op_sel_hi:[1,0]
	v_pk_fma_f32 v[22:23], v[16:17], v[22:23], v[112:113]
	v_pk_fma_f32 v[20:21], v[12:13], v[18:19], v[114:115]
	v_mul_f32_e32 v12, 0x41000000, v22
	v_mul_f32_e32 v13, 0x41000000, v23
	v_med3_f32 v12, v12, s8, v225
	v_med3_f32 v13, v13, s8, v225
	v_mov_b32_e32 v17, v3
	v_cvt_pk_fp8_f32 v17, v12, v13
	v_mul_f32_e32 v16, 0x41000000, v20
	v_mul_f32_e32 v12, 0x41000000, v21
	v_med3_f32 v13, v16, s8, v225
	v_med3_f32 v12, v12, s8, v225
	v_cvt_pk_fp8_f32 v17, v13, v12 op_sel:[0,0,1]
	v_mul_f32_e32 v15, v15, v77
	v_fmac_f32_e32 v15, v14, v76
	v_add_f32_e32 v12, v96, v15
	global_store_dword v[32:33], v17, off offset:256
	v_add_f32_e32 v96, 0, v12
	ds_read_b128 v[12:15], v109 offset:1024
	ds_read_b128 v[16:19], v109 offset:9216
	v_mov_b32_e32 v102, v8
	v_mov_b32_e32 v103, v5
	v_pk_mov_b32 v[4:5], v[8:9], v[4:5] op_sel:[1,0]
	v_mov_b32_e32 v8, v10
	v_mov_b32_e32 v9, v7
	v_pk_mul_f32 v[102:103], v[102:103], v[78:79]
	v_pk_mul_f32 v[8:9], v[8:9], v[76:77]
	v_pk_mov_b32 v[6:7], v[10:11], v[6:7] op_sel:[1,0]
	v_pk_fma_f32 v[4:5], v[4:5], v[78:79], v[102:103] op_sel:[0,1,0] op_sel_hi:[1,0,1]
	v_pk_fma_f32 v[6:7], v[6:7], v[76:77], v[8:9] op_sel:[0,1,0] op_sel_hi:[1,0,1]
	s_nop 0
	v_pk_add_f32 v[4:5], v[4:5], v[6:7]
	s_waitcnt lgkmcnt(0)
	v_pk_mov_b32 v[6:7], v[16:17], v[12:13] op_sel:[1,0]
	v_pk_add_f32 v[8:9], v[4:5], 0 op_sel_hi:[1,0]
	v_mov_b32_e32 v4, v16
	v_mov_b32_e32 v5, v13
	v_pk_mul_f32 v[4:5], v[22:23], v[4:5]
	s_nop 0
	v_pk_fma_f32 v[10:11], v[22:23], v[6:7], v[4:5] op_sel:[1,0,0] op_sel_hi:[0,1,1]
	v_mov_b32_e32 v4, v18
	v_mov_b32_e32 v5, v15
	v_pk_mul_f32 v[12:13], v[20:21], v[4:5]
	ds_read_b128 v[4:7], v109 offset:17408
	v_pk_mov_b32 v[14:15], v[18:19], v[14:15] op_sel:[1,0]
	s_waitcnt lgkmcnt(0)
	v_mul_f32_e32 v5, v23, v5
	v_pk_fma_f32 v[12:13], v[20:21], v[14:15], v[12:13] op_sel:[1,0,0] op_sel_hi:[0,1,1]
	v_pk_add_f32 v[10:11], v[10:11], v[12:13]
	v_fmac_f32_e32 v5, v22, v4
	v_pk_add_f32 v[76:77], v[8:9], v[10:11]
	ds_read_b128 v[10:13], v109 offset:25600
	v_mul_f32_e32 v4, v21, v7
	v_fmac_f32_e32 v4, v20, v6
	v_add_f32_e32 v4, v5, v4
	v_add_f32_e32 v8, v100, v4
	ds_read_b128 v[4:7], v109 offset:33792
	s_waitcnt lgkmcnt(1)
	v_mul_f32_e32 v9, v23, v11
	v_fmac_f32_e32 v9, v22, v10
	v_mul_f32_e32 v10, v21, v13
	v_fmac_f32_e32 v10, v20, v12
	v_add_f32_e32 v9, v9, v10
	ds_read_b128 v[10:13], v109 offset:41984
	s_waitcnt lgkmcnt(1)
	v_mul_f32_e32 v5, v23, v5
	v_fmac_f32_e32 v5, v22, v4
	v_mul_f32_e32 v4, v21, v7
	v_fmac_f32_e32 v4, v20, v6
	v_add_f32_e32 v4, v5, v4
	v_add_f32_e32 v98, v98, v4
	s_waitcnt lgkmcnt(0)
	v_mul_f32_e32 v4, v23, v11
	v_mul_f32_e32 v5, v21, v13
	v_fmac_f32_e32 v4, v22, v10
	v_fmac_f32_e32 v5, v20, v12
	ds_read_b128 v[14:17], v109 offset:50176
	v_add_f32_e32 v4, v4, v5
	v_add_f32_e32 v97, v97, v4
	ds_read_b128 v[4:7], v109 offset:58368
	v_add_f32_e32 v9, v99, v9
	s_waitcnt lgkmcnt(1)
	v_mul_f32_e32 v10, v23, v15
	v_mul_f32_e32 v11, v21, v17
	v_fmac_f32_e32 v10, v22, v14
	v_fmac_f32_e32 v11, v20, v16
	s_waitcnt lgkmcnt(0)
	v_mul_f32_e32 v23, v23, v5
	v_add_f32_e32 v10, v10, v11
	v_fmac_f32_e32 v23, v22, v4
	v_mul_f32_e32 v22, v21, v7
	v_add_f32_e32 v35, v35, v10
	v_fmac_f32_e32 v22, v20, v6
	ds_read_b128 v[4:7], v108 offset:2048
	ds_read_b128 v[10:13], v110 offset:26624
	ds_read_b128 v[14:17], v110 offset:51200
	v_pk_mul_f32 v[20:21], v[94:95], v[34:35] op_sel_hi:[1,0]
	v_pk_mul_f32 v[18:19], v[92:93], v[34:35] op_sel_hi:[1,0]
	s_waitcnt lgkmcnt(2)
	v_pk_mul_f32 v[4:5], v[20:21], v[4:5]
	v_pk_mul_f32 v[6:7], v[18:19], v[6:7]
	s_waitcnt lgkmcnt(0)
	v_pk_add_f32 v[14:15], v[14:15], 1.0 op_sel_hi:[1,0]
	v_pk_add_f32 v[16:17], v[16:17], 1.0 op_sel_hi:[1,0]
	v_pk_fma_f32 v[20:21], v[4:5], v[14:15], v[10:11]
	v_mov_b32_e32 v14, v3
	v_mul_f32_e32 v4, 0x41000000, v20
	v_mul_f32_e32 v5, 0x41000000, v21
	v_med3_f32 v4, v4, s8, v225
	v_med3_f32 v5, v5, s8, v225
	v_cvt_pk_fp8_f32 v14, v4, v5
	v_pk_fma_f32 v[18:19], v[6:7], v[16:17], v[12:13]
	v_add_f32_e32 v15, v23, v22
	v_mul_f32_e32 v6, 0x41000000, v18
	v_mul_f32_e32 v4, 0x41000000, v19
	v_med3_f32 v5, v6, s8, v225
	v_med3_f32 v4, v4, s8, v225
	v_cvt_pk_fp8_f32 v14, v5, v4 op_sel:[0,0,1]
	ds_read_b128 v[4:7], v109 offset:10240
	ds_read_b128 v[10:13], v109 offset:2048
	v_add_f32_e32 v92, v96, v15
	global_store_dword v[32:33], v14, off offset:512
	s_waitcnt lgkmcnt(1)
	v_mov_b32_e32 v14, v4
	s_waitcnt lgkmcnt(0)
	v_mov_b32_e32 v15, v11
	v_pk_mov_b32 v[4:5], v[4:5], v[10:11] op_sel:[1,0]
	v_mov_b32_e32 v10, v6
	v_mov_b32_e32 v11, v13
	v_pk_mul_f32 v[14:15], v[20:21], v[14:15]
	v_pk_mul_f32 v[10:11], v[18:19], v[10:11]
	v_pk_mov_b32 v[6:7], v[6:7], v[12:13] op_sel:[1,0]
	v_pk_fma_f32 v[4:5], v[20:21], v[4:5], v[14:15] op_sel:[1,0,0] op_sel_hi:[0,1,1]
	v_pk_fma_f32 v[6:7], v[18:19], v[6:7], v[10:11] op_sel:[1,0,0] op_sel_hi:[0,1,1]
	v_pk_add_f32 v[78:79], v[4:5], v[6:7]
	ds_read_b128 v[4:7], v109 offset:26624
	ds_read_b128 v[14:17], v109 offset:18432
	v_pk_add_f32 v[76:77], v[76:77], v[78:79]
	s_waitcnt lgkmcnt(1)
	v_mul_f32_e32 v5, v21, v5
	v_fmac_f32_e32 v5, v20, v4
	v_mul_f32_e32 v4, v19, v7
	s_waitcnt lgkmcnt(0)
	v_mul_f32_e32 v10, v21, v15
	v_mul_f32_e32 v11, v19, v17
	v_fmac_f32_e32 v4, v18, v6
	v_fmac_f32_e32 v10, v20, v14
	v_fmac_f32_e32 v11, v18, v16
	v_add_f32_e32 v4, v5, v4
	v_add_f32_e32 v10, v10, v11
	ds_read_b128 v[14:17], v109 offset:34816
	v_add_f32_e32 v11, v9, v4
	ds_read_b128 v[4:7], v109 offset:43008
	v_add_f32_e32 v12, v8, v10
	s_waitcnt lgkmcnt(1)
	v_mul_f32_e32 v8, v21, v15
	v_mul_f32_e32 v9, v19, v17
	s_waitcnt lgkmcnt(0)
	v_mul_f32_e32 v5, v21, v5
	v_fmac_f32_e32 v8, v20, v14
	v_fmac_f32_e32 v9, v18, v16
	v_fmac_f32_e32 v5, v20, v4
	ds_read_b128 v[14:17], v109 offset:51200
	v_mul_f32_e32 v4, v19, v7
	v_fmac_f32_e32 v4, v18, v6
	v_add_f32_e32 v4, v5, v4
	v_add_f32_e32 v8, v8, v9
	v_add_f32_e32 v9, v97, v4
	ds_read_b128 v[4:7], v109 offset:59392
	v_add_f32_e32 v10, v98, v8
	s_waitcnt lgkmcnt(1)
	v_mul_f32_e32 v8, v21, v15
	v_mul_f32_e32 v13, v19, v17
	v_fmac_f32_e32 v8, v20, v14
	v_fmac_f32_e32 v13, v18, v16
	v_add_f32_e32 v8, v8, v13
	v_add_f32_e32 v8, v35, v8
	s_waitcnt lgkmcnt(0)
	v_mul_f32_e32 v13, v21, v5
	v_mul_f32_e32 v35, v19, v7
	v_fmac_f32_e32 v13, v20, v4
	v_fmac_f32_e32 v35, v18, v6
	ds_read_b128 v[4:7], v108 offset:3072
	ds_read_b128 v[14:17], v110 offset:27648
	ds_read_b128 v[18:21], v110 offset:52224
	v_pk_mul_f32 v[22:23], v[88:89], v[34:35] op_sel_hi:[1,0]
	v_pk_mul_f32 v[88:89], v[90:91], v[34:35] op_sel_hi:[1,0]
	v_add_f32_e32 v13, v13, v35
	s_waitcnt lgkmcnt(2)
	v_pk_mul_f32 v[88:89], v[88:89], v[4:5]
	v_pk_mul_f32 v[4:5], v[22:23], v[6:7]
	s_waitcnt lgkmcnt(0)
	v_pk_add_f32 v[6:7], v[20:21], 1.0 op_sel_hi:[1,0]
	v_pk_add_f32 v[18:19], v[18:19], 1.0 op_sel_hi:[1,0]
	v_pk_fma_f32 v[4:5], v[4:5], v[6:7], v[16:17]
	v_pk_fma_f32 v[6:7], v[88:89], v[18:19], v[14:15]
	v_mov_b32_e32 v22, v3
	v_mul_f32_e32 v14, 0x41000000, v6
	v_mul_f32_e32 v15, 0x41000000, v7
	v_med3_f32 v14, v14, s8, v225
	v_med3_f32 v15, v15, s8, v225
	v_cvt_pk_fp8_f32 v22, v14, v15
	v_mul_f32_e32 v16, 0x41000000, v4
	v_mul_f32_e32 v14, 0x41000000, v5
	v_med3_f32 v15, v16, s8, v225
	v_med3_f32 v14, v14, s8, v225
	v_cvt_pk_fp8_f32 v22, v15, v14 op_sel:[0,0,1]
	ds_read_b128 v[14:17], v109 offset:11264
	ds_read_b128 v[18:21], v109 offset:3072
	v_add_f32_e32 v13, v92, v13
	ds_read_b128 v[92:95], v109 offset:19456
	global_store_dword v[32:33], v22, off offset:768
	s_waitcnt lgkmcnt(2)
	v_mov_b32_e32 v22, v14
	s_waitcnt lgkmcnt(1)
	v_mov_b32_e32 v23, v19
	v_pk_mul_f32 v[22:23], v[6:7], v[22:23]
	v_pk_mov_b32 v[14:15], v[14:15], v[18:19] op_sel:[1,0]
	s_waitcnt lgkmcnt(0)
	v_mul_f32_e32 v18, v7, v93
	v_pk_fma_f32 v[88:89], v[6:7], v[14:15], v[22:23] op_sel:[1,0,0] op_sel_hi:[0,1,1]
	v_mov_b32_e32 v14, v16
	v_mov_b32_e32 v15, v21
	v_pk_mul_f32 v[14:15], v[4:5], v[14:15]
	v_pk_mov_b32 v[16:17], v[16:17], v[20:21] op_sel:[1,0]
	v_mul_f32_e32 v19, v5, v95
	v_pk_fma_f32 v[90:91], v[4:5], v[16:17], v[14:15] op_sel:[1,0,0] op_sel_hi:[0,1,1]
	ds_read_b128 v[14:17], v109 offset:27648
	v_fmac_f32_e32 v18, v6, v92
	v_fmac_f32_e32 v19, v4, v94
	v_add_f32_e32 v18, v18, v19
	v_add_f32_e32 v22, v12, v18
	s_waitcnt lgkmcnt(0)
	v_mul_f32_e32 v12, v7, v15
	ds_read_b128 v[18:21], v109 offset:35840
	v_fmac_f32_e32 v12, v6, v14
	v_mul_f32_e32 v14, v5, v17
	v_fmac_f32_e32 v14, v4, v16
	v_add_f32_e32 v12, v12, v14
	ds_read_b128 v[14:17], v109 offset:44032
	v_add_f32_e32 v23, v11, v12
	s_waitcnt lgkmcnt(1)
	v_mul_f32_e32 v11, v7, v19
	v_mul_f32_e32 v12, v5, v21
	v_fmac_f32_e32 v11, v6, v18
	v_fmac_f32_e32 v12, v4, v20
	v_add_f32_e32 v11, v11, v12
	ds_read_b128 v[18:21], v109 offset:52224
	v_add_f32_e32 v97, v10, v11
	s_waitcnt lgkmcnt(1)
	v_mul_f32_e32 v10, v7, v15
	v_mul_f32_e32 v11, v5, v17
	v_fmac_f32_e32 v10, v6, v14
	v_fmac_f32_e32 v11, v4, v16
	ds_read_b128 v[14:17], v109 offset:60416
	v_add_f32_e32 v10, v10, v11
	v_add_f32_e32 v98, v9, v10
	s_waitcnt lgkmcnt(1)
	v_mul_f32_e32 v9, v7, v19
	v_mul_f32_e32 v10, v5, v21
	v_fmac_f32_e32 v9, v6, v18
	v_fmac_f32_e32 v10, v4, v20
	v_add_f32_e32 v9, v9, v10
	s_waitcnt lgkmcnt(0)
	v_mul_f32_e32 v12, v7, v15
	v_mul_f32_e32 v35, v5, v17
	v_add_f32_e32 v99, v8, v9
	v_fmac_f32_e32 v12, v6, v14
	v_fmac_f32_e32 v35, v4, v16
	ds_read_b128 v[4:7], v108 offset:4096
	ds_read_b128 v[8:11], v110 offset:28672
	ds_read_b128 v[14:17], v110 offset:53248
	v_pk_mul_f32 v[20:21], v[86:87], v[34:35] op_sel_hi:[1,0]
	v_pk_mul_f32 v[18:19], v[84:85], v[34:35] op_sel_hi:[1,0]
	s_waitcnt lgkmcnt(2)
	v_pk_mul_f32 v[4:5], v[20:21], v[4:5]
	v_pk_mul_f32 v[6:7], v[18:19], v[6:7]
	s_waitcnt lgkmcnt(0)
	v_pk_add_f32 v[14:15], v[14:15], 1.0 op_sel_hi:[1,0]
	v_pk_add_f32 v[16:17], v[16:17], 1.0 op_sel_hi:[1,0]
	v_pk_fma_f32 v[86:87], v[4:5], v[14:15], v[8:9]
	v_mov_b32_e32 v14, v3
	v_mul_f32_e32 v4, 0x41000000, v86
	v_mul_f32_e32 v5, 0x41000000, v87
	v_med3_f32 v4, v4, s8, v225
	v_med3_f32 v5, v5, s8, v225
	v_cvt_pk_fp8_f32 v14, v4, v5
	v_pk_fma_f32 v[84:85], v[6:7], v[16:17], v[10:11]
	v_add_f32_e32 v12, v12, v35
	v_mul_f32_e32 v6, 0x41000000, v84
	v_mul_f32_e32 v4, 0x41000000, v85
	v_med3_f32 v5, v6, s8, v225
	v_med3_f32 v4, v4, s8, v225
	v_cvt_pk_fp8_f32 v14, v5, v4 op_sel:[0,0,1]
	ds_read_b128 v[4:7], v109 offset:12288
	ds_read_b128 v[8:11], v109 offset:4096
	v_add_f32_e32 v102, v13, v12
	v_pk_add_f32 v[78:79], v[88:89], v[90:91]
	global_store_dword v[32:33], v14, off offset:1024
	ds_read_b128 v[12:15], v109 offset:20480
	s_waitcnt lgkmcnt(2)
	v_mov_b32_e32 v16, v4
	s_waitcnt lgkmcnt(1)
	v_mov_b32_e32 v17, v9
	v_pk_mul_f32 v[92:93], v[86:87], v[16:17]
	v_mov_b32_e32 v16, v6
	v_mov_b32_e32 v17, v11
	v_pk_mul_f32 v[94:95], v[84:85], v[16:17]
	ds_read_b128 v[16:19], v109 offset:28672
	s_waitcnt lgkmcnt(1)
	v_mul_f32_e32 v13, v87, v13
	v_fmac_f32_e32 v13, v86, v12
	v_mul_f32_e32 v12, v85, v15
	v_fmac_f32_e32 v12, v84, v14
	v_add_f32_e32 v12, v13, v12
	s_waitcnt lgkmcnt(0)
	v_mul_f32_e32 v17, v87, v17
	v_add_f32_e32 v96, v22, v12
	v_fmac_f32_e32 v17, v86, v16
	ds_read_b128 v[12:15], v109 offset:36864
	v_mul_f32_e32 v16, v85, v19
	v_fmac_f32_e32 v16, v84, v18
	v_add_f32_e32 v16, v17, v16
	v_add_f32_e32 v35, v23, v16
	ds_read_b128 v[16:19], v109 offset:45056
	s_waitcnt lgkmcnt(1)
	v_mul_f32_e32 v13, v87, v13
	v_fmac_f32_e32 v13, v86, v12
	v_mul_f32_e32 v12, v85, v15
	v_fmac_f32_e32 v12, v84, v14
	v_add_f32_e32 v12, v13, v12
	s_waitcnt lgkmcnt(0)
	v_mul_f32_e32 v17, v87, v17
	v_add_f32_e32 v22, v97, v12
	v_fmac_f32_e32 v17, v86, v16
	ds_read_b128 v[12:15], v109 offset:53248
	v_mul_f32_e32 v16, v85, v19
	v_fmac_f32_e32 v16, v84, v18
	v_add_f32_e32 v16, v17, v16
	v_add_f32_e32 v21, v98, v16
	ds_read_b128 v[16:19], v109 offset:61440
	s_waitcnt lgkmcnt(1)
	v_mul_f32_e32 v13, v87, v13
	v_fmac_f32_e32 v13, v86, v12
	v_mul_f32_e32 v12, v85, v15
	v_fmac_f32_e32 v12, v84, v14
	v_add_f32_e32 v12, v13, v12
	s_waitcnt lgkmcnt(0)
	v_mul_f32_e32 v23, v87, v17
	v_mul_f32_e32 v97, v85, v19
	v_add_f32_e32 v20, v99, v12
	v_fmac_f32_e32 v23, v86, v16
	v_fmac_f32_e32 v97, v84, v18
	ds_read_b128 v[12:15], v108 offset:5120
	ds_read_b128 v[16:19], v110 offset:29696
	ds_read_b128 v[98:101], v110 offset:54272
	v_pk_mul_f32 v[82:83], v[82:83], v[34:35] op_sel_hi:[1,0]
	v_pk_mul_f32 v[80:81], v[80:81], v[34:35] op_sel_hi:[1,0]
	s_waitcnt lgkmcnt(2)
	v_pk_mul_f32 v[12:13], v[82:83], v[12:13]
	v_pk_mul_f32 v[14:15], v[80:81], v[14:15]
	s_waitcnt lgkmcnt(0)
	v_pk_add_f32 v[82:83], v[98:99], 1.0 op_sel_hi:[1,0]
	v_pk_add_f32 v[80:81], v[100:101], 1.0 op_sel_hi:[1,0]
	v_pk_fma_f32 v[82:83], v[12:13], v[82:83], v[16:17]
	v_pk_fma_f32 v[80:81], v[14:15], v[80:81], v[18:19]
	v_mul_f32_e32 v12, 0x41000000, v82
	v_mul_f32_e32 v13, 0x41000000, v83
	v_med3_f32 v12, v12, s8, v225
	v_med3_f32 v13, v13, s8, v225
	v_mov_b32_e32 v15, v3
	v_cvt_pk_fp8_f32 v15, v12, v13
	v_mul_f32_e32 v14, 0x41000000, v80
	v_mul_f32_e32 v12, 0x41000000, v81
	v_med3_f32 v13, v14, s8, v225
	v_med3_f32 v12, v12, s8, v225
	v_cvt_pk_fp8_f32 v15, v13, v12 op_sel:[0,0,1]
	ds_read_b128 v[98:101], v109 offset:21504
	v_add_f32_e32 v12, v23, v97
	v_add_f32_e32 v23, v102, v12
	global_store_dword v[32:33], v15, off offset:1280
	ds_read_b128 v[12:15], v109 offset:5120
	ds_read_b128 v[16:19], v109 offset:13312
	s_waitcnt lgkmcnt(2)
	v_mul_f32_e32 v97, v83, v99
	ds_read_b128 v[112:115], v109 offset:29696
	v_fmac_f32_e32 v97, v82, v98
	v_mul_f32_e32 v98, v81, v101
	v_fmac_f32_e32 v98, v80, v100
	v_add_f32_e32 v97, v97, v98
	v_add_f32_e32 v111, v96, v97
	ds_read_b128 v[96:99], v109 offset:37888
	s_waitcnt lgkmcnt(1)
	v_mul_f32_e32 v100, v83, v113
	v_mul_f32_e32 v101, v81, v115
	v_fmac_f32_e32 v100, v82, v112
	v_fmac_f32_e32 v101, v80, v114
	v_add_f32_e32 v100, v100, v101
	v_add_f32_e32 v35, v35, v100
	ds_read_b128 v[100:103], v109 offset:46080
	s_waitcnt lgkmcnt(1)
	v_mul_f32_e32 v97, v83, v97
	v_fmac_f32_e32 v97, v82, v96
	v_mul_f32_e32 v96, v81, v99
	v_fmac_f32_e32 v96, v80, v98
	v_add_f32_e32 v96, v97, v96
	v_add_f32_e32 v116, v22, v96
	s_waitcnt lgkmcnt(0)
	v_mul_f32_e32 v22, v83, v101
	v_fmac_f32_e32 v22, v82, v100
	ds_read_b128 v[96:99], v109 offset:54272
	v_mul_f32_e32 v100, v81, v103
	v_fmac_f32_e32 v100, v80, v102
	v_add_f32_e32 v22, v22, v100
	ds_read_b128 v[100:103], v109 offset:62464
	v_add_f32_e32 v117, v21, v22
	s_waitcnt lgkmcnt(1)
	v_mul_f32_e32 v21, v83, v97
	v_mul_f32_e32 v22, v81, v99
	v_fmac_f32_e32 v21, v82, v96
	v_fmac_f32_e32 v22, v80, v98
	v_add_f32_e32 v21, v21, v22
	s_waitcnt lgkmcnt(0)
	v_mul_f32_e32 v22, v83, v101
	v_mul_f32_e32 v118, v81, v103
	v_fmac_f32_e32 v22, v82, v100
	v_fmac_f32_e32 v118, v80, v102
	ds_read_b128 v[96:99], v108 offset:6144
	ds_read_b128 v[100:103], v110 offset:30720
	ds_read_b128 v[112:115], v110 offset:55296
	v_add_f32_e32 v122, v20, v21
	v_pk_mul_f32 v[20:21], v[24:25], v[34:35] op_sel_hi:[1,0]
	v_pk_mul_f32 v[24:25], v[26:27], v[34:35] op_sel_hi:[1,0]
	s_waitcnt lgkmcnt(2)
	v_pk_mul_f32 v[20:21], v[20:21], v[98:99]
	v_pk_mul_f32 v[24:25], v[24:25], v[96:97]
	s_waitcnt lgkmcnt(0)
	v_pk_add_f32 v[98:99], v[112:113], 1.0 op_sel_hi:[1,0]
	v_pk_add_f32 v[26:27], v[114:115], 1.0 op_sel_hi:[1,0]
	v_pk_fma_f32 v[98:99], v[24:25], v[98:99], v[100:101]
	v_pk_fma_f32 v[96:97], v[20:21], v[26:27], v[102:103]
	v_mul_f32_e32 v20, 0x41000000, v98
	v_mul_f32_e32 v21, 0x41000000, v99
	v_med3_f32 v20, v20, s8, v225
	v_med3_f32 v21, v21, s8, v225
	v_mov_b32_e32 v25, v3
	v_cvt_pk_fp8_f32 v25, v20, v21
	v_mul_f32_e32 v24, 0x41000000, v96
	v_mul_f32_e32 v20, 0x41000000, v97
	v_med3_f32 v21, v24, s8, v225
	v_med3_f32 v20, v20, s8, v225
	v_cvt_pk_fp8_f32 v25, v21, v20 op_sel:[0,0,1]
	ds_read_b128 v[100:103], v109 offset:22528
	v_add_f32_e32 v20, v22, v118
	v_add_f32_e32 v126, v23, v20
	global_store_dword v[32:33], v25, off offset:1536
	ds_read_b128 v[20:23], v109 offset:6144
	ds_read_b128 v[24:27], v109 offset:14336
	s_waitcnt lgkmcnt(2)
	v_mul_f32_e32 v101, v99, v101
	ds_read_b128 v[112:115], v109 offset:30720
	v_fmac_f32_e32 v101, v98, v100
	v_mul_f32_e32 v100, v97, v103
	v_fmac_f32_e32 v100, v96, v102
	v_add_f32_e32 v100, v101, v100
	v_add_f32_e32 v127, v111, v100
	ds_read_b128 v[100:103], v109 offset:38912
	s_waitcnt lgkmcnt(1)
	v_mul_f32_e32 v111, v99, v113
	v_fmac_f32_e32 v111, v98, v112
	v_mul_f32_e32 v112, v97, v115
	v_fmac_f32_e32 v112, v96, v114
	v_add_f32_e32 v111, v111, v112
	v_add_f32_e32 v115, v35, v111
	s_waitcnt lgkmcnt(0)
	v_mul_f32_e32 v35, v99, v101
	ds_read_b128 v[118:121], v109 offset:47104
	v_fmac_f32_e32 v35, v98, v100
	v_mul_f32_e32 v100, v97, v103
	v_fmac_f32_e32 v100, v96, v102
	v_add_f32_e32 v35, v35, v100
	ds_read_b128 v[100:103], v109 offset:55296
	v_add_f32_e32 v116, v116, v35
	s_waitcnt lgkmcnt(1)
	v_mul_f32_e32 v35, v99, v119
	v_mul_f32_e32 v111, v97, v121
	v_fmac_f32_e32 v35, v98, v118
	v_fmac_f32_e32 v111, v96, v120
	ds_read_b128 v[118:121], v109 offset:63488
	v_add_f32_e32 v35, v35, v111
	v_add_f32_e32 v113, v117, v35
	s_waitcnt lgkmcnt(1)
	v_mul_f32_e32 v35, v99, v101
	v_fmac_f32_e32 v35, v98, v100
	v_mul_f32_e32 v100, v97, v103
	v_fmac_f32_e32 v100, v96, v102
	v_add_f32_e32 v35, v35, v100
	s_waitcnt lgkmcnt(0)
	v_mul_f32_e32 v112, v99, v119
	v_mul_f32_e32 v114, v97, v121
	v_add_f32_e32 v111, v122, v35
	v_fmac_f32_e32 v112, v98, v118
	v_fmac_f32_e32 v114, v96, v120
	ds_read_b128 v[100:103], v108 offset:7168
	ds_read_b128 v[118:121], v110 offset:31744
	ds_read_b128 v[122:125], v110 offset:56320
	v_pk_mul_f32 v[28:29], v[28:29], v[34:35] op_sel_hi:[1,0]
	v_pk_mul_f32 v[30:31], v[30:31], v[34:35] op_sel_hi:[1,0]
	s_waitcnt lgkmcnt(2)
	v_pk_mul_f32 v[28:29], v[28:29], v[102:103]
	v_pk_mul_f32 v[30:31], v[30:31], v[100:101]
	s_waitcnt lgkmcnt(0)
	v_pk_add_f32 v[102:103], v[122:123], 1.0 op_sel_hi:[1,0]
	v_pk_add_f32 v[34:35], v[124:125], 1.0 op_sel_hi:[1,0]
	v_pk_fma_f32 v[102:103], v[30:31], v[102:103], v[118:119]
	v_pk_fma_f32 v[100:101], v[28:29], v[34:35], v[120:121]
	v_mul_f32_e32 v28, 0x41000000, v102
	v_mul_f32_e32 v29, 0x41000000, v103
	v_med3_f32 v28, v28, s8, v225
	v_med3_f32 v29, v29, s8, v225
	v_mov_b32_e32 v31, v3
	v_cvt_pk_fp8_f32 v31, v28, v29
	v_mul_f32_e32 v30, 0x41000000, v100
	v_mul_f32_e32 v28, 0x41000000, v101
	v_med3_f32 v29, v30, s8, v225
	v_med3_f32 v28, v28, s8, v225
	v_cvt_pk_fp8_f32 v31, v29, v28 op_sel:[0,0,1]
	ds_read_b128 v[118:121], v109 offset:23552
	v_add_f32_e32 v28, v112, v114
	v_add_f32_e32 v114, v126, v28
	global_store_dword v[32:33], v31, off offset:1792
	ds_read_b128 v[28:31], v109 offset:7168
	ds_read_b128 v[32:35], v109 offset:15360
	ds_read_b128 v[122:125], v109 offset:31744
	s_waitcnt lgkmcnt(3)
	v_mul_f32_e32 v110, v103, v119
	v_mul_f32_e32 v112, v101, v121
	v_fmac_f32_e32 v110, v102, v118
	v_fmac_f32_e32 v112, v100, v120
	ds_read_b128 v[118:121], v109 offset:39936
	v_add_f32_e32 v110, v110, v112
	v_pk_mov_b32 v[4:5], v[4:5], v[8:9] op_sel:[1,0]
	v_pk_mov_b32 v[6:7], v[6:7], v[10:11] op_sel:[1,0]
	v_add_f32_e32 v112, v127, v110
	s_waitcnt lgkmcnt(1)
	v_mul_f32_e32 v110, v103, v123
	v_mul_f32_e32 v117, v101, v125
	v_pk_fma_f32 v[4:5], v[86:87], v[4:5], v[92:93] op_sel:[1,0,0] op_sel_hi:[0,1,1]
	v_pk_fma_f32 v[6:7], v[84:85], v[6:7], v[94:95] op_sel:[1,0,0] op_sel_hi:[0,1,1]
	v_fmac_f32_e32 v110, v102, v122
	v_fmac_f32_e32 v117, v100, v124
	v_pk_add_f32 v[4:5], v[4:5], v[6:7]
	v_mov_b32_e32 v6, v16
	v_mov_b32_e32 v7, v13
	v_add_f32_e32 v110, v110, v117
	ds_read_b128 v[122:125], v109 offset:48128
	v_pk_mul_f32 v[6:7], v[82:83], v[6:7]
	v_pk_mov_b32 v[8:9], v[16:17], v[12:13] op_sel:[1,0]
	v_add_f32_e32 v115, v115, v110
	s_waitcnt lgkmcnt(1)
	v_mul_f32_e32 v110, v103, v119
	v_mul_f32_e32 v117, v101, v121
	v_pk_fma_f32 v[6:7], v[82:83], v[8:9], v[6:7] op_sel:[1,0,0] op_sel_hi:[0,1,1]
	v_mov_b32_e32 v8, v18
	v_mov_b32_e32 v9, v15
	v_fmac_f32_e32 v110, v102, v118
	v_fmac_f32_e32 v117, v100, v120
	v_pk_mul_f32 v[8:9], v[80:81], v[8:9]
	v_pk_mov_b32 v[10:11], v[18:19], v[14:15] op_sel:[1,0]
	v_add_f32_e32 v110, v110, v117
	v_pk_add_f32 v[76:77], v[76:77], v[78:79]
	v_pk_fma_f32 v[8:9], v[80:81], v[10:11], v[8:9] op_sel:[1,0,0] op_sel_hi:[0,1,1]
	v_add_f32_e32 v110, v116, v110
	ds_read_b128 v[116:119], v109 offset:56320
	v_pk_add_f32 v[4:5], v[76:77], v[4:5]
	v_pk_add_f32 v[6:7], v[6:7], v[8:9]
	s_waitcnt lgkmcnt(1)
	v_mul_f32_e32 v120, v103, v123
	v_mul_f32_e32 v121, v101, v125
	v_pk_add_f32 v[4:5], v[4:5], v[6:7]
	v_mov_b32_e32 v6, v24
	v_mov_b32_e32 v7, v21
	v_fmac_f32_e32 v120, v102, v122
	v_fmac_f32_e32 v121, v100, v124
	v_pk_mul_f32 v[6:7], v[98:99], v[6:7]
	v_pk_mov_b32 v[8:9], v[24:25], v[20:21] op_sel:[1,0]
	v_add_f32_e32 v120, v120, v121
	v_pk_fma_f32 v[6:7], v[98:99], v[8:9], v[6:7] op_sel:[1,0,0] op_sel_hi:[0,1,1]
	v_mov_b32_e32 v8, v26
	v_mov_b32_e32 v9, v23
	v_add_f32_e32 v113, v113, v120
	ds_read_b128 v[120:123], v109 offset:64512
	v_pk_mul_f32 v[8:9], v[96:97], v[8:9]
	v_pk_mov_b32 v[10:11], v[26:27], v[22:23] op_sel:[1,0]
	s_waitcnt lgkmcnt(1)
	v_mul_f32_e32 v117, v103, v117
	v_pk_fma_f32 v[8:9], v[96:97], v[10:11], v[8:9] op_sel:[1,0,0] op_sel_hi:[0,1,1]
	v_fmac_f32_e32 v117, v102, v116
	v_mul_f32_e32 v116, v101, v119
	v_pk_add_f32 v[6:7], v[6:7], v[8:9]
	v_fmac_f32_e32 v116, v100, v118
	v_pk_add_f32 v[4:5], v[4:5], v[6:7]
	v_mov_b32_e32 v6, v32
	v_mov_b32_e32 v7, v29
	v_add_f32_e32 v116, v117, v116
	v_pk_mul_f32 v[6:7], v[102:103], v[6:7]
	v_pk_mov_b32 v[8:9], v[32:33], v[28:29] op_sel:[1,0]
	v_add_f32_e32 v111, v111, v116
	s_waitcnt lgkmcnt(0)
	v_mul_f32_e32 v116, v103, v121
	v_mul_f32_e32 v117, v101, v123
	v_pk_fma_f32 v[6:7], v[102:103], v[8:9], v[6:7] op_sel:[1,0,0] op_sel_hi:[0,1,1]
	v_mov_b32_e32 v8, v34
	v_mov_b32_e32 v9, v31
	v_fmac_f32_e32 v116, v102, v120
	v_fmac_f32_e32 v117, v100, v122
	v_mov_b32_e32 v118, v222
	v_mov_b32_e32 v119, v222
	v_mov_b32_e32 v120, v222
	v_mov_b32_e32 v121, v222
	v_mov_b32_e32 v122, v222
	v_mov_b32_e32 v123, v222
	v_mov_b32_e32 v124, v222
	v_pk_mul_f32 v[8:9], v[100:101], v[8:9]
	v_pk_mov_b32 v[10:11], v[34:35], v[30:31] op_sel:[1,0]
	s_nop 0
	v_pk_fma_f32 v[8:9], v[100:101], v[10:11], v[8:9] op_sel:[1,0,0] op_sel_hi:[0,1,1]
	v_lshlrev_b32_e32 v118, 2, v118
	v_lshlrev_b32_e32 v124, 2, v124
	v_pk_add_f32 v[6:7], v[6:7], v[8:9]
	v_xor_b32_e32 v118, 4, v118
	v_xor_b32_e32 v124, 4, v124
	v_pk_add_f32 v[4:5], v[4:5], v[6:7]
	ds_bpermute_b32 v7, v118, v5
	ds_bpermute_b32 v6, v124, v4
	v_mov_b32_e32 v8, v222
	v_lshlrev_b32_e32 v119, 2, v119
	v_lshlrev_b32_e32 v8, 2, v8
	v_xor_b32_e32 v119, 8, v119
	v_xor_b32_e32 v8, 8, v8
	s_waitcnt lgkmcnt(0)
	v_pk_add_f32 v[4:5], v[4:5], v[6:7]
	ds_bpermute_b32 v7, v119, v5
	ds_bpermute_b32 v6, v8, v4
	v_mov_b32_e32 v8, v222
	v_lshlrev_b32_e32 v120, 2, v120
	v_lshlrev_b32_e32 v8, 2, v8
	v_xor_b32_e32 v120, 16, v120
	v_xor_b32_e32 v8, 16, v8
	s_waitcnt lgkmcnt(0)
	v_pk_add_f32 v[4:5], v[4:5], v[6:7]
	ds_bpermute_b32 v7, v120, v5
	ds_bpermute_b32 v6, v8, v4
	v_mov_b32_e32 v8, v222
	v_lshlrev_b32_e32 v121, 2, v121
	v_lshlrev_b32_e32 v8, 2, v8
	v_xor_b32_e32 v121, 32, v121
	v_xor_b32_e32 v8, 32, v8
	s_waitcnt lgkmcnt(0)
	v_pk_add_f32 v[4:5], v[4:5], v[6:7]
	ds_bpermute_b32 v7, v121, v5
	ds_bpermute_b32 v6, v8, v4
	v_mov_b32_e32 v8, v222
	v_lshlrev_b32_e32 v122, 2, v122
	v_lshlrev_b32_e32 v8, 2, v8
	v_xor_b32_e32 v122, 64, v122
	v_xor_b32_e32 v8, 64, v8
	s_waitcnt lgkmcnt(0)
	v_pk_add_f32 v[4:5], v[4:5], v[6:7]
	ds_bpermute_b32 v7, v122, v5
	ds_bpermute_b32 v6, v8, v4
	v_add_f32_e32 v8, v116, v117
	v_add_f32_e32 v16, v114, v8
	v_lshlrev_b32_e32 v8, 2, v123
	v_xor_b32_e32 v8, 0x80, v8
	s_waitcnt lgkmcnt(0)
	v_pk_add_f32 v[4:5], v[4:5], v[6:7]
	ds_bpermute_b32 v7, v8, v5
	v_mov_b32_e32 v6, v222
	v_mov_b32_e32 v8, v222
	v_mov_b32_e32 v9, v222
	v_mov_b32_e32 v10, v222
	v_mov_b32_e32 v11, v222
	v_mov_b32_e32 v12, v222
	v_mov_b32_e32 v13, v222
	v_mov_b32_e32 v14, v222
	v_lshlrev_b32_e32 v8, 2, v8
	v_xor_b32_e32 v8, 4, v8
	v_lshlrev_b32_e32 v14, 2, v14
	ds_bpermute_b32 v8, v8, v112
	v_xor_b32_e32 v14, 4, v14
	ds_bpermute_b32 v14, v14, v115
	v_mov_b32_e32 v15, v222
	v_lshlrev_b32_e32 v9, 2, v9
	s_waitcnt lgkmcnt(1)
	v_add_f32_e32 v8, v112, v8
	v_xor_b32_e32 v9, 8, v9
	v_lshlrev_b32_e32 v15, 2, v15
	ds_bpermute_b32 v9, v9, v8
	s_waitcnt lgkmcnt(1)
	v_add_f32_e32 v14, v115, v14
	v_xor_b32_e32 v15, 8, v15
	ds_bpermute_b32 v15, v15, v14
	v_mov_b32_e32 v17, v222
	s_waitcnt lgkmcnt(1)
	v_add_f32_e32 v8, v8, v9
	v_lshlrev_b32_e32 v9, 2, v10
	v_xor_b32_e32 v9, 16, v9
	s_waitcnt lgkmcnt(0)
	v_add_f32_e32 v10, v14, v15
	v_mov_b32_e32 v14, v222
	ds_bpermute_b32 v9, v9, v8
	v_mov_b32_e32 v15, v222
	v_lshlrev_b32_e32 v14, 2, v14
	v_xor_b32_e32 v14, 16, v14
	ds_bpermute_b32 v14, v14, v10
	s_waitcnt lgkmcnt(1)
	v_add_f32_e32 v8, v8, v9
	v_lshlrev_b32_e32 v9, 2, v11
	v_mov_b32_e32 v11, v222
	s_waitcnt lgkmcnt(0)
	v_add_f32_e32 v10, v10, v14
	v_lshlrev_b32_e32 v11, 2, v11
	v_xor_b32_e32 v11, 32, v11
	ds_bpermute_b32 v11, v11, v10
	v_xor_b32_e32 v9, 32, v9
	ds_bpermute_b32 v9, v9, v8
	v_mov_b32_e32 v14, v222
	v_mov_b32_e32 v18, v222
	s_waitcnt lgkmcnt(1)
	v_add_f32_e32 v10, v10, v11
	v_mov_b32_e32 v11, v222
	s_waitcnt lgkmcnt(0)
	v_add_f32_e32 v8, v8, v9
	v_lshlrev_b32_e32 v11, 2, v11
	v_lshlrev_b32_e32 v9, 2, v12
	v_xor_b32_e32 v11, 64, v11
	v_xor_b32_e32 v9, 64, v9
	ds_bpermute_b32 v11, v11, v10
	ds_bpermute_b32 v9, v9, v8
	v_mov_b32_e32 v12, v222
	v_mov_b32_e32 v19, v222
	v_mov_b32_e32 v20, v222
	s_waitcnt lgkmcnt(1)
	v_add_f32_e32 v10, v10, v11
	v_mov_b32_e32 v11, v222
	s_waitcnt lgkmcnt(0)
	v_add_f32_e32 v8, v8, v9
	v_lshlrev_b32_e32 v9, 2, v13
	v_mov_b32_e32 v13, v222
	v_lshlrev_b32_e32 v12, 2, v12
	v_xor_b32_e32 v12, 4, v12
	v_lshlrev_b32_e32 v19, 2, v19
	ds_bpermute_b32 v12, v12, v110
	v_xor_b32_e32 v19, 4, v19
	ds_bpermute_b32 v19, v19, v113
	v_lshlrev_b32_e32 v13, 2, v13
	s_waitcnt lgkmcnt(1)
	v_add_f32_e32 v12, v110, v12
	v_xor_b32_e32 v13, 8, v13
	v_lshlrev_b32_e32 v20, 2, v20
	ds_bpermute_b32 v13, v13, v12
	s_waitcnt lgkmcnt(1)
	v_add_f32_e32 v19, v113, v19
	v_xor_b32_e32 v20, 8, v20
	ds_bpermute_b32 v20, v20, v19
	v_mov_b32_e32 v21, v222
	s_waitcnt lgkmcnt(1)
	v_add_f32_e32 v12, v12, v13
	v_lshlrev_b32_e32 v13, 2, v14
	v_xor_b32_e32 v13, 16, v13
	s_waitcnt lgkmcnt(0)
	v_add_f32_e32 v14, v19, v20
	v_mov_b32_e32 v19, v222
	ds_bpermute_b32 v13, v13, v12
	v_mov_b32_e32 v20, v222
	v_lshlrev_b32_e32 v19, 2, v19
	v_xor_b32_e32 v19, 16, v19
	ds_bpermute_b32 v19, v19, v14
	s_waitcnt lgkmcnt(1)
	v_add_f32_e32 v12, v12, v13
	v_lshlrev_b32_e32 v13, 2, v15
	v_mov_b32_e32 v15, v222
	s_waitcnt lgkmcnt(0)
	v_add_f32_e32 v14, v14, v19
	v_lshlrev_b32_e32 v15, 2, v15
	v_xor_b32_e32 v15, 32, v15
	ds_bpermute_b32 v15, v15, v14
	v_xor_b32_e32 v13, 32, v13
	ds_bpermute_b32 v13, v13, v12
	v_mov_b32_e32 v19, v222
	v_mov_b32_e32 v22, v222
	s_waitcnt lgkmcnt(1)
	v_add_f32_e32 v14, v14, v15
	v_mov_b32_e32 v15, v222
	s_waitcnt lgkmcnt(0)
	v_add_f32_e32 v12, v12, v13
	v_lshlrev_b32_e32 v13, 2, v17
	v_lshlrev_b32_e32 v15, 2, v15
	v_xor_b32_e32 v13, 64, v13
	v_xor_b32_e32 v15, 64, v15
	ds_bpermute_b32 v13, v13, v12
	ds_bpermute_b32 v15, v15, v14
	v_mov_b32_e32 v17, v222
	v_mov_b32_e32 v23, v222
	v_lshlrev_b32_e32 v6, 2, v6
	s_waitcnt lgkmcnt(1)
	v_add_f32_e32 v12, v12, v13
	v_lshlrev_b32_e32 v13, 2, v18
	s_waitcnt lgkmcnt(0)
	v_add_f32_e32 v14, v14, v15
	v_mov_b32_e32 v15, v222
	v_mov_b32_e32 v18, v222
	s_nop 0
	v_lshlrev_b32_e32 v17, 2, v17
	v_lshlrev_b32_e32 v23, 2, v23
	v_xor_b32_e32 v17, 4, v17
	v_xor_b32_e32 v23, 4, v23
	ds_bpermute_b32 v17, v17, v111
	ds_bpermute_b32 v23, v23, v16
	v_lshlrev_b32_e32 v18, 2, v18
	v_xor_b32_e32 v18, 8, v18
	v_lshlrev_b32_e32 v11, 2, v11
	s_waitcnt lgkmcnt(1)
	v_add_f32_e32 v17, v111, v17
	s_waitcnt lgkmcnt(0)
	v_add_f32_e32 v16, v16, v23
	v_mov_b32_e32 v23, v222
	ds_bpermute_b32 v18, v18, v17
	v_lshlrev_b32_e32 v15, 2, v15
	v_lshlrev_b32_e32 v23, 2, v23
	v_xor_b32_e32 v23, 8, v23
	ds_bpermute_b32 v23, v23, v16
	s_waitcnt lgkmcnt(1)
	v_add_f32_e32 v17, v17, v18
	v_lshlrev_b32_e32 v18, 2, v19
	v_mov_b32_e32 v19, v222
	s_waitcnt lgkmcnt(0)
	v_add_f32_e32 v16, v16, v23
	v_lshlrev_b32_e32 v19, 2, v19
	v_xor_b32_e32 v19, 16, v19
	ds_bpermute_b32 v19, v19, v16
	v_xor_b32_e32 v18, 16, v18
	ds_bpermute_b32 v18, v18, v17
	v_xor_b32_e32 v6, 0x80, v6
	v_xor_b32_e32 v9, 0x80, v9
	s_waitcnt lgkmcnt(1)
	v_add_f32_e32 v16, v16, v19
	v_mov_b32_e32 v19, v222
	s_waitcnt lgkmcnt(0)
	v_add_f32_e32 v17, v17, v18
	v_lshlrev_b32_e32 v19, 2, v19
	v_xor_b32_e32 v19, 32, v19
	v_lshlrev_b32_e32 v18, 2, v20
	ds_bpermute_b32 v19, v19, v16
	v_xor_b32_e32 v18, 32, v18
	ds_bpermute_b32 v18, v18, v17
	v_xor_b32_e32 v11, 0x80, v11
	v_xor_b32_e32 v13, 0x80, v13
	s_waitcnt lgkmcnt(1)
	v_add_f32_e32 v19, v16, v19
	v_mov_b32_e32 v16, v222
	s_waitcnt lgkmcnt(0)
	v_add_f32_e32 v17, v17, v18
	v_lshlrev_b32_e32 v18, 2, v21
	v_lshlrev_b32_e32 v16, 2, v16
	v_xor_b32_e32 v18, 64, v18
	v_xor_b32_e32 v16, 64, v16
	ds_bpermute_b32 v18, v18, v17
	ds_bpermute_b32 v20, v16, v19
	v_xor_b32_e32 v15, 0x80, v15
	ds_bpermute_b32 v6, v6, v4
	ds_bpermute_b32 v9, v9, v8
	s_waitcnt lgkmcnt(3)
	v_add_f32_e32 v16, v17, v18
	s_waitcnt lgkmcnt(2)
	v_add_f32_e32 v18, v19, v20
	v_mov_b32_e32 v19, v222
	v_lshlrev_b32_e32 v17, 2, v22
	v_lshlrev_b32_e32 v19, 2, v19
	v_xor_b32_e32 v17, 0x80, v17
	v_xor_b32_e32 v19, 0x80, v19
	ds_bpermute_b32 v11, v11, v10
	ds_bpermute_b32 v13, v13, v12
	ds_bpermute_b32 v15, v15, v14
	ds_bpermute_b32 v17, v17, v16
	ds_bpermute_b32 v19, v19, v18
	s_and_saveexec_b64 s[60:61], s[38:39]
	s_cbranch_execz .LBB0_1573
	s_waitcnt lgkmcnt(6)
	v_pk_add_f32 v[6:7], v[4:5], v[6:7]
	s_waitcnt lgkmcnt(5)
	v_add_f32_e32 v8, v8, v9
	v_cmp_gt_f32_e32 vcc, v6, v7
	s_waitcnt lgkmcnt(4)
	v_add_f32_e32 v10, v10, v11
	s_waitcnt lgkmcnt(3)
	v_add_f32_e32 v12, v12, v13
	v_cndmask_b32_e32 v4, v7, v6, vcc
	v_cmp_gt_f32_e64 s[0:1], v8, v4
	s_waitcnt lgkmcnt(2)
	v_add_f32_e32 v14, v14, v15
	s_waitcnt lgkmcnt(1)
	v_add_f32_e32 v16, v16, v17
	v_cndmask_b32_e64 v4, v4, v8, s[0:1]
	v_cmp_gt_f32_e64 s[4:5], v10, v4
	s_waitcnt lgkmcnt(0)
	v_add_f32_e32 v18, v18, v19
	s_mov_b32 s11, 0xff61b1e6
	v_cndmask_b32_e64 v4, v4, v10, s[4:5]
	v_cmp_gt_f32_e64 s[44:45], v12, v4
	v_cmp_nlt_f32_e64 s[52:53], s11, v7
	v_mov_b32_e32 v9, 0xff61b1e6
	v_cndmask_b32_e64 v4, v4, v12, s[44:45]
	v_cmp_gt_f32_e64 s[46:47], v14, v4
	s_mov_b32 s11, 0x3fb8aa3b
	s_nop 0
	v_cndmask_b32_e64 v4, v4, v14, s[46:47]
	v_cmp_gt_f32_e64 s[48:49], v16, v4
	s_nop 1
	v_cndmask_b32_e64 v5, v4, v16, s[48:49]
	v_cndmask_b32_e64 v4, 0, 1, vcc
	v_cndmask_b32_e64 v4, v4, 2, s[0:1]
	v_cndmask_b32_e64 v4, v4, 3, s[4:5]
	v_cndmask_b32_e64 v4, v4, 4, s[44:45]
	v_cndmask_b32_e64 v4, v4, 5, s[46:47]
	v_cndmask_b32_e64 v4, v4, 6, s[48:49]
	v_cmp_ngt_f32_e32 vcc, v18, v5
	s_and_b64 s[42:43], s[48:49], vcc
	s_nop 0
	v_cndmask_b32_e32 v4, 7, v4, vcc
	v_cmp_eq_u32_e64 s[50:51], 0, v4
	s_or_b64 s[50:51], s[50:51], s[52:53]
	v_cmp_ne_u32_e64 s[48:49], 1, v4
	v_cndmask_b32_e64 v7, v7, v9, s[50:51]
	v_cmp_gt_f32_e64 s[52:53], v6, v7
	s_and_b64 s[48:49], s[48:49], s[52:53]
	v_cndmask_b32_e64 v6, v7, v6, s[48:49]
	v_cmp_ne_u32_e64 s[46:47], 2, v4
	v_cmp_gt_f32_e64 s[52:53], v8, v6
	s_and_b64 s[46:47], s[46:47], s[52:53]
	v_cndmask_b32_e64 v6, v6, v8, s[46:47]
	v_cmp_ne_u32_e64 s[44:45], 3, v4
	v_cmp_gt_f32_e64 s[52:53], v10, v6
	s_and_b64 s[44:45], s[44:45], s[52:53]
	v_cndmask_b32_e64 v6, v6, v10, s[44:45]
	v_cmp_ne_u32_e64 s[4:5], 4, v4
	v_cmp_gt_f32_e64 s[52:53], v12, v6
	s_and_b64 s[4:5], s[4:5], s[52:53]
	v_cndmask_b32_e64 v6, v6, v12, s[4:5]
	v_cmp_ne_u32_e64 s[0:1], 5, v4
	v_cmp_gt_f32_e64 s[52:53], v14, v6
	s_and_b64 s[0:1], s[0:1], s[52:53]
	v_cndmask_b32_e64 v6, v6, v14, s[0:1]
	v_cmp_ngt_f32_e64 s[52:53], v16, v6
	s_or_b64 s[52:53], s[42:43], s[52:53]
	v_cndmask_b32_e32 v5, v18, v5, vcc
	v_cndmask_b32_e64 v6, v16, v6, s[52:53]
	v_cmp_gt_f32_e64 s[54:55], v18, v6
	s_and_b64 s[54:55], vcc, s[54:55]
	v_cndmask_b32_e64 v7, 0, -1, s[50:51]
	v_cndmask_b32_e64 v6, v6, v18, s[54:55]
	v_sub_f32_e32 v5, v6, v5
	v_mul_f32_e32 v6, 0x3fb8aa3b, v5
	v_fma_f32 v8, v5, s11, -v6
	v_rndne_f32_e32 v9, v6
	v_fmac_f32_e32 v8, 0x32a5705f, v5
	v_sub_f32_e32 v6, v6, v9
	v_add_f32_e32 v6, v6, v8
	v_cndmask_b32_e64 v7, v7, 1, s[48:49]
	v_exp_f32_e32 v6, v6
	v_cvt_i32_f32_e32 v8, v9
	v_cndmask_b32_e64 v7, v7, 2, s[46:47]
	v_cndmask_b32_e64 v7, v7, 3, s[44:45]
	v_cndmask_b32_e64 v7, v7, 4, s[4:5]
	s_mov_b32 s4, 0xc2ce8ed0
	v_ldexp_f32 v6, v6, v8
	v_cmp_ngt_f32_e32 vcc, s4, v5
	s_mov_b32 s4, 0x42b17218
	s_nop 0
	v_cndmask_b32_e32 v6, 0, v6, vcc
	v_cmp_nlt_f32_e32 vcc, s4, v5
	s_nop 1
	v_cndmask_b32_e32 v5, v223, v6, vcc
	v_add_f32_e32 v6, 1.0, v5
	v_div_scale_f32 v8, s[4:5], v6, v6, 1.0
	v_rcp_f32_e32 v9, v8
	v_cndmask_b32_e64 v5, v7, 5, s[0:1]
	v_readlane_b32 s0, v253, 37
	v_cndmask_b32_e64 v5, 6, v5, s[52:53]
	v_fma_f32 v7, -v8, v9, 1.0
	v_fmac_f32_e32 v9, v7, v9
	v_div_scale_f32 v7, vcc, 1.0, v6, 1.0
	v_mul_f32_e32 v10, v7, v9
	v_fma_f32 v11, -v8, v10, v7
	v_fmac_f32_e32 v10, v11, v9
	v_fma_f32 v7, -v8, v10, v7
	v_div_fmas_f32 v7, v7, v9, v10
	v_div_fixup_f32 v6, v7, v6, 1.0
	v_readlane_b32 s1, v253, 38
	v_cndmask_b32_e64 v5, v5, 7, s[54:55]
	v_sub_f32_e32 v7, 1.0, v6
	v_lshl_add_u64 v[8:9], v[58:59], 4, s[0:1]
	s_add_i32 s0, 0, 0x26000
	global_store_dwordx4 v[8:9], v[4:7], off
	s_nop 1
	v_lshl_add_u32 v4, v4, 2, s0
	v_mov_b32_e32 v6, 1
	ds_add_u32 v4, v6
	v_lshl_add_u32 v4, v5, 2, s0
	ds_add_u32 v4, v6
	s_branch .LBB0_1573

.LBB0_2023:
	v_mov_b32_e32 v66, v13
	v_mov_b32_e32 v67, v5
	v_mov_b32_e32 v64, v12
	v_mov_b32_e32 v65, v4
	v_pk_mul_f32 v[66:67], v[66:67], v[66:67]
	v_mov_b32_e32 v68, v15
	v_mov_b32_e32 v69, v7
	v_pk_fma_f32 v[64:65], v[64:65], v[64:65], v[66:67]
	v_mov_b32_e32 v66, v14
	v_mov_b32_e32 v67, v6
	v_pk_mul_f32 v[68:69], v[68:69], v[68:69]
	v_mul_f32_e32 v63, v24, v24
	v_pk_fma_f32 v[66:67], v[66:67], v[66:67], v[68:69]
	v_pk_mul_f32 v[68:69], v[20:21], v[20:21]
	v_pk_add_f32 v[64:65], v[64:65], v[66:67]
	v_pk_mul_f32 v[66:67], v[22:23], v[22:23]
	v_pk_add_f32 v[64:65], v[64:65], v[64:65] op_sel:[0,1] op_sel_hi:[1,0]
	v_pk_mov_b32 v[70:71], v[68:69], v[66:67] op_sel:[1,0]
	v_mov_b32_e32 v69, v67
	v_pk_add_f32 v[66:67], v[70:71], v[68:69]
	v_mul_f32_e32 v68, v25, v25
	v_pk_add_f32 v[66:67], v[66:67], v[66:67] op_sel:[0,1] op_sel_hi:[1,0]
	v_mov_b32_e32 v65, v63
	v_mov_b32_e32 v67, v68
	v_pk_add_f32 v[64:65], v[64:65], v[66:67]
	v_mul_f32_e32 v66, v9, v9
	v_mul_f32_e32 v69, v26, v26
	v_pk_fma_f32 v[66:67], v[8:9], v[8:9], v[66:67] op_sel_hi:[1,1,0]
	v_mul_f32_e32 v68, v11, v11
	v_mul_f32_e32 v70, v27, v27
	v_mov_b32_e32 v67, v69
	v_pk_fma_f32 v[68:69], v[10:11], v[10:11], v[68:69] op_sel_hi:[1,1,0]
	v_mul_f32_e32 v63, v28, v28
	v_mov_b32_e32 v69, v70
	v_pk_add_f32 v[66:67], v[66:67], v[68:69]
	v_pk_mul_f32 v[68:69], v[16:17], v[16:17]
	v_pk_add_f32 v[64:65], v[64:65], v[66:67]
	v_pk_mul_f32 v[66:67], v[18:19], v[18:19]
	v_pk_add_f32 v[64:65], v[64:65], v[64:65] op_sel:[0,1] op_sel_hi:[1,0]
	v_pk_mov_b32 v[70:71], v[68:69], v[66:67] op_sel:[1,0]
	v_mov_b32_e32 v69, v67
	v_pk_add_f32 v[66:67], v[70:71], v[68:69]
	v_mul_f32_e32 v68, v29, v29
	v_pk_add_f32 v[66:67], v[66:67], v[66:67] op_sel:[0,1] op_sel_hi:[1,0]
	v_mov_b32_e32 v65, v63
	v_mov_b32_e32 v67, v68
	v_pk_add_f32 v[64:65], v[64:65], v[66:67]
	v_mul_f32_e32 v66, v33, v33
	v_mul_f32_e32 v69, v30, v30
	v_pk_fma_f32 v[66:67], v[32:33], v[32:33], v[66:67] op_sel_hi:[1,1,0]
	v_mul_f32_e32 v68, v35, v35
	v_mul_f32_e32 v70, v31, v31
	v_mov_b32_e32 v67, v69
	v_pk_fma_f32 v[68:69], v[34:35], v[34:35], v[68:69] op_sel_hi:[1,1,0]
	s_and_b64 s[0:1], exec, s[0:1]
	v_mov_b32_e32 v69, v70
	v_pk_add_f32 v[66:67], v[66:67], v[68:69]
	s_or_b64 s[48:49], s[0:1], s[48:49]
	v_pk_add_f32 v[64:65], v[64:65], v[66:67]
	s_mov_b32 s0, 0x800000
	v_add_f32_e32 v63, v64, v65
	v_add_u32_e32 v129, 8, v129
	s_nop 1
	v_add_f32_dpp v63, v63, v63 quad_perm:[1,0,3,2] row_mask:0xf bank_mask:0xf
	s_nop 1
	v_add_f32_dpp v63, v63, v63 quad_perm:[2,3,0,1] row_mask:0xf bank_mask:0xf
	s_nop 1
	v_add_f32_dpp v63, v63, v63 row_half_mirror row_mask:0xf bank_mask:0xf
	s_nop 1
	v_add_f32_dpp v63, v63, v63 row_mirror row_mask:0xf bank_mask:0xf
	s_nop 0
	v_readlane_b32 s100, v63, 0
	v_readlane_b32 s101, v63, 16
	s_nop 1
	v_mov_b32_e32 v64, s101
	v_add_f32_e32 v64, s100, v64
	v_readlane_b32 s100, v63, 32
	v_readlane_b32 s101, v63, 48
	s_nop 1
	v_mov_b32_e32 v63, s101
	v_add_f32_e32 v63, s100, v63
	v_add_f32_e32 v63, v64, v63
	s_waitcnt lgkmcnt(0)
	ds_read_b128 v[66:69], v128
	ds_read_b128 v[70:73], v102 offset:24576
	ds_read_b128 v[74:77], v102 offset:49152
	v_fmamk_f32 v63, v63, 0x3a000000, v213
	v_cmp_gt_f32_e32 vcc, s0, v63
	v_mul_f32_e32 v64, 0x4b800000, v63
	s_nop 0
	v_cndmask_b32_e32 v63, v63, v64, vcc
	v_rsq_f32_e32 v63, v63
	s_nop 0
	v_mul_f32_e32 v64, 0x45800000, v63
	v_cndmask_b32_e32 v64, v63, v64, vcc
	v_pk_mul_f32 v[14:15], v[14:15], v[64:65] op_sel_hi:[1,0]
	v_pk_mul_f32 v[12:13], v[12:13], v[64:65] op_sel_hi:[1,0]
	v_ashrrev_i32_e32 v63, 31, v62
	s_waitcnt lgkmcnt(0)
	v_pk_mul_f32 v[12:13], v[66:67], v[12:13]
	v_pk_mul_f32 v[14:15], v[68:69], v[14:15]
	v_pk_add_f32 v[66:67], v[76:77], 1.0 op_sel_hi:[1,0]
	v_pk_add_f32 v[68:69], v[74:75], 1.0 op_sel_hi:[1,0]
	v_lshlrev_b64 v[62:63], 12, v[62:63]
	v_pk_fma_f32 v[14:15], v[66:67], v[14:15], v[72:73]
	v_pk_fma_f32 v[12:13], v[68:69], v[12:13], v[70:71]
	v_lshl_add_u64 v[62:63], v[58:59], 0, v[62:63]
	v_cvt_pk_bf16_f32 v12, v12, v13
	v_cvt_pk_bf16_f32 v13, v14, v15
	global_store_dwordx2 v[62:63], v[12:13], off
	ds_read_b128 v[12:15], v128 offset:1024
	ds_read_b128 v[66:69], v102 offset:25600
	ds_read_b128 v[70:73], v102 offset:50176
	v_pk_mul_f32 v[6:7], v[6:7], v[64:65] op_sel_hi:[1,0]
	v_pk_mul_f32 v[4:5], v[4:5], v[64:65] op_sel_hi:[1,0]
	s_waitcnt lgkmcnt(2)
	v_pk_mul_f32 v[6:7], v[14:15], v[6:7]
	v_pk_mul_f32 v[4:5], v[12:13], v[4:5]
	s_waitcnt lgkmcnt(0)
	v_pk_add_f32 v[12:13], v[72:73], 1.0 op_sel_hi:[1,0]
	v_pk_add_f32 v[14:15], v[70:71], 1.0 op_sel_hi:[1,0]
	v_pk_fma_f32 v[6:7], v[12:13], v[6:7], v[68:69]
	v_pk_fma_f32 v[4:5], v[14:15], v[4:5], v[66:67]
	v_pk_mul_f32 v[22:23], v[22:23], v[64:65] op_sel_hi:[1,0]
	v_cvt_pk_bf16_f32 v4, v4, v5
	v_cvt_pk_bf16_f32 v5, v6, v7
	global_store_dwordx2 v[62:63], v[4:5], off offset:512
	ds_read_b128 v[4:7], v128 offset:2048
	ds_read_b128 v[12:15], v102 offset:26624
	ds_read_b128 v[66:69], v102 offset:51200
	v_pk_mul_f32 v[20:21], v[20:21], v[64:65] op_sel_hi:[1,0]
	v_pk_mul_f32 v[10:11], v[10:11], v[64:65] op_sel_hi:[1,0]
	s_waitcnt lgkmcnt(2)
	v_pk_mul_f32 v[4:5], v[4:5], v[20:21]
	v_pk_mul_f32 v[6:7], v[6:7], v[22:23]
	s_waitcnt lgkmcnt(0)
	v_pk_add_f32 v[20:21], v[68:69], 1.0 op_sel_hi:[1,0]
	v_pk_add_f32 v[22:23], v[66:67], 1.0 op_sel_hi:[1,0]
	v_pk_fma_f32 v[6:7], v[20:21], v[6:7], v[14:15]
	v_pk_fma_f32 v[4:5], v[22:23], v[4:5], v[12:13]
	v_pk_mul_f32 v[8:9], v[8:9], v[64:65] op_sel_hi:[1,0]
	v_cvt_pk_bf16_f32 v4, v4, v5
	v_cvt_pk_bf16_f32 v5, v6, v7
	global_store_dwordx2 v[62:63], v[4:5], off offset:1024
	ds_read_b128 v[4:7], v128 offset:3072
	ds_read_b128 v[12:15], v102 offset:27648
	ds_read_b128 v[20:23], v102 offset:52224
	v_pk_mul_f32 v[18:19], v[18:19], v[64:65] op_sel_hi:[1,0]
	v_pk_mul_f32 v[16:17], v[16:17], v[64:65] op_sel_hi:[1,0]
	s_waitcnt lgkmcnt(2)
	v_pk_mul_f32 v[4:5], v[8:9], v[4:5]
	v_pk_mul_f32 v[6:7], v[10:11], v[6:7]
	s_waitcnt lgkmcnt(0)
	v_pk_add_f32 v[8:9], v[22:23], 1.0 op_sel_hi:[1,0]
	v_pk_add_f32 v[10:11], v[20:21], 1.0 op_sel_hi:[1,0]
	v_pk_fma_f32 v[6:7], v[6:7], v[8:9], v[14:15]
	v_pk_fma_f32 v[4:5], v[4:5], v[10:11], v[12:13]
	v_pk_mul_f32 v[20:21], v[26:27], v[64:65] op_sel_hi:[1,0]
	v_cvt_pk_bf16_f32 v4, v4, v5
	v_cvt_pk_bf16_f32 v5, v6, v7
	global_store_dwordx2 v[62:63], v[4:5], off offset:1536
	ds_read_b128 v[4:7], v128 offset:4096
	ds_read_b128 v[8:11], v102 offset:28672
	ds_read_b128 v[12:15], v102 offset:53248
	v_pk_mul_f32 v[22:23], v[24:25], v[64:65] op_sel_hi:[1,0]
	s_waitcnt lgkmcnt(2)
	v_pk_mul_f32 v[6:7], v[20:21], v[6:7]
	v_pk_mul_f32 v[4:5], v[22:23], v[4:5]
	s_waitcnt lgkmcnt(0)
	v_pk_add_f32 v[14:15], v[14:15], 1.0 op_sel_hi:[1,0]
	v_pk_add_f32 v[12:13], v[12:13], 1.0 op_sel_hi:[1,0]
	v_pk_fma_f32 v[6:7], v[6:7], v[14:15], v[10:11]
	v_pk_fma_f32 v[4:5], v[4:5], v[12:13], v[8:9]
	s_nop 0
	v_cvt_pk_bf16_f32 v4, v4, v5
	v_cvt_pk_bf16_f32 v5, v6, v7
	global_store_dwordx2 v[62:63], v[4:5], off offset:2048
	ds_read_b128 v[4:7], v128 offset:5120
	ds_read_b128 v[8:11], v102 offset:29696
	ds_read_b128 v[12:15], v102 offset:54272
	s_waitcnt lgkmcnt(2)
	v_pk_mul_f32 v[4:5], v[16:17], v[4:5]
	v_pk_mul_f32 v[6:7], v[18:19], v[6:7]
	s_waitcnt lgkmcnt(0)
	v_pk_add_f32 v[14:15], v[14:15], 1.0 op_sel_hi:[1,0]
	v_pk_add_f32 v[12:13], v[12:13], 1.0 op_sel_hi:[1,0]
	v_pk_fma_f32 v[6:7], v[6:7], v[14:15], v[10:11]
	v_pk_fma_f32 v[4:5], v[4:5], v[12:13], v[8:9]
	v_pk_mul_f32 v[16:17], v[34:35], v[64:65] op_sel_hi:[1,0]
	v_cvt_pk_bf16_f32 v4, v4, v5
	v_cvt_pk_bf16_f32 v5, v6, v7
	global_store_dwordx2 v[62:63], v[4:5], off offset:2560
	ds_read_b128 v[4:7], v128 offset:6144
	ds_read_b128 v[8:11], v102 offset:30720
	ds_read_b128 v[12:15], v102 offset:55296
	v_pk_mul_f32 v[18:19], v[32:33], v[64:65] op_sel_hi:[1,0]
	s_waitcnt lgkmcnt(2)
	v_pk_mul_f32 v[6:7], v[16:17], v[6:7]
	v_pk_mul_f32 v[4:5], v[18:19], v[4:5]
	s_waitcnt lgkmcnt(0)
	v_pk_add_f32 v[14:15], v[14:15], 1.0 op_sel_hi:[1,0]
	v_pk_add_f32 v[12:13], v[12:13], 1.0 op_sel_hi:[1,0]
	v_pk_fma_f32 v[6:7], v[6:7], v[14:15], v[10:11]
	v_pk_fma_f32 v[4:5], v[4:5], v[12:13], v[8:9]
	v_pk_mul_f32 v[16:17], v[30:31], v[64:65] op_sel_hi:[1,0]
	v_cvt_pk_bf16_f32 v4, v4, v5
	v_cvt_pk_bf16_f32 v5, v6, v7
	global_store_dwordx2 v[62:63], v[4:5], off offset:3072
	ds_read_b128 v[4:7], v128 offset:7168
	ds_read_b128 v[8:11], v102 offset:31744
	ds_read_b128 v[12:15], v102 offset:56320
	v_pk_mul_f32 v[18:19], v[28:29], v[64:65] op_sel_hi:[1,0]
	s_waitcnt vmcnt(8)
	v_mov_b64_e32 v[30:31], v[92:93]
	s_waitcnt lgkmcnt(2)
	v_pk_mul_f32 v[4:5], v[18:19], v[4:5]
	v_pk_mul_f32 v[6:7], v[16:17], v[6:7]
	s_waitcnt lgkmcnt(0)
	v_pk_add_f32 v[14:15], v[14:15], 1.0 op_sel_hi:[1,0]
	v_pk_add_f32 v[12:13], v[12:13], 1.0 op_sel_hi:[1,0]
	v_pk_fma_f32 v[6:7], v[6:7], v[14:15], v[10:11]
	v_pk_fma_f32 v[4:5], v[4:5], v[12:13], v[8:9]
	v_mov_b64_e32 v[10:11], v[84:85]
	v_cvt_pk_bf16_f32 v4, v4, v5
	v_cvt_pk_bf16_f32 v5, v6, v7
	global_store_dwordx2 v[62:63], v[4:5], off offset:3584
	v_mov_b64_e32 v[6:7], v[80:81]
	v_mov_b64_e32 v[4:5], v[82:83]
	v_mov_b64_e32 v[8:9], v[86:87]
	v_mov_b64_e32 v[18:19], v[88:89]
	v_mov_b64_e32 v[16:17], v[90:91]
	s_waitcnt vmcnt(8)
	v_mov_b64_e32 v[28:29], v[94:95]
	s_andn2_b64 exec, exec, s[48:49]
	s_cbranch_execz .LBB0_2077

.LBB0_2033:
	s_or_b64 exec, exec, s[4:5]
	v_pk_mul_f32 v[108:109], v[14:15], v[14:15]
	v_pk_mul_f32 v[110:111], v[78:79], v[78:79]
	v_pk_mul_f32 v[104:105], v[12:13], v[12:13]
	v_pk_mul_f32 v[106:107], v[76:77], v[76:77]
	v_mov_b32_e32 v112, v108
	v_mov_b32_e32 v113, v110
	v_mov_b32_e32 v110, v109
	v_pk_mul_f32 v[100:101], v[20:21], v[20:21]
	v_pk_mul_f32 v[102:103], v[22:23], v[22:23]
	v_pk_add_f32 v[108:109], v[112:113], v[110:111]
	v_mov_b32_e32 v110, v104
	v_mov_b32_e32 v111, v106
	v_mov_b32_e32 v106, v105
	v_pk_add_f32 v[104:105], v[110:111], v[106:107]
	v_pk_mov_b32 v[106:107], v[102:103], v[100:101] op_sel:[1,0]
	v_mov_b32_e32 v103, v101
	v_pk_add_f32 v[100:101], v[106:107], v[102:103]
	v_pk_add_f32 v[104:105], v[108:109], v[104:105]
	v_pk_add_f32 v[100:101], v[100:101], v[100:101] op_sel_hi:[0,1]
	v_mul_f32_e32 v100, v74, v74
	v_pk_fma_f32 v[102:103], v[74:75], v[74:75], v[100:101] op_sel_hi:[1,1,0]
	v_mul_f32_e32 v100, v72, v72
	v_pk_add_f32 v[104:105], v[104:105], v[104:105] op_sel_hi:[0,1]
	v_pk_fma_f32 v[106:107], v[72:73], v[72:73], v[100:101] op_sel_hi:[1,1,0]
	v_mul_f32_e32 v102, v26, v26
	v_mul_f32_e32 v106, v27, v27
	v_mul_f32_e32 v100, v24, v24
	v_mul_f32_e32 v104, v25, v25
	v_pk_mul_f32 v[96:97], v[66:67], v[66:67]
	v_pk_mul_f32 v[98:99], v[68:69], v[68:69]
	v_pk_add_f32 v[102:103], v[102:103], v[106:107]
	v_pk_add_f32 v[100:101], v[100:101], v[104:105]
	v_readlane_b32 s20, v249, 26
	v_pk_add_f32 v[100:101], v[102:103], v[100:101]
	v_pk_mov_b32 v[102:103], v[98:99], v[96:97] op_sel:[1,0]
	v_mov_b32_e32 v99, v97
	v_pk_add_f32 v[96:97], v[102:103], v[98:99]
	v_pk_add_f32 v[100:101], v[100:101], v[100:101] op_sel_hi:[0,1]
	v_pk_add_f32 v[96:97], v[96:97], v[96:97] op_sel_hi:[0,1]
	v_mul_f32_e32 v96, v34, v34
	v_pk_fma_f32 v[98:99], v[34:35], v[34:35], v[96:97] op_sel_hi:[1,1,0]
	v_mul_f32_e32 v96, v32, v32
	v_pk_fma_f32 v[102:103], v[32:33], v[32:33], v[96:97] op_sel_hi:[1,1,0]
	v_mul_f32_e32 v98, v64, v64
	v_mul_f32_e32 v102, v65, v65
	v_mul_f32_e32 v96, v70, v70
	v_mul_f32_e32 v100, v71, v71
	v_pk_add_f32 v[98:99], v[98:99], v[102:103]
	v_pk_add_f32 v[96:97], v[96:97], v[100:101]
	s_movk_i32 s4, 0x1fff
	v_pk_add_f32 v[96:97], v[98:99], v[96:97]
	v_readlane_b32 s21, v249, 27
	v_add_f32_e32 v63, v96, v97
	v_cmp_lt_i32_e64 s[4:5], s4, v62
	s_nop 1
	v_add_f32_dpp v63, v63, v63 quad_perm:[1,0,3,2] row_mask:0xf bank_mask:0xf
	s_nop 1
	v_add_f32_dpp v63, v63, v63 quad_perm:[2,3,0,1] row_mask:0xf bank_mask:0xf
	s_nop 1
	v_add_f32_dpp v63, v63, v63 row_half_mirror row_mask:0xf bank_mask:0xf
	s_nop 1
	v_add_f32_dpp v63, v63, v63 row_mirror row_mask:0xf bank_mask:0xf
	s_nop 0
	v_readlane_b32 s100, v63, 0
	v_readlane_b32 s101, v63, 16
	s_nop 1
	v_mov_b32_e32 v96, s101
	v_add_f32_e32 v96, s100, v96
	v_readlane_b32 s100, v63, 32
	v_readlane_b32 s101, v63, 48
	s_nop 1
	v_mov_b32_e32 v98, s101
	v_add_f32_e32 v98, s100, v98
	v_add_f32_e32 v98, v96, v98
	v_mov_b32_e32 v99, 0
	s_mov_b64 s[10:11], -1
	s_and_b64 vcc, exec, s[20:21]
	s_waitcnt lgkmcnt(0)
	s_cbranch_vccz .LBB0_2039
	s_and_saveexec_b64 s[10:11], s[4:5]
	s_xor_b64 s[10:11], exec, s[10:11]
	s_cbranch_execz .LBB0_2036
	v_add_u32_e32 v96, 0xffffe000, v62
	v_mov_b32_e32 v97, v3
	v_readlane_b32 s52, v248, 0
	v_lshlrev_b64 v[96:97], 13, v[96:97]
	v_readlane_b32 s56, v248, 4
	v_readlane_b32 s57, v248, 5
	v_readlane_b32 s53, v248, 1
	v_readlane_b32 s54, v248, 2
	v_readlane_b32 s55, v248, 3
	v_readlane_b32 s58, v248, 6
	v_readlane_b32 s59, v248, 7
	v_lshl_add_u64 v[96:97], s[56:57], 0, v[96:97]

.LBB0_2089:
	s_or_b64 exec, exec, s[46:47]
	v_lshlrev_b32_e32 v131, 16, v112
	v_lshlrev_b32_e32 v130, 16, v104
	v_lshlrev_b32_e32 v126, 16, v100
	v_and_b32_e32 v127, 0xffff0000, v100
	v_lshlrev_b32_e32 v128, 16, v101
	v_and_b32_e32 v129, 0xffff0000, v101
	v_lshlrev_b32_e32 v120, 16, v96
	v_and_b32_e32 v121, 0xffff0000, v96
	v_lshlrev_b32_e32 v122, 16, v97
	v_and_b32_e32 v123, 0xffff0000, v97
	v_lshlrev_b32_e32 v116, 16, v78
	v_and_b32_e32 v117, 0xffff0000, v78
	v_lshlrev_b32_e32 v118, 16, v79
	v_and_b32_e32 v119, 0xffff0000, v79
	v_lshlrev_b32_e32 v106, 16, v72
	v_and_b32_e32 v107, 0xffff0000, v72
	v_lshlrev_b32_e32 v108, 16, v73
	v_and_b32_e32 v109, 0xffff0000, v73
	v_lshlrev_b32_e32 v96, 16, v70
	v_and_b32_e32 v97, 0xffff0000, v70
	v_lshlrev_b32_e32 v100, 16, v71
	v_and_b32_e32 v101, 0xffff0000, v71
	v_lshlrev_b32_e32 v72, 16, v68
	v_and_b32_e32 v73, 0xffff0000, v68
	v_lshlrev_b32_e32 v78, 16, v69
	v_and_b32_e32 v79, 0xffff0000, v69
	v_lshlrev_b32_e32 v68, 16, v66
	v_and_b32_e32 v69, 0xffff0000, v66
	v_lshlrev_b32_e32 v70, 16, v67
	v_and_b32_e32 v71, 0xffff0000, v67
	v_lshlrev_b32_e32 v66, 16, v124
	v_and_b32_e32 v67, 0xffff0000, v124
	v_lshlrev_b32_e32 v8, 16, v125
	v_and_b32_e32 v9, 0xffff0000, v125
	v_lshlrev_b32_e32 v125, 16, v110
	v_lshlrev_b32_e32 v124, 16, v114
	v_pk_mul_f32 v[130:131], v[10:11], v[130:131]
	v_and_b32_e32 v133, 0xffff0000, v112
	v_and_b32_e32 v132, 0xffff0000, v104
	v_pk_fma_f32 v[124:125], v[10:11], v[124:125], v[130:131] op_sel:[1,0,0] op_sel_hi:[0,1,1]
	v_and_b32_e32 v131, 0xffff0000, v110
	v_and_b32_e32 v130, 0xffff0000, v114
	v_pk_mul_f32 v[132:133], v[10:11], v[132:133]
	v_lshlrev_b32_e32 v137, 16, v113
	v_and_b32_e32 v113, 0xffff0000, v113
	v_and_b32_e32 v112, 0xffff0000, v105
	v_pk_fma_f32 v[130:131], v[10:11], v[130:131], v[132:133] op_sel:[1,0,0] op_sel_hi:[0,1,1]
	v_lshlrev_b32_e32 v133, 16, v111
	v_lshlrev_b32_e32 v136, 16, v105
	v_and_b32_e32 v111, 0xffff0000, v111
	v_and_b32_e32 v110, 0xffff0000, v115
	v_pk_mul_f32 v[104:105], v[10:11], v[112:113]
	v_lshlrev_b32_e32 v113, 16, v103
	v_lshlrev_b32_e32 v112, 16, v98
	v_pk_fma_f32 v[110:111], v[10:11], v[110:111], v[104:105] op_sel:[1,0,0] op_sel_hi:[0,1,1]
	v_lshlrev_b32_e32 v105, 16, v99
	v_lshlrev_b32_e32 v104, 16, v102
	v_pk_mul_f32 v[112:113], v[10:11], v[112:113]
	v_and_b32_e32 v98, 0xffff0000, v98
	v_pk_fma_f32 v[104:105], v[10:11], v[104:105], v[112:113] op_sel:[1,0,0] op_sel_hi:[0,1,1]
	v_and_b32_e32 v113, 0xffff0000, v99
	v_and_b32_e32 v99, 0xffff0000, v103
	v_and_b32_e32 v112, 0xffff0000, v102
	v_pk_mul_f32 v[98:99], v[10:11], v[98:99]
	v_lshlrev_b32_e32 v132, 16, v115
	v_pk_fma_f32 v[102:103], v[10:11], v[112:113], v[98:99] op_sel:[1,0,0] op_sel_hi:[0,1,1]
	v_lshlrev_b32_e32 v112, 16, v92
	v_and_b32_e32 v113, 0xffff0000, v94
	v_lshlrev_b32_e32 v98, 16, v94
	v_and_b32_e32 v99, 0xffff0000, v92
	v_pk_mul_f32 v[112:113], v[10:11], v[112:113]
	v_lshlrev_b32_e32 v92, 16, v93
	v_pk_fma_f32 v[98:99], v[10:11], v[98:99], v[112:113] op_sel:[1,0,0] op_sel_hi:[0,1,1]
	v_and_b32_e32 v113, 0xffff0000, v93
	v_and_b32_e32 v93, 0xffff0000, v95
	v_lshlrev_b32_e32 v112, 16, v95
	v_pk_mul_f32 v[92:93], v[10:11], v[92:93]
	v_pk_mul_f32 v[136:137], v[10:11], v[136:137]
	v_pk_fma_f32 v[94:95], v[10:11], v[112:113], v[92:93] op_sel:[1,0,0] op_sel_hi:[0,1,1]
	v_lshlrev_b32_e32 v112, 16, v88
	v_and_b32_e32 v113, 0xffff0000, v90
	v_lshlrev_b32_e32 v92, 16, v90
	v_and_b32_e32 v93, 0xffff0000, v88
	v_pk_mul_f32 v[112:113], v[10:11], v[112:113]
	v_lshlrev_b32_e32 v88, 16, v89
	v_pk_fma_f32 v[92:93], v[10:11], v[92:93], v[112:113] op_sel:[1,0,0] op_sel_hi:[0,1,1]
	v_and_b32_e32 v113, 0xffff0000, v89
	v_and_b32_e32 v89, 0xffff0000, v91
	v_lshlrev_b32_e32 v112, 16, v91
	v_pk_mul_f32 v[88:89], v[10:11], v[88:89]
	v_pk_fma_f32 v[132:133], v[10:11], v[132:133], v[136:137] op_sel:[1,0,0] op_sel_hi:[0,1,1]
	v_pk_fma_f32 v[90:91], v[10:11], v[112:113], v[88:89] op_sel:[1,0,0] op_sel_hi:[0,1,1]
	v_lshlrev_b32_e32 v113, 16, v87
	v_lshlrev_b32_e32 v112, 16, v84
	v_lshlrev_b32_e32 v89, 16, v85
	v_lshlrev_b32_e32 v88, 16, v86
	v_pk_mul_f32 v[112:113], v[10:11], v[112:113]
	v_and_b32_e32 v84, 0xffff0000, v84
	v_pk_fma_f32 v[88:89], v[10:11], v[88:89], v[112:113] op_sel:[1,0,0] op_sel_hi:[0,1,1]
	v_and_b32_e32 v113, 0xffff0000, v85
	v_and_b32_e32 v85, 0xffff0000, v87
	v_and_b32_e32 v112, 0xffff0000, v86
	v_pk_mul_f32 v[84:85], v[10:11], v[84:85]
	v_mul_f32_e32 v2, v94, v94
	v_pk_fma_f32 v[86:87], v[10:11], v[112:113], v[84:85] op_sel:[1,0,0] op_sel_hi:[0,1,1]
	v_lshlrev_b32_e32 v112, 16, v80
	v_and_b32_e32 v113, 0xffff0000, v82
	v_lshlrev_b32_e32 v84, 16, v82
	v_and_b32_e32 v85, 0xffff0000, v80
	v_pk_mul_f32 v[112:113], v[10:11], v[112:113]
	v_lshlrev_b32_e32 v80, 16, v81
	v_pk_fma_f32 v[84:85], v[10:11], v[84:85], v[112:113] op_sel:[1,0,0] op_sel_hi:[0,1,1]
	v_and_b32_e32 v113, 0xffff0000, v81
	v_and_b32_e32 v81, 0xffff0000, v83
	v_lshlrev_b32_e32 v112, 16, v83
	v_pk_mul_f32 v[80:81], v[10:11], v[80:81]
	v_pk_mul_f32 v[114:115], v[92:93], v[92:93]
	v_pk_fma_f32 v[82:83], v[10:11], v[112:113], v[80:81] op_sel:[1,0,0] op_sel_hi:[0,1,1]
	v_lshlrev_b32_e32 v112, 16, v74
	v_and_b32_e32 v113, 0xffff0000, v76
	v_lshlrev_b32_e32 v80, 16, v76
	v_and_b32_e32 v81, 0xffff0000, v74
	v_pk_mul_f32 v[112:113], v[10:11], v[112:113]
	v_lshlrev_b32_e32 v74, 16, v75
	v_pk_fma_f32 v[80:81], v[10:11], v[80:81], v[112:113] op_sel:[1,0,0] op_sel_hi:[0,1,1]
	v_and_b32_e32 v113, 0xffff0000, v75
	v_and_b32_e32 v75, 0xffff0000, v77
	v_lshlrev_b32_e32 v112, 16, v77
	v_pk_mul_f32 v[74:75], v[10:11], v[74:75]
	v_pk_mul_f32 v[76:77], v[110:111], v[110:111]
	v_pk_fma_f32 v[10:11], v[10:11], v[112:113], v[74:75] op_sel:[1,0,0] op_sel_hi:[0,1,1]
	v_pk_mul_f32 v[74:75], v[130:131], v[130:131]
	v_pk_fma_f32 v[76:77], v[132:133], v[132:133], v[76:77]
	v_pk_fma_f32 v[74:75], v[124:125], v[124:125], v[74:75]
	v_pk_fma_f32 v[112:113], v[94:95], v[94:95], v[2:3] op_sel_hi:[1,1,0]
	v_pk_add_f32 v[74:75], v[74:75], v[76:77]
	v_pk_mul_f32 v[76:77], v[102:103], v[102:103]
	v_mul_f32_e32 v2, v98, v98
	v_pk_fma_f32 v[76:77], v[104:105], v[104:105], v[76:77]
	v_pk_add_f32 v[74:75], v[74:75], v[74:75] op_sel_hi:[0,1]
	v_pk_add_f32 v[76:77], v[76:77], v[76:77] op_sel_hi:[0,1]
	v_pk_mul_f32 v[136:137], v[90:91], v[90:91]
	v_pk_fma_f32 v[138:139], v[98:99], v[98:99], v[2:3] op_sel_hi:[1,1,0]
	v_mov_b32_e32 v112, v115
	v_mov_b32_e32 v138, v114
	v_mov_b32_e32 v76, v136
	v_mov_b32_e32 v74, v137
	v_pk_add_f32 v[112:113], v[138:139], v[112:113]
	v_pk_add_f32 v[74:75], v[76:77], v[74:75]
	v_pk_mul_f32 v[76:77], v[86:87], v[86:87]
	v_mul_f32_e32 v2, v82, v82
	v_pk_add_f32 v[74:75], v[112:113], v[74:75]
	v_pk_fma_f32 v[76:77], v[88:89], v[88:89], v[76:77]
	v_pk_fma_f32 v[112:113], v[82:83], v[82:83], v[2:3] op_sel_hi:[1,1,0]
	v_mul_f32_e32 v2, v84, v84
	v_pk_add_f32 v[74:75], v[74:75], v[74:75] op_sel_hi:[0,1]
	v_pk_add_f32 v[76:77], v[76:77], v[76:77] op_sel_hi:[0,1]
	v_pk_mul_f32 v[114:115], v[80:81], v[80:81]
	v_pk_mul_f32 v[136:137], v[10:11], v[10:11]
	v_pk_fma_f32 v[138:139], v[84:85], v[84:85], v[2:3] op_sel_hi:[1,1,0]
	v_mov_b32_e32 v112, v115
	v_mov_b32_e32 v138, v114
	v_mov_b32_e32 v76, v136
	v_mov_b32_e32 v74, v137
	v_pk_add_f32 v[112:113], v[138:139], v[112:113]
	v_pk_add_f32 v[74:75], v[76:77], v[74:75]
	s_and_b64 s[0:1], exec, vcc
	v_pk_add_f32 v[74:75], v[112:113], v[74:75]
	s_or_b64 s[42:43], s[0:1], s[42:43]
	v_add_f32_e32 v2, v74, v75
	s_mov_b32 s0, 0x800000
	s_nop 1
	v_add_f32_dpp v2, v2, v2 quad_perm:[1,0,3,2] row_mask:0xf bank_mask:0xf
	s_nop 1
	v_add_f32_dpp v2, v2, v2 quad_perm:[2,3,0,1] row_mask:0xf bank_mask:0xf
	s_nop 1
	v_add_f32_dpp v2, v2, v2 row_half_mirror row_mask:0xf bank_mask:0xf
	s_nop 1
	v_add_f32_dpp v2, v2, v2 row_mirror row_mask:0xf bank_mask:0xf
	s_nop 0
	v_readlane_b32 s100, v2, 0
	v_readlane_b32 s101, v2, 16
	s_nop 1
	v_mov_b32_e32 v74, s101
	v_add_f32_e32 v74, s100, v74
	v_readlane_b32 s100, v2, 32
	v_readlane_b32 s101, v2, 48
	s_nop 1
	v_mov_b32_e32 v2, s101
	v_add_f32_e32 v2, s100, v2
	v_add_f32_e32 v2, v74, v2
	v_cmp_gt_i32_e32 vcc, s84, v135
	v_ashrrev_i32_e32 v75, 31, v135
	v_min_i32_e32 v17, 0x2000, v135
	v_cndmask_b32_e32 v77, 0, v75, vcc
	s_waitcnt lgkmcnt(0)
	v_mov_b32_e32 v75, s12
	v_mov_b32_e32 v140, v132
	v_mov_b32_e32 v141, v110
	v_mov_b32_e32 v142, v124
	v_mov_b32_e32 v143, v130
	v_mov_b32_e32 v110, v133
	v_mov_b32_e32 v130, v125
	v_add_u32_e32 v16, 16, v16
	v_fmamk_f32 v2, v2, 0x3a000000, v213
	v_cmp_gt_f32_e64 s[0:1], s0, v2
	v_mul_f32_e32 v74, 0x4b800000, v2
	s_nop 0
	v_cndmask_b32_e64 v2, v2, v74, s[0:1]
	v_rsq_f32_e32 v2, v2
	s_nop 0
	v_mul_f32_e32 v74, 0x45800000, v2
	v_cndmask_b32_e64 v74, v2, v74, s[0:1]
	v_add_u32_e32 v2, 0xffffe000, v135
	v_cndmask_b32_e32 v76, v2, v135, vcc
	v_mov_b32_e32 v2, s49
	v_cndmask_b32_e32 v113, v2, v75, vcc
	v_mov_b32_e32 v2, s50
	v_mov_b32_e32 v75, s48
	v_cndmask_b32_e32 v112, v2, v75, vcc
	v_lshlrev_b32_e32 v2, 1, v17
	v_and_b32_e32 v2, 0xffffe000, v2
	v_lshlrev_b64 v[76:77], 13, v[76:77]
	v_add_u32_e32 v17, v13, v2
	v_lshl_add_u64 v[76:77], v[112:113], 0, v[76:77]
	ds_read_b128 v[112:115], v17
	ds_read_b128 v[136:139], v134
	v_pk_mul_f32 v[140:141], v[140:141], v[74:75] op_sel_hi:[1,0]
	v_pk_mul_f32 v[142:143], v[142:143], v[74:75] op_sel_hi:[1,0]
	v_lshlrev_b32_e32 v2, 2, v12
	v_lshl_add_u64 v[76:77], v[76:77], 0, v[2:3]
	s_waitcnt lgkmcnt(0)
	v_pk_mul_f32 v[136:137], v[142:143], v[136:137]
	v_pk_mul_f32 v[138:139], v[140:141], v[138:139]
	v_pk_fma_f32 v[112:113], v[112:113], v[136:137], v[126:127]
	v_pk_fma_f32 v[114:115], v[114:115], v[138:139], v[128:129]
	global_store_dwordx4 v[76:77], v[112:115], off
	ds_read_b128 v[112:115], v17 offset:1024
	ds_read_b128 v[126:129], v134 offset:1024
	v_pk_mul_f32 v[110:111], v[110:111], v[74:75] op_sel_hi:[1,0]
	v_pk_mul_f32 v[124:125], v[130:131], v[74:75] op_sel_hi:[1,0]
	v_pk_mul_f32 v[94:95], v[94:95], v[74:75] op_sel_hi:[1,0]
	v_pk_mul_f32 v[98:99], v[98:99], v[74:75] op_sel_hi:[1,0]
	s_waitcnt lgkmcnt(0)
	v_pk_mul_f32 v[124:125], v[124:125], v[126:127]
	v_pk_mul_f32 v[110:111], v[110:111], v[128:129]
	v_pk_fma_f32 v[112:113], v[112:113], v[124:125], v[120:121]
	v_pk_fma_f32 v[114:115], v[114:115], v[110:111], v[122:123]
	global_store_dwordx4 v[76:77], v[112:115], off offset:1024
	ds_read_b128 v[110:113], v17 offset:2048
	ds_read_b128 v[120:123], v134 offset:2048
	v_mov_b32_e32 v114, v105
	v_mov_b32_e32 v115, v103
	v_mov_b32_e32 v105, v102
	v_pk_mul_f32 v[114:115], v[114:115], v[74:75] op_sel_hi:[1,0]
	v_pk_mul_f32 v[102:103], v[104:105], v[74:75] op_sel_hi:[1,0]
	s_waitcnt lgkmcnt(0)
	v_pk_mul_f32 v[104:105], v[114:115], v[122:123]
	v_pk_mul_f32 v[102:103], v[102:103], v[120:121]
	v_pk_fma_f32 v[104:105], v[112:113], v[104:105], v[118:119]
	v_pk_fma_f32 v[102:103], v[110:111], v[102:103], v[116:117]
	global_store_dwordx4 v[76:77], v[102:105], off offset:2048
	ds_read_b128 v[102:105], v17 offset:3072
	ds_read_b128 v[110:113], v134 offset:3072
	v_pk_mul_f32 v[90:91], v[90:91], v[74:75] op_sel_hi:[1,0]
	v_pk_mul_f32 v[92:93], v[92:93], v[74:75] op_sel_hi:[1,0]
	s_movk_i32 s0, 0x1000
	v_pk_mul_f32 v[82:83], v[82:83], v[74:75] op_sel_hi:[1,0]
	s_waitcnt lgkmcnt(0)
	v_pk_mul_f32 v[98:99], v[98:99], v[110:111]
	v_pk_mul_f32 v[94:95], v[94:95], v[112:113]
	v_pk_fma_f32 v[102:103], v[102:103], v[98:99], v[106:107]
	v_pk_fma_f32 v[104:105], v[104:105], v[94:95], v[108:109]
	global_store_dwordx4 v[76:77], v[102:105], off offset:3072
	ds_read_b128 v[102:105], v17 offset:4096
	ds_read_b128 v[106:109], v134 offset:4096
	v_add_co_u32_e32 v98, vcc, s0, v76
	v_mov_b32_e32 v76, v89
	s_nop 0
	v_addc_co_u32_e32 v99, vcc, 0, v77, vcc
	s_waitcnt lgkmcnt(0)
	v_pk_mul_f32 v[94:95], v[92:93], v[106:107]
	v_pk_mul_f32 v[90:91], v[90:91], v[108:109]
	v_mov_b32_e32 v77, v87
	v_pk_fma_f32 v[92:93], v[104:105], v[90:91], v[100:101]
	v_pk_fma_f32 v[90:91], v[102:103], v[94:95], v[96:97]
	global_store_dwordx4 v[98:99], v[90:93], off
	ds_read_b128 v[90:93], v17 offset:5120
	ds_read_b128 v[94:97], v134 offset:5120
	v_mov_b32_e32 v89, v86
	v_pk_mul_f32 v[76:77], v[76:77], v[74:75] op_sel_hi:[1,0]
	v_pk_mul_f32 v[86:87], v[88:89], v[74:75] op_sel_hi:[1,0]
	v_pk_mul_f32 v[10:11], v[10:11], v[74:75] op_sel_hi:[1,0]
	s_waitcnt lgkmcnt(0)
	v_pk_mul_f32 v[86:87], v[86:87], v[94:95]
	v_pk_mul_f32 v[76:77], v[76:77], v[96:97]
	s_waitcnt vmcnt(19)
	v_mov_b64_e32 v[110:111], v[52:53]
	v_pk_fma_f32 v[78:79], v[92:93], v[76:77], v[78:79]
	v_pk_fma_f32 v[76:77], v[90:91], v[86:87], v[72:73]
	global_store_dwordx4 v[98:99], v[76:79], off offset:1024
	ds_read_b128 v[76:79], v17 offset:6144
	ds_read_b128 v[86:89], v134 offset:6144
	v_pk_mul_f32 v[72:73], v[84:85], v[74:75] op_sel_hi:[1,0]
	s_waitcnt vmcnt(18)
	v_mov_b64_e32 v[92:93], v[62:63]
	v_mov_b64_e32 v[104:105], v[42:43]
	v_mov_b64_e32 v[124:125], v[32:33]
	s_waitcnt lgkmcnt(0)
	v_pk_mul_f32 v[82:83], v[82:83], v[88:89]
	v_pk_mul_f32 v[72:73], v[72:73], v[86:87]
	v_pk_fma_f32 v[70:71], v[78:79], v[82:83], v[70:71]
	v_pk_fma_f32 v[68:69], v[76:77], v[72:73], v[68:69]
	global_store_dwordx4 v[98:99], v[68:71], off offset:2048
	ds_read_b128 v[68:71], v17 offset:7168
	ds_read_b128 v[76:79], v134 offset:7168
	v_pk_mul_f32 v[72:73], v[80:81], v[74:75] op_sel_hi:[1,0]
	s_waitcnt vmcnt(14)
	v_mov_b64_e32 v[88:89], v[64:65]
	v_mov_b64_e32 v[96:97], v[20:21]
	v_mov_b64_e32 v[100:101], v[18:19]
	s_waitcnt lgkmcnt(0)
	v_pk_mul_f32 v[10:11], v[10:11], v[78:79]
	v_pk_mul_f32 v[72:73], v[72:73], v[76:77]
	v_mov_b64_e32 v[78:79], v[22:23]
	v_pk_fma_f32 v[66:67], v[68:69], v[72:73], v[66:67]
	v_pk_fma_f32 v[68:69], v[70:71], v[10:11], v[8:9]
	global_store_dwordx4 v[98:99], v[66:69], off offset:3072
	v_mov_b64_e32 v[98:99], v[60:61]
	v_mov_b64_e32 v[70:71], v[26:27]
	v_mov_b64_e32 v[66:67], v[30:31]
	v_mov_b64_e32 v[68:69], v[28:29]
	v_mov_b64_e32 v[72:73], v[24:25]
	s_waitcnt vmcnt(14)
	v_mov_b64_e32 v[84:85], v[54:55]
	s_waitcnt vmcnt(13)
	v_mov_b64_e32 v[80:81], v[56:57]
	s_waitcnt vmcnt(12)
	v_mov_b64_e32 v[74:75], v[58:59]
	v_mov_b64_e32 v[114:115], v[40:41]
	v_mov_b64_e32 v[112:113], v[38:39]
	v_mov_b64_e32 v[102:103], v[36:37]
	v_mov_b64_e32 v[94:95], v[34:35]
	s_waitcnt vmcnt(11)
	v_mov_b64_e32 v[90:91], v[50:51]
	s_waitcnt vmcnt(10)
	v_mov_b64_e32 v[86:87], v[48:49]
	s_waitcnt vmcnt(9)
	v_mov_b64_e32 v[82:83], v[46:47]
	s_waitcnt vmcnt(8)
	v_mov_b64_e32 v[76:77], v[44:45]
	v_mov_b64_e32 v[10:11], v[6:7]
	v_mov_b64_e32 v[8:9], v[4:5]
	s_andn2_b64 exec, exec, s[42:43]
	s_cbranch_execz .LBB0_2095

.LBB0_2110:
	s_or_b64 exec, exec, s[36:37]
	v_lshlrev_b32_e32 v121, 16, v108
	v_lshlrev_b32_e32 v120, 16, v104
	v_lshlrev_b32_e32 v119, 16, v106
	v_lshlrev_b32_e32 v118, 16, v110
	v_pk_mul_f32 v[120:121], v[10:11], v[120:121]
	v_and_b32_e32 v123, 0xffff0000, v108
	v_and_b32_e32 v122, 0xffff0000, v104
	v_pk_fma_f32 v[118:119], v[10:11], v[118:119], v[120:121] op_sel:[1,0,0] op_sel_hi:[0,1,1]
	v_and_b32_e32 v121, 0xffff0000, v106
	v_and_b32_e32 v120, 0xffff0000, v110
	v_pk_mul_f32 v[122:123], v[10:11], v[122:123]
	v_lshlrev_b32_e32 v125, 16, v109
	v_and_b32_e32 v109, 0xffff0000, v109
	v_and_b32_e32 v108, 0xffff0000, v105
	v_pk_fma_f32 v[120:121], v[10:11], v[120:121], v[122:123] op_sel:[1,0,0] op_sel_hi:[0,1,1]
	v_lshlrev_b32_e32 v123, 16, v107
	v_lshlrev_b32_e32 v124, 16, v105
	v_and_b32_e32 v107, 0xffff0000, v107
	v_and_b32_e32 v106, 0xffff0000, v111
	v_pk_mul_f32 v[104:105], v[10:11], v[108:109]
	v_lshlrev_b32_e32 v109, 16, v103
	v_lshlrev_b32_e32 v108, 16, v100
	v_pk_fma_f32 v[106:107], v[10:11], v[106:107], v[104:105] op_sel:[1,0,0] op_sel_hi:[0,1,1]
	v_lshlrev_b32_e32 v105, 16, v101
	v_lshlrev_b32_e32 v104, 16, v102
	v_pk_mul_f32 v[108:109], v[10:11], v[108:109]
	v_and_b32_e32 v100, 0xffff0000, v100
	v_pk_fma_f32 v[104:105], v[10:11], v[104:105], v[108:109] op_sel:[1,0,0] op_sel_hi:[0,1,1]
	v_and_b32_e32 v109, 0xffff0000, v101
	v_and_b32_e32 v101, 0xffff0000, v103
	v_and_b32_e32 v108, 0xffff0000, v102
	v_pk_mul_f32 v[100:101], v[10:11], v[100:101]
	s_and_b64 s[0:1], exec, vcc
	v_pk_fma_f32 v[102:103], v[10:11], v[108:109], v[100:101] op_sel:[1,0,0] op_sel_hi:[0,1,1]
	v_lshlrev_b32_e32 v108, 16, v96
	v_and_b32_e32 v109, 0xffff0000, v98
	v_lshlrev_b32_e32 v100, 16, v98
	v_and_b32_e32 v101, 0xffff0000, v96
	v_pk_mul_f32 v[108:109], v[10:11], v[108:109]
	v_lshlrev_b32_e32 v96, 16, v97
	v_pk_fma_f32 v[100:101], v[10:11], v[100:101], v[108:109] op_sel:[1,0,0] op_sel_hi:[0,1,1]
	v_and_b32_e32 v109, 0xffff0000, v97
	v_and_b32_e32 v97, 0xffff0000, v99
	v_lshlrev_b32_e32 v108, 16, v99
	v_pk_mul_f32 v[96:97], v[10:11], v[96:97]
	s_or_b64 s[14:15], s[0:1], s[14:15]
	v_pk_fma_f32 v[98:99], v[10:11], v[108:109], v[96:97] op_sel:[1,0,0] op_sel_hi:[0,1,1]
	v_lshlrev_b32_e32 v108, 16, v92
	v_and_b32_e32 v109, 0xffff0000, v94
	v_lshlrev_b32_e32 v96, 16, v94
	v_and_b32_e32 v97, 0xffff0000, v92
	v_pk_mul_f32 v[108:109], v[10:11], v[108:109]
	v_lshlrev_b32_e32 v92, 16, v93
	v_pk_fma_f32 v[96:97], v[10:11], v[96:97], v[108:109] op_sel:[1,0,0] op_sel_hi:[0,1,1]
	v_and_b32_e32 v109, 0xffff0000, v93
	v_and_b32_e32 v93, 0xffff0000, v95
	v_lshlrev_b32_e32 v108, 16, v95
	v_pk_mul_f32 v[92:93], v[10:11], v[92:93]
	v_readlane_b32 s0, v249, 30
	v_pk_fma_f32 v[94:95], v[10:11], v[108:109], v[92:93] op_sel:[1,0,0] op_sel_hi:[0,1,1]
	v_lshlrev_b32_e32 v109, 16, v91
	v_lshlrev_b32_e32 v108, 16, v88
	v_lshlrev_b32_e32 v93, 16, v89
	v_lshlrev_b32_e32 v92, 16, v90
	v_pk_mul_f32 v[108:109], v[10:11], v[108:109]
	v_and_b32_e32 v88, 0xffff0000, v88
	v_pk_fma_f32 v[92:93], v[10:11], v[92:93], v[108:109] op_sel:[1,0,0] op_sel_hi:[0,1,1]
	v_and_b32_e32 v109, 0xffff0000, v89
	v_and_b32_e32 v89, 0xffff0000, v91
	v_and_b32_e32 v108, 0xffff0000, v90
	v_pk_mul_f32 v[88:89], v[10:11], v[88:89]
	v_mov_b32_e32 v2, s0
	v_pk_fma_f32 v[90:91], v[10:11], v[108:109], v[88:89] op_sel:[1,0,0] op_sel_hi:[0,1,1]
	v_lshlrev_b32_e32 v108, 16, v84
	v_and_b32_e32 v109, 0xffff0000, v86
	v_lshlrev_b32_e32 v88, 16, v86
	v_and_b32_e32 v89, 0xffff0000, v84
	v_pk_mul_f32 v[108:109], v[10:11], v[108:109]
	v_lshlrev_b32_e32 v84, 16, v85
	v_pk_fma_f32 v[88:89], v[10:11], v[88:89], v[108:109] op_sel:[1,0,0] op_sel_hi:[0,1,1]
	v_and_b32_e32 v109, 0xffff0000, v85
	v_and_b32_e32 v85, 0xffff0000, v87
	v_lshlrev_b32_e32 v108, 16, v87
	v_pk_mul_f32 v[84:85], v[10:11], v[84:85]
	v_readlane_b32 s0, v249, 23
	v_pk_fma_f32 v[86:87], v[10:11], v[108:109], v[84:85] op_sel:[1,0,0] op_sel_hi:[0,1,1]
	v_lshlrev_b32_e32 v108, 16, v80
	v_and_b32_e32 v109, 0xffff0000, v82
	v_lshlrev_b32_e32 v84, 16, v82
	v_and_b32_e32 v85, 0xffff0000, v80
	v_pk_mul_f32 v[108:109], v[10:11], v[108:109]
	v_lshlrev_b32_e32 v80, 16, v81
	v_pk_fma_f32 v[84:85], v[10:11], v[84:85], v[108:109] op_sel:[1,0,0] op_sel_hi:[0,1,1]
	v_and_b32_e32 v109, 0xffff0000, v81
	v_and_b32_e32 v81, 0xffff0000, v83
	v_mov_b32_e32 v8, s0
	v_readlane_b32 s0, v249, 33
	v_lshlrev_b32_e32 v122, 16, v111
	v_pk_mul_f32 v[124:125], v[10:11], v[124:125]
	v_lshlrev_b32_e32 v108, 16, v83
	v_pk_mul_f32 v[80:81], v[10:11], v[80:81]
	v_cmp_gt_i32_e32 vcc, s0, v114
	v_pk_fma_f32 v[122:123], v[10:11], v[122:123], v[124:125] op_sel:[1,0,0] op_sel_hi:[0,1,1]
	v_pk_fma_f32 v[10:11], v[10:11], v[108:109], v[80:81] op_sel:[1,0,0] op_sel_hi:[0,1,1]
	v_pk_mul_f32 v[80:81], v[120:121], v[120:121]
	v_pk_mul_f32 v[82:83], v[106:107], v[106:107]
	v_cndmask_b32_e32 v2, v2, v8, vcc
	v_pk_fma_f32 v[80:81], v[118:119], v[118:119], v[80:81]
	v_pk_fma_f32 v[82:83], v[122:123], v[122:123], v[82:83]
	v_add_u32_e32 v8, v2, v114
	v_pk_add_f32 v[80:81], v[80:81], v[82:83]
	v_pk_mul_f32 v[82:83], v[102:103], v[102:103]
	v_mul_f32_e32 v2, v98, v98
	v_pk_fma_f32 v[82:83], v[104:105], v[104:105], v[82:83]
	v_pk_fma_f32 v[108:109], v[98:99], v[98:99], v[2:3] op_sel_hi:[1,1,0]
	v_mul_f32_e32 v2, v100, v100
	v_pk_add_f32 v[80:81], v[80:81], v[80:81] op_sel_hi:[0,1]
	v_pk_add_f32 v[82:83], v[82:83], v[82:83] op_sel_hi:[0,1]
	v_pk_mul_f32 v[110:111], v[96:97], v[96:97]
	v_pk_mul_f32 v[124:125], v[94:95], v[94:95]
	v_pk_fma_f32 v[128:129], v[100:101], v[100:101], v[2:3] op_sel_hi:[1,1,0]
	v_mov_b32_e32 v108, v111
	v_mov_b32_e32 v128, v110
	v_mov_b32_e32 v82, v124
	v_mov_b32_e32 v80, v125
	v_pk_add_f32 v[108:109], v[128:129], v[108:109]
	v_pk_add_f32 v[80:81], v[82:83], v[80:81]
	v_pk_mul_f32 v[82:83], v[90:91], v[90:91]
	v_mul_f32_e32 v2, v86, v86
	v_pk_add_f32 v[80:81], v[108:109], v[80:81]
	v_pk_fma_f32 v[82:83], v[92:93], v[92:93], v[82:83]
	v_pk_fma_f32 v[108:109], v[86:87], v[86:87], v[2:3] op_sel_hi:[1,1,0]
	v_mul_f32_e32 v2, v88, v88
	v_pk_add_f32 v[80:81], v[80:81], v[80:81] op_sel_hi:[0,1]
	v_pk_add_f32 v[82:83], v[82:83], v[82:83] op_sel_hi:[0,1]
	v_pk_mul_f32 v[110:111], v[84:85], v[84:85]
	v_pk_mul_f32 v[124:125], v[10:11], v[10:11]
	v_pk_fma_f32 v[128:129], v[88:89], v[88:89], v[2:3] op_sel_hi:[1,1,0]
	v_mov_b32_e32 v108, v111
	v_mov_b32_e32 v128, v110
	v_mov_b32_e32 v82, v124
	v_mov_b32_e32 v80, v125
	v_pk_add_f32 v[108:109], v[128:129], v[108:109]
	v_pk_add_f32 v[80:81], v[82:83], v[80:81]
	s_mov_b32 s0, 0x800000
	v_pk_add_f32 v[80:81], v[108:109], v[80:81]
	v_add_f32_e32 v2, v80, v81
	s_nop 1
	v_add_f32_dpp v2, v2, v2 quad_perm:[1,0,3,2] row_mask:0xf bank_mask:0xf
	s_nop 1
	v_add_f32_dpp v2, v2, v2 quad_perm:[2,3,0,1] row_mask:0xf bank_mask:0xf
	s_nop 1
	v_add_f32_dpp v2, v2, v2 row_half_mirror row_mask:0xf bank_mask:0xf
	s_nop 1
	v_add_f32_dpp v2, v2, v2 row_mirror row_mask:0xf bank_mask:0xf
	s_nop 0
	v_readlane_b32 s100, v2, 0
	v_readlane_b32 s101, v2, 16
	s_nop 1
	v_mov_b32_e32 v9, s101
	v_add_f32_e32 v9, s100, v9
	v_readlane_b32 s100, v2, 32
	v_readlane_b32 s101, v2, 48
	s_nop 1
	v_mov_b32_e32 v2, s101
	v_add_f32_e32 v2, s100, v2
	v_add_f32_e32 v2, v9, v2
	v_lshlrev_b32_e32 v136, 16, v74
	v_and_b32_e32 v137, 0xffff0000, v74
	v_lshlrev_b32_e32 v138, 16, v75
	v_and_b32_e32 v139, 0xffff0000, v75
	s_waitcnt lgkmcnt(0)
	v_lshlrev_b32_e32 v108, 16, v68
	v_and_b32_e32 v109, 0xffff0000, v68
	v_lshlrev_b32_e32 v74, 16, v66
	v_and_b32_e32 v75, 0xffff0000, v66
	v_mov_b32_e32 v68, s12
	v_min_i32_e32 v149, 0x2000, v8
	v_lshlrev_b32_e32 v124, 16, v69
	v_and_b32_e32 v125, 0xffff0000, v69
	v_lshlrev_b32_e32 v110, 16, v67
	v_and_b32_e32 v111, 0xffff0000, v67
	v_lshlrev_b32_e32 v140, 16, v72
	v_and_b32_e32 v141, 0xffff0000, v72
	v_lshlrev_b32_e32 v142, 16, v73
	v_and_b32_e32 v143, 0xffff0000, v73
	v_lshlrev_b32_e32 v144, 16, v70
	v_and_b32_e32 v145, 0xffff0000, v70
	v_lshlrev_b32_e32 v146, 16, v71
	v_and_b32_e32 v147, 0xffff0000, v71
	v_lshlrev_b32_e32 v132, 16, v76
	v_and_b32_e32 v133, 0xffff0000, v76
	v_lshlrev_b32_e32 v134, 16, v77
	v_and_b32_e32 v135, 0xffff0000, v77
	v_mov_b32_e32 v76, v122
	v_mov_b32_e32 v77, v106
	v_lshlrev_b32_e32 v114, 16, v112
	v_fmamk_f32 v2, v2, 0x3a000000, v213
	v_mul_f32_e32 v9, 0x4b800000, v2
	v_cmp_gt_f32_e32 vcc, s0, v2
	v_and_b32_e32 v115, 0xffff0000, v112
	v_lshlrev_b32_e32 v116, 16, v113
	v_cndmask_b32_e32 v2, v2, v9, vcc
	v_rsq_f32_e32 v2, v2
	v_and_b32_e32 v117, 0xffff0000, v113
	v_lshlrev_b32_e32 v112, 16, v78
	v_and_b32_e32 v113, 0xffff0000, v78
	v_mul_f32_e32 v9, 0x45800000, v2
	v_cndmask_b32_e32 v148, v2, v9, vcc
	v_add_u32_e32 v2, 0xffffe000, v8
	v_cmp_gt_i32_e32 vcc, s84, v8
	v_ashrrev_i32_e32 v9, 31, v8
	v_pk_mul_f32 v[80:81], v[76:77], v[148:149] op_sel_hi:[1,0]
	v_cndmask_b32_e32 v66, v2, v8, vcc
	v_mov_b32_e32 v2, s49
	v_cndmask_b32_e32 v69, v2, v68, vcc
	v_mov_b32_e32 v2, s50
	v_mov_b32_e32 v68, s48
	v_cndmask_b32_e32 v67, 0, v9, vcc
	v_cndmask_b32_e32 v68, v2, v68, vcc
	v_lshlrev_b32_e32 v2, 1, v149
	v_lshlrev_b64 v[66:67], 12, v[66:67]
	v_and_b32_e32 v2, 0xffffe000, v2
	v_lshl_add_u64 v[66:67], v[68:69], 0, v[66:67]
	v_add_u32_e32 v128, v1, v2
	v_lshlrev_b32_e32 v2, 1, v12
	v_lshl_add_u64 v[150:151], v[66:67], 0, v[2:3]
	ds_read_b128 v[66:69], v128
	ds_read_b128 v[70:73], v13
	v_mov_b32_e32 v76, v118
	v_mov_b32_e32 v77, v120
	v_lshlrev_b32_e32 v130, 16, v79
	v_and_b32_e32 v131, 0xffff0000, v79
	v_pk_mul_f32 v[82:83], v[76:77], v[148:149] op_sel_hi:[1,0]
	ds_read_b128 v[76:79], v13 offset:1024
	s_waitcnt lgkmcnt(1)
	v_pk_mul_f32 v[82:83], v[82:83], v[70:71]
	v_pk_mul_f32 v[80:81], v[80:81], v[72:73]
	ds_read_b128 v[70:73], v128 offset:1024
	v_pk_fma_f32 v[80:81], v[68:69], v[80:81], v[116:117]
	v_pk_fma_f32 v[82:83], v[66:67], v[82:83], v[114:115]
	v_cvt_pk_bf16_f32 v67, v80, v81
	v_cvt_pk_bf16_f32 v66, v82, v83
	v_mov_b32_e32 v106, v123
	v_mov_b32_e32 v120, v119
	global_store_dwordx2 v[150:151], v[66:67], off
	v_pk_mul_f32 v[66:67], v[106:107], v[148:149] op_sel_hi:[1,0]
	v_pk_mul_f32 v[68:69], v[120:121], v[148:149] op_sel_hi:[1,0]
	s_waitcnt lgkmcnt(1)
	v_pk_mul_f32 v[66:67], v[66:67], v[78:79]
	v_pk_mul_f32 v[68:69], v[68:69], v[76:77]
	s_waitcnt lgkmcnt(0)
	v_pk_fma_f32 v[66:67], v[72:73], v[66:67], v[130:131]
	v_pk_fma_f32 v[68:69], v[70:71], v[68:69], v[112:113]
	v_cvt_pk_bf16_f32 v71, v66, v67
	v_cvt_pk_bf16_f32 v70, v68, v69
	global_store_dwordx2 v[150:151], v[70:71], off offset:512
	ds_read_b128 v[70:73], v128 offset:2048
	ds_read_b128 v[76:79], v13 offset:2048
	v_mov_b32_e32 v106, v105
	v_mov_b32_e32 v107, v103
	v_mov_b32_e32 v105, v102
	v_pk_mul_f32 v[106:107], v[106:107], v[148:149] op_sel_hi:[1,0]
	v_pk_mul_f32 v[102:103], v[104:105], v[148:149] op_sel_hi:[1,0]
	ds_read_b128 v[112:115], v13 offset:3072
	s_waitcnt lgkmcnt(1)
	v_pk_mul_f32 v[104:105], v[102:103], v[76:77]
	v_pk_mul_f32 v[102:103], v[106:107], v[78:79]
	ds_read_b128 v[76:79], v128 offset:3072
	v_pk_fma_f32 v[102:103], v[72:73], v[102:103], v[134:135]
	v_pk_fma_f32 v[104:105], v[70:71], v[104:105], v[132:133]
	v_cvt_pk_bf16_f32 v71, v102, v103
	v_cvt_pk_bf16_f32 v70, v104, v105
	global_store_dwordx2 v[150:151], v[70:71], off offset:1024
	v_pk_mul_f32 v[70:71], v[98:99], v[148:149] op_sel_hi:[1,0]
	v_pk_mul_f32 v[72:73], v[100:101], v[148:149] op_sel_hi:[1,0]
	s_waitcnt lgkmcnt(1)
	v_pk_mul_f32 v[70:71], v[70:71], v[114:115]
	v_pk_mul_f32 v[72:73], v[72:73], v[112:113]
	s_waitcnt lgkmcnt(0)
	v_pk_fma_f32 v[70:71], v[78:79], v[70:71], v[138:139]
	v_pk_fma_f32 v[72:73], v[76:77], v[72:73], v[136:137]
	v_cvt_pk_bf16_f32 v77, v70, v71
	v_cvt_pk_bf16_f32 v76, v72, v73
	global_store_dwordx2 v[150:151], v[76:77], off offset:1536
	ds_read_b128 v[76:79], v13 offset:4096
	ds_read_b128 v[98:101], v128 offset:4096
	v_pk_mul_f32 v[94:95], v[94:95], v[148:149] op_sel_hi:[1,0]
	v_pk_mul_f32 v[96:97], v[96:97], v[148:149] op_sel_hi:[1,0]
	ds_read_b128 v[112:115], v13 offset:5120
	s_waitcnt lgkmcnt(2)
	v_pk_mul_f32 v[76:77], v[96:97], v[76:77]
	v_pk_mul_f32 v[78:79], v[94:95], v[78:79]
	ds_read_b128 v[116:119], v128 offset:5120
	s_waitcnt lgkmcnt(2)
	v_pk_fma_f32 v[94:95], v[100:101], v[78:79], v[142:143]
	v_pk_fma_f32 v[96:97], v[98:99], v[76:77], v[140:141]
	v_cvt_pk_bf16_f32 v77, v94, v95
	v_cvt_pk_bf16_f32 v76, v96, v97
	global_store_dwordx2 v[150:151], v[76:77], off offset:2048
	v_mov_b32_e32 v76, v93
	v_mov_b32_e32 v77, v91
	v_mov_b32_e32 v93, v90
	v_pk_mul_f32 v[76:77], v[76:77], v[148:149] op_sel_hi:[1,0]
	v_pk_mul_f32 v[78:79], v[92:93], v[148:149] op_sel_hi:[1,0]
	s_waitcnt lgkmcnt(1)
	v_pk_mul_f32 v[76:77], v[76:77], v[114:115]
	v_pk_mul_f32 v[78:79], v[78:79], v[112:113]
	s_waitcnt lgkmcnt(0)
	v_pk_fma_f32 v[76:77], v[118:119], v[76:77], v[146:147]
	v_pk_fma_f32 v[78:79], v[116:117], v[78:79], v[144:145]
	v_cvt_pk_bf16_f32 v91, v76, v77
	v_cvt_pk_bf16_f32 v90, v78, v79
	global_store_dwordx2 v[150:151], v[90:91], off offset:2560
	ds_read_b128 v[90:93], v13 offset:6144
	ds_read_b128 v[98:101], v128 offset:6144
	v_pk_mul_f32 v[86:87], v[86:87], v[148:149] op_sel_hi:[1,0]
	v_pk_mul_f32 v[88:89], v[88:89], v[148:149] op_sel_hi:[1,0]
	ds_read_b128 v[112:115], v13 offset:7168
	s_waitcnt lgkmcnt(2)
	v_pk_mul_f32 v[88:89], v[88:89], v[90:91]
	v_pk_mul_f32 v[86:87], v[86:87], v[92:93]
	ds_read_b128 v[90:93], v128 offset:7168
	v_pk_mul_f32 v[10:11], v[10:11], v[148:149] op_sel_hi:[1,0]
	v_pk_mul_f32 v[84:85], v[84:85], v[148:149] op_sel_hi:[1,0]
	s_waitcnt lgkmcnt(1)
	v_pk_mul_f32 v[10:11], v[10:11], v[114:115]
	v_pk_mul_f32 v[84:85], v[84:85], v[112:113]
	s_waitcnt lgkmcnt(0)
	v_pk_fma_f32 v[10:11], v[92:93], v[10:11], v[110:111]
	v_pk_fma_f32 v[74:75], v[90:91], v[84:85], v[74:75]
	v_cvt_pk_bf16_f32 v85, v10, v11
	v_cvt_pk_bf16_f32 v84, v74, v75
	v_mov_b32_e32 v90, v83
	v_mov_b32_e32 v91, v69
	global_store_dwordx2 v[150:151], v[84:85], off offset:3584
	v_mov_b32_e32 v84, v82
	v_mov_b32_e32 v85, v68
	v_pk_mul_f32 v[90:91], v[90:91], v[90:91]
	v_mov_b32_e32 v92, v81
	v_mov_b32_e32 v93, v67
	v_pk_fma_f32 v[84:85], v[84:85], v[84:85], v[90:91]
	v_mov_b32_e32 v90, v80
	v_mov_b32_e32 v91, v66
	v_pk_mul_f32 v[92:93], v[92:93], v[92:93]
	v_pk_fma_f32 v[86:87], v[100:101], v[86:87], v[124:125]
	v_pk_fma_f32 v[88:89], v[98:99], v[88:89], v[108:109]
	v_pk_fma_f32 v[90:91], v[90:91], v[90:91], v[92:93]
	v_cvt_pk_bf16_f32 v98, v88, v89
	v_cvt_pk_bf16_f32 v99, v86, v87
	v_pk_add_f32 v[84:85], v[84:85], v[90:91]
	v_pk_mul_f32 v[90:91], v[102:103], v[102:103]
	v_pk_mul_f32 v[92:93], v[104:105], v[104:105]
	global_store_dwordx2 v[150:151], v[98:99], off offset:3072
	v_pk_mov_b32 v[98:99], v[92:93], v[90:91] op_sel:[1,0]
	v_mov_b32_e32 v93, v91
	v_pk_add_f32 v[90:91], v[98:99], v[92:93]
	v_mul_f32_e32 v2, v96, v96
	v_mul_f32_e32 v92, v97, v97
	v_pk_add_f32 v[84:85], v[84:85], v[84:85] op_sel:[0,1] op_sel_hi:[1,0]
	v_pk_add_f32 v[90:91], v[90:91], v[90:91] op_sel:[0,1] op_sel_hi:[1,0]
	v_mov_b32_e32 v85, v2
	v_mov_b32_e32 v91, v92
	v_mul_f32_e32 v2, v73, v73
	v_mul_f32_e32 v93, v94, v94
	v_pk_add_f32 v[84:85], v[84:85], v[90:91]
	v_pk_fma_f32 v[90:91], v[72:73], v[72:73], v[2:3] op_sel_hi:[1,1,0]
	v_mul_f32_e32 v2, v71, v71
	v_mul_f32_e32 v98, v95, v95
	v_mov_b32_e32 v91, v93
	v_pk_fma_f32 v[92:93], v[70:71], v[70:71], v[2:3] op_sel_hi:[1,1,0]
	v_mul_f32_e32 v2, v74, v74
	v_mov_b32_e32 v93, v98
	v_pk_add_f32 v[90:91], v[90:91], v[92:93]
	v_pk_mul_f32 v[92:93], v[78:79], v[78:79]
	v_pk_add_f32 v[84:85], v[84:85], v[90:91]
	v_pk_mul_f32 v[90:91], v[76:77], v[76:77]
	v_pk_add_f32 v[84:85], v[84:85], v[84:85] op_sel:[0,1] op_sel_hi:[1,0]
	v_pk_mov_b32 v[98:99], v[92:93], v[90:91] op_sel:[1,0]
	v_mov_b32_e32 v93, v91
	v_pk_add_f32 v[90:91], v[98:99], v[92:93]
	v_mul_f32_e32 v92, v75, v75
	v_pk_add_f32 v[90:91], v[90:91], v[90:91] op_sel:[0,1] op_sel_hi:[1,0]
	v_mov_b32_e32 v85, v2
	v_mov_b32_e32 v91, v92
	v_mul_f32_e32 v2, v89, v89
	v_mul_f32_e32 v93, v10, v10
	v_pk_add_f32 v[84:85], v[84:85], v[90:91]
	v_pk_fma_f32 v[90:91], v[88:89], v[88:89], v[2:3] op_sel_hi:[1,1,0]
	v_mul_f32_e32 v2, v87, v87
	v_mul_f32_e32 v98, v11, v11
	v_mov_b32_e32 v91, v93
	v_pk_fma_f32 v[92:93], v[86:87], v[86:87], v[2:3] op_sel_hi:[1,1,0]
	v_lshlrev_b64 v[8:9], 12, v[8:9]
	v_mov_b32_e32 v93, v98
	v_pk_add_f32 v[90:91], v[90:91], v[92:93]
	v_lshl_add_u64 v[8:9], v[16:17], 0, v[8:9]
	v_pk_add_f32 v[84:85], v[84:85], v[90:91]
	s_nop 0
	v_add_f32_e32 v2, v84, v85
	s_nop 1
	v_add_f32_dpp v2, v2, v2 quad_perm:[1,0,3,2] row_mask:0xf bank_mask:0xf
	s_nop 1
	v_add_f32_dpp v2, v2, v2 quad_perm:[2,3,0,1] row_mask:0xf bank_mask:0xf
	s_nop 1
	v_add_f32_dpp v2, v2, v2 row_half_mirror row_mask:0xf bank_mask:0xf
	s_nop 1
	v_add_f32_dpp v2, v2, v2 row_mirror row_mask:0xf bank_mask:0xf
	s_nop 0
	v_readlane_b32 s100, v2, 0
	v_readlane_b32 s101, v2, 16
	s_nop 1
	v_mov_b32_e32 v84, s101
	v_add_f32_e32 v84, s100, v84
	v_readlane_b32 s100, v2, 32
	v_readlane_b32 s101, v2, 48
	s_nop 1
	v_mov_b32_e32 v2, s101
	v_add_f32_e32 v2, s100, v2
	v_add_f32_e32 v2, v84, v2
	s_waitcnt lgkmcnt(0)
	ds_read_b128 v[90:93], v126
	ds_read_b128 v[98:101], v128 offset:24576
	ds_read_b128 v[106:109], v128 offset:49152
	s_waitcnt lgkmcnt(0)
	v_pk_add_f32 v[112:113], v[108:109], 1.0 op_sel_hi:[1,0]
	v_pk_add_f32 v[114:115], v[106:107], 1.0 op_sel_hi:[1,0]
	ds_read_b128 v[106:109], v128 offset:25600
	v_fmamk_f32 v2, v2, 0x3a000000, v213
	v_mul_f32_e32 v84, 0x4b800000, v2
	v_cmp_gt_f32_e32 vcc, s0, v2
	s_nop 1
	v_cndmask_b32_e32 v2, v2, v84, vcc
	v_rsq_f32_e32 v2, v2
	s_nop 0
	v_mul_f32_e32 v84, 0x45800000, v2
	v_cndmask_b32_e32 v2, v2, v84, vcc
	v_pk_mul_f32 v[84:85], v[80:81], v[2:3] op_sel_hi:[1,0]
	v_pk_mul_f32 v[110:111], v[82:83], v[2:3] op_sel_hi:[1,0]
	s_waitcnt lgkmcnt(0)
	ds_read_b128 v[80:83], v126 offset:1024
	v_pk_mul_f32 v[110:111], v[90:91], v[110:111]
	v_pk_mul_f32 v[84:85], v[92:93], v[84:85]
	ds_read_b128 v[90:93], v128 offset:50176
	v_pk_mul_f32 v[66:67], v[66:67], v[2:3] op_sel_hi:[1,0]
	v_pk_mul_f32 v[68:69], v[68:69], v[2:3] op_sel_hi:[1,0]
	s_waitcnt lgkmcnt(1)
	v_pk_mul_f32 v[66:67], v[82:83], v[66:67]
	v_pk_mul_f32 v[68:69], v[80:81], v[68:69]
	s_waitcnt lgkmcnt(0)
	v_pk_add_f32 v[80:81], v[92:93], 1.0 op_sel_hi:[1,0]
	v_pk_add_f32 v[82:83], v[90:91], 1.0 op_sel_hi:[1,0]
	v_pk_fma_f32 v[84:85], v[112:113], v[84:85], v[100:101]
	v_pk_fma_f32 v[98:99], v[114:115], v[110:111], v[98:99]
	v_pk_fma_f32 v[66:67], v[80:81], v[66:67], v[108:109]
	v_pk_fma_f32 v[68:69], v[82:83], v[68:69], v[106:107]
	v_cvt_pk_bf16_f32 v98, v98, v99
	v_cvt_pk_bf16_f32 v99, v84, v85
	v_cvt_pk_bf16_f32 v68, v68, v69
	v_cvt_pk_bf16_f32 v69, v66, v67
	global_store_dwordx2 v[8:9], v[98:99], off
	global_store_dwordx2 v[8:9], v[68:69], off offset:512
	ds_read_b128 v[66:69], v126 offset:2048
	ds_read_b128 v[80:83], v128 offset:26624
	ds_read_b128 v[90:93], v128 offset:51200
	v_pk_mul_f32 v[84:85], v[102:103], v[2:3] op_sel_hi:[1,0]
	v_pk_mul_f32 v[102:103], v[104:105], v[2:3] op_sel_hi:[1,0]
	ds_read_b128 v[98:101], v126 offset:3072
	s_waitcnt lgkmcnt(3)
	v_pk_mul_f32 v[102:103], v[66:67], v[102:103]
	v_pk_mul_f32 v[84:85], v[68:69], v[84:85]
	ds_read_b128 v[66:69], v128 offset:52224
	s_waitcnt lgkmcnt(2)
	v_pk_add_f32 v[104:105], v[92:93], 1.0 op_sel_hi:[1,0]
	v_pk_add_f32 v[106:107], v[90:91], 1.0 op_sel_hi:[1,0]
	ds_read_b128 v[90:93], v128 offset:27648
	v_pk_mul_f32 v[70:71], v[70:71], v[2:3] op_sel_hi:[1,0]
	v_pk_mul_f32 v[72:73], v[72:73], v[2:3] op_sel_hi:[1,0]
	s_waitcnt lgkmcnt(2)
	v_pk_mul_f32 v[70:71], v[70:71], v[100:101]
	v_pk_mul_f32 v[72:73], v[72:73], v[98:99]
	s_waitcnt lgkmcnt(1)
	v_pk_add_f32 v[68:69], v[68:69], 1.0 op_sel_hi:[1,0]
	v_pk_add_f32 v[66:67], v[66:67], 1.0 op_sel_hi:[1,0]
	v_pk_fma_f32 v[82:83], v[104:105], v[84:85], v[82:83]
	v_pk_fma_f32 v[80:81], v[106:107], v[102:103], v[80:81]
	s_waitcnt lgkmcnt(0)
	v_pk_fma_f32 v[68:69], v[70:71], v[68:69], v[92:93]
	v_pk_fma_f32 v[66:67], v[72:73], v[66:67], v[90:91]
	v_cvt_pk_bf16_f32 v80, v80, v81
	v_cvt_pk_bf16_f32 v81, v82, v83
	v_cvt_pk_bf16_f32 v66, v66, v67
	v_cvt_pk_bf16_f32 v67, v68, v69
	global_store_dwordx2 v[8:9], v[80:81], off offset:1024
	global_store_dwordx2 v[8:9], v[66:67], off offset:1536
	ds_read_b128 v[66:69], v126 offset:4096
	ds_read_b128 v[70:73], v128 offset:28672
	ds_read_b128 v[80:83], v128 offset:53248
	v_pk_mul_f32 v[84:85], v[94:95], v[2:3] op_sel_hi:[1,0]
	v_pk_mul_f32 v[94:95], v[96:97], v[2:3] op_sel_hi:[1,0]
	ds_read_b128 v[90:93], v126 offset:5120
	s_waitcnt lgkmcnt(3)
	v_pk_mul_f32 v[94:95], v[94:95], v[66:67]
	v_pk_mul_f32 v[84:85], v[84:85], v[68:69]
	ds_read_b128 v[66:69], v128 offset:54272
	s_waitcnt lgkmcnt(2)
	v_pk_add_f32 v[96:97], v[82:83], 1.0 op_sel_hi:[1,0]
	v_pk_add_f32 v[98:99], v[80:81], 1.0 op_sel_hi:[1,0]
	ds_read_b128 v[80:83], v128 offset:29696
	v_pk_fma_f32 v[72:73], v[84:85], v[96:97], v[72:73]
	v_pk_fma_f32 v[70:71], v[94:95], v[98:99], v[70:71]
	s_waitcnt lgkmcnt(1)
	v_pk_add_f32 v[68:69], v[68:69], 1.0 op_sel_hi:[1,0]
	v_cvt_pk_bf16_f32 v70, v70, v71
	v_cvt_pk_bf16_f32 v71, v72, v73
	global_store_dwordx2 v[8:9], v[70:71], off offset:2048
	v_pk_mul_f32 v[70:71], v[76:77], v[2:3] op_sel_hi:[1,0]
	v_pk_mul_f32 v[72:73], v[78:79], v[2:3] op_sel_hi:[1,0]
	v_pk_mul_f32 v[70:71], v[70:71], v[92:93]
	v_pk_mul_f32 v[72:73], v[72:73], v[90:91]
	v_pk_add_f32 v[66:67], v[66:67], 1.0 op_sel_hi:[1,0]
	s_waitcnt lgkmcnt(0)
	v_pk_fma_f32 v[68:69], v[70:71], v[68:69], v[82:83]
	v_pk_fma_f32 v[66:67], v[72:73], v[66:67], v[80:81]
	v_pk_mul_f32 v[84:85], v[86:87], v[2:3] op_sel_hi:[1,0]
	v_cvt_pk_bf16_f32 v66, v66, v67
	v_cvt_pk_bf16_f32 v67, v68, v69
	global_store_dwordx2 v[8:9], v[66:67], off offset:2560
	ds_read_b128 v[66:69], v126 offset:6144
	ds_read_b128 v[70:73], v128 offset:30720
	ds_read_b128 v[76:79], v128 offset:55296
	v_pk_mul_f32 v[86:87], v[88:89], v[2:3] op_sel_hi:[1,0]
	ds_read_b128 v[80:83], v126 offset:7168
	s_waitcnt lgkmcnt(3)
	v_pk_mul_f32 v[86:87], v[86:87], v[66:67]
	v_pk_mul_f32 v[84:85], v[84:85], v[68:69]
	ds_read_b128 v[66:69], v128 offset:56320
	s_waitcnt lgkmcnt(2)
	v_pk_add_f32 v[88:89], v[78:79], 1.0 op_sel_hi:[1,0]
	v_pk_add_f32 v[90:91], v[76:77], 1.0 op_sel_hi:[1,0]
	ds_read_b128 v[76:79], v128 offset:31744
	v_pk_fma_f32 v[72:73], v[84:85], v[88:89], v[72:73]
	v_pk_fma_f32 v[70:71], v[86:87], v[90:91], v[70:71]
	v_pk_mul_f32 v[10:11], v[10:11], v[2:3] op_sel_hi:[1,0]
	v_cvt_pk_bf16_f32 v70, v70, v71
	v_cvt_pk_bf16_f32 v71, v72, v73
	global_store_dwordx2 v[8:9], v[70:71], off offset:3072
	v_pk_mul_f32 v[70:71], v[74:75], v[2:3] op_sel_hi:[1,0]
	s_waitcnt lgkmcnt(2)
	v_pk_mul_f32 v[10:11], v[10:11], v[82:83]
	v_pk_mul_f32 v[70:71], v[70:71], v[80:81]
	s_waitcnt lgkmcnt(1)
	v_pk_add_f32 v[68:69], v[68:69], 1.0 op_sel_hi:[1,0]
	v_pk_add_f32 v[66:67], v[66:67], 1.0 op_sel_hi:[1,0]
	s_waitcnt lgkmcnt(0)
	v_pk_fma_f32 v[10:11], v[10:11], v[68:69], v[78:79]
	v_pk_fma_f32 v[66:67], v[70:71], v[66:67], v[76:77]
	s_waitcnt vmcnt(33)
	v_mov_b64_e32 v[68:69], v[32:33]
	v_cvt_pk_bf16_f32 v66, v66, v67
	v_cvt_pk_bf16_f32 v67, v10, v11
	global_store_dwordx2 v[8:9], v[66:67], off offset:3584
	v_mov_b64_e32 v[70:71], v[30:31]
	v_mov_b64_e32 v[72:73], v[28:29]
	v_mov_b64_e32 v[74:75], v[26:27]
	v_mov_b64_e32 v[76:77], v[22:23]
	v_mov_b64_e32 v[78:79], v[20:21]
	v_mov_b64_e32 v[112:113], v[18:19]
	s_waitcnt vmcnt(33)
	v_mov_b64_e32 v[66:67], v[24:25]
	s_waitcnt vmcnt(31)
	v_mov_b64_e32 v[104:105], v[42:43]
	s_waitcnt vmcnt(30)
	v_mov_b64_e32 v[106:107], v[44:45]
	s_waitcnt vmcnt(29)
	v_mov_b64_e32 v[100:101], v[46:47]
	s_waitcnt vmcnt(28)
	v_mov_b64_e32 v[96:97], v[48:49]
	s_waitcnt vmcnt(23)
	v_mov_b64_e32 v[92:93], v[58:59]
	s_waitcnt vmcnt(22)
	v_mov_b64_e32 v[88:89], v[60:61]
	s_waitcnt vmcnt(21)
	v_mov_b64_e32 v[84:85], v[62:63]
	s_waitcnt vmcnt(20)
	v_mov_b64_e32 v[80:81], v[64:65]
	v_mov_b64_e32 v[110:111], v[40:41]
	v_mov_b64_e32 v[108:109], v[38:39]
	v_mov_b64_e32 v[102:103], v[36:37]
	v_mov_b64_e32 v[98:99], v[34:35]
	s_waitcnt vmcnt(19)
	v_mov_b64_e32 v[94:95], v[56:57]
	s_waitcnt vmcnt(18)
	v_mov_b64_e32 v[90:91], v[54:55]
	s_waitcnt vmcnt(17)
	v_mov_b64_e32 v[86:87], v[52:53]
	s_waitcnt vmcnt(16)
	v_mov_b64_e32 v[82:83], v[50:51]
	v_mov_b32_e32 v114, v127
	v_mov_b64_e32 v[10:11], v[6:7]
	v_mov_b64_e32 v[8:9], v[4:5]
	s_andn2_b64 exec, exec, s[14:15]
	s_cbranch_execz .LBB0_2116
